# speedup vs baseline: 1.0013x; 1.0013x over previous
.LE_tok16:
	s_and_b32 s64, s71, 1
	s_lshl_b32 s64, s64, 22
	s_add_u32 s64, s64, s49
	s_add_u32 s64, s64, 0x20000
	s_add_u32 s34, s6, s64
	s_addc_u32 s35, s7, 0
	s_mov_b32 m0, s52
	s_add_u32 s44, s34, 0x0
	s_addc_u32 s45, s35, 0
	global_load_lds_dwordx4 v192, s[44:45] sc1
	v_rcp_f32_e32 v207, v207
	v_mul_f32_e32 v206, v206, v158
	v_mfma_f32_32x32x16_f16 v[0:15], a[128:131], v[160:163], v[0:15]
	ds_read_b128 v[160:163], v193 offset:8192
	v_rcp_f32_e32 v208, v208
	v_mul_f32_e32 v207, v207, v159
	v_mfma_f32_32x32x16_f16 v[16:31], a[128:131], v[164:167], v[16:31]
	ds_read_b128 v[164:167], v193 offset:9216
	v_rcp_f32_e32 v209, v209
	v_fmamk_f32 v208, v208, 0xc0b8aa3b, v198
	s_waitcnt lgkmcnt(2)
	v_mfma_f32_32x32x16_f16 v[0:15], a[132:135], v[168:171], v[0:15]
	ds_read_b128 v[168:171], v193 offset:10240
	v_rcp_f32_e32 v210, v210
	v_fmamk_f32 v209, v209, 0xc0b8aa3b, v198
	v_fma_f32 v156, v200, v208, v204
	v_mfma_f32_32x32x16_f16 v[16:31], a[132:135], v[172:175], v[16:31]
	ds_read_b128 v[172:175], v193 offset:11264
	global_load_lds_dwordx4 v192, s[44:45] offset:1024 sc1
	v_rcp_f32_e32 v211, v211
	v_fmamk_f32 v210, v210, 0xc0b8aa3b, v198
	v_fma_f32 v157, v201, v209, v205
	v_mfma_f32_32x32x16_f16 v[0:15], a[136:139], v[176:179], v[0:15]
	ds_read_b128 v[176:179], v193 offset:12288
	v_rcp_f32_e32 v212, v212
	v_fmamk_f32 v211, v211, 0xc0b8aa3b, v198
	v_fma_f32 v158, v202, v210, v206
	v_mfma_f32_32x32x16_f16 v[16:31], a[136:139], v[180:183], v[16:31]
	ds_read_b128 v[180:183], v193 offset:13312
	v_rcp_f32_e32 v213, v213
	v_fma_f32 v159, v203, v211, v207
	v_mfma_f32_32x32x16_f16 v[0:15], a[140:143], v[184:187], v[0:15]
	ds_read_b128 v[184:187], v193 offset:14336
	v_rcp_f32_e32 v214, v214
	v_mfma_f32_32x32x16_f16 v[16:31], a[140:143], v[188:191], v[16:31]
	ds_read_b128 v[188:191], v193 offset:15360
	global_load_lds_dwordx4 v192, s[44:45] offset:2048 sc1
	v_rcp_f32_e32 v215, v215
	s_waitcnt lgkmcnt(2)
	v_mfma_f32_32x32x16_f16 v[0:15], a[144:147], v[160:163], v[0:15]
	ds_read_b128 v[160:163], v193 offset:16384
	v_exp_f32_e32 v200, v156
	v_mfma_f32_32x32x16_f16 v[16:31], a[144:147], v[164:167], v[16:31]
	ds_read_b128 v[164:167], v193 offset:17408
	v_exp_f32_e32 v201, v157
	v_add_f32_e32 v200, 1.0, v200
	v_mfma_f32_32x32x16_f16 v[0:15], a[148:151], v[168:171], v[0:15]
	ds_read_b128 v[168:171], v193 offset:18432
	v_exp_f32_e32 v202, v158
	v_add_f32_e32 v201, 1.0, v201
	v_mfma_f32_32x32x16_f16 v[16:31], a[148:151], v[172:175], v[16:31]
	ds_read_b128 v[172:175], v193 offset:19456
	global_load_lds_dwordx4 v192, s[44:45] offset:3072 sc1
	v_exp_f32_e32 v203, v159
	v_add_f32_e32 v202, 1.0, v202
	v_mfma_f32_32x32x16_f16 v[0:15], a[152:155], v[176:179], v[0:15]
	ds_read_b128 v[176:179], v193 offset:20480
	v_add_f32_e32 v203, 1.0, v203
	v_rcp_f32_e32 v200, v200
	v_mfma_f32_32x32x16_f16 v[16:31], a[152:155], v[180:183], v[16:31]
	ds_read_b128 v[180:183], v193 offset:21504
	v_rcp_f32_e32 v201, v201
	v_fma_f32 v200, v200, 2.0, -1.0
	s_waitcnt lgkmcnt(2)
	v_mfma_f32_32x32x16_f16 v[0:15], a[156:159], v[184:187], v[0:15]
	ds_read_b128 v[184:187], v193 offset:22528
	v_rcp_f32_e32 v202, v202
	v_fma_f32 v201, v201, 2.0, -1.0
	v_mul_f32_e32 v216, v212, v200
	v_mfma_f32_32x32x16_f16 v[16:31], a[156:159], v[188:191], v[16:31]
	ds_read_b128 v[188:191], v193 offset:23552
	s_mov_b32 m0, s53
	s_add_u32 s44, s34, 0x1000
	s_addc_u32 s45, s35, 0
	global_load_lds_dwordx4 v192, s[44:45] sc1
	v_rcp_f32_e32 v203, v203
	v_fma_f32 v202, v202, 2.0, -1.0
	v_mul_f32_e32 v217, v213, v201
	v_mfma_f32_32x32x16_f16 v[0:15], a[160:163], v[160:163], v[0:15]
	ds_read_b128 v[160:163], v193 offset:24576
	v_fma_f32 v203, v203, 2.0, -1.0
	v_mul_f32_e32 v218, v214, v202
	v_mfma_f32_32x32x16_f16 v[16:31], a[160:163], v[164:167], v[16:31]
	ds_read_b128 v[164:167], v193 offset:25600
	v_mul_f32_e32 v219, v215, v203
	v_cvt_pk_f16_f32 v222, v216, v217
	v_mfma_f32_32x32x16_f16 v[0:15], a[164:167], v[168:171], v[0:15]
	ds_read_b128 v[168:171], v193 offset:26624
	v_cvt_pk_f16_f32 v223, v218, v219
	v_mfma_f32_32x32x16_f16 v[16:31], a[164:167], v[172:175], v[16:31]
	ds_read_b128 v[172:175], v193 offset:27648
	global_load_lds_dwordx4 v192, s[44:45] offset:1024 sc1
	v_permlane32_swap_b32_e32 v220, v222
	v_permlane32_swap_b32_e32 v221, v223
	s_cmp_eq_u32 s31, 0
	s_cbranch_scc1 .LE_slow18
	global_store_dwordx4 v195, v[220:223], s[36:37] offset:0

.LE_htb27:
	s_waitcnt lgkmcnt(2)
	v_mfma_f32_32x32x16_f16 v[32:47], a[168:171], v[176:179], v[32:47]
	ds_read_b128 v[176:179], v193 offset:28672
	v_permlane32_swap_b32_e32 v220, v222
	v_permlane32_swap_b32_e32 v221, v223
	s_cmp_eq_u32 s31, 0
	s_cbranch_scc1 .LE_slow28
	global_store_dwordx4 v195, v[220:223], s[36:37] offset:0

.LE_htb37:
	s_waitcnt lgkmcnt(2)
	v_mfma_f32_32x32x16_f16 v[64:79], a[168:171], v[176:179], v[64:79]
	ds_read_b128 v[176:179], v193 offset:28672
	v_permlane32_swap_b32_e32 v220, v222
	v_permlane32_swap_b32_e32 v221, v223
	s_cmp_eq_u32 s31, 0
	s_cbranch_scc1 .LE_slow38
	global_store_dwordx4 v195, v[220:223], s[36:37] offset:0

.LE_htb47:
	s_waitcnt lgkmcnt(2)
	v_mfma_f32_32x32x16_f16 v[96:111], a[168:171], v[176:179], v[96:111]
	ds_read_b128 v[176:179], v193 offset:28672
	v_permlane32_swap_b32_e32 v220, v222
	v_permlane32_swap_b32_e32 v221, v223
	s_cmp_eq_u32 s31, 0
	s_cbranch_scc1 .LE_slow48
	global_store_dwordx4 v195, v[220:223], s[36:37] offset:0

.LD_cdone1:
	s_waitcnt lgkmcnt(0)
	s_barrier
	v_mov_b32_e32 v252, 0x22000
	ds_read_b32 v200, v252
	ds_read_b32 v201, v252 offset:4
	ds_read_b32 v202, v252 offset:8
	s_waitcnt lgkmcnt(0)
	s_nop 1
	v_readfirstlane_b32 s31, v200
	v_readfirstlane_b32 s29, v201
	v_readfirstlane_b32 s30, v202
	s_nop 3
	s_barrier
	s_lshl_b32 s49, s29, 19
	s_lshl_b32 s64, s32, 13
	s_add_u32 s49, s49, s64
	s_mov_b32 s51, s64
	s_add_u32 s52, s51, 0x0
	s_add_u32 s53, s51, 0x1000
	s_add_u32 s54, s51, 0x8000
	s_add_u32 s55, s51, 0x9000
	s_add_u32 s56, s51, 0x10000
	s_add_u32 s57, s51, 0x11000
	s_add_u32 s58, s51, 0x18000
	s_add_u32 s59, s51, 0x19000
	s_lshl_b32 s64, s29, 8
	s_lshl_b32 s65, s30, 1
	s_add_u32 s64, s64, s65
	s_lshr_b32 s65, s32, 1
	s_add_u32 s64, s64, s65
	s_lshl_b32 s64, s64, 11
	s_and_b32 s65, s32, 1
	s_lshl_b32 s65, s65, 9
	s_add_u32 s50, s64, s65
	s_sub_u32 s60, s28, 1
	v_mov_b32_e32 v128, 0
	v_mov_b32_e32 v129, 0
	v_mov_b32_e32 v130, 0
	v_mov_b32_e32 v131, 0
	v_mov_b32_e32 v132, 0
	v_mov_b32_e32 v133, 0
	v_mov_b32_e32 v134, 0
	v_mov_b32_e32 v135, 0
	v_mov_b32_e32 v136, 0
	v_mov_b32_e32 v137, 0
	v_mov_b32_e32 v138, 0
	v_mov_b32_e32 v139, 0
	v_mov_b32_e32 v140, 0
	v_mov_b32_e32 v141, 0
	v_mov_b32_e32 v142, 0
	v_mov_b32_e32 v143, 0
	v_mov_b32_e32 v144, 0
	v_mov_b32_e32 v145, 0
	v_mov_b32_e32 v146, 0
	v_mov_b32_e32 v147, 0
	v_mov_b32_e32 v148, 0
	v_mov_b32_e32 v149, 0
	v_mov_b32_e32 v150, 0
	v_mov_b32_e32 v151, 0
	v_mov_b32_e32 v152, 0
	v_mov_b32_e32 v153, 0
	v_mov_b32_e32 v154, 0
	v_mov_b32_e32 v155, 0
	v_mov_b32_e32 v156, 0
	v_mov_b32_e32 v157, 0
	v_mov_b32_e32 v158, 0
	v_mov_b32_e32 v159, 0
	s_lshl_b32 s64, s30, 5
	s_lshl_b32 s65, s32, 3
	s_add_u32 s64, s64, s65
	v_lshlrev_b32_e32 v255, 2, v254
	v_add_u32_e32 v255, s64, v255
	v_lshlrev_b32_e32 v200, 2, v255
	global_load_dwordx4 v[228:231], v200, s[22:23]
	v_add_u32_e32 v201, 0x1000, v200
	global_load_dwordx4 v[232:235], v201, s[22:23]
	s_lshl_b32 s65, s32, 11
	v_lshl_add_u32 v248, v253, 3, s65
	v_add_u32_e32 v248, 0x20000, v248
	v_and_b32_e32 v250, 15, v194
	s_mul_i32 s65, s32, 128
	v_lshl_add_u32 v249, v250, 3, s65
	v_add_u32_e32 v249, 0x20000, v249
	v_lshlrev_b32_e32 v250, 3, v250
	s_lshl_b32 s65, s30, 11
	s_lshl_b32 s66, s29, 8
	s_add_u32 s65, s65, s66
	s_mul_i32 s66, s32, 16
	s_add_u32 s65, s65, s66
	s_lshl_b32 s65, s65, 3
	s_add_u32 s62, s24, s65
	s_addc_u32 s63, s25, 0
	s_lshl_b32 s65, s29, 5
	s_add_u32 s65, s65, s30
	s_lshl_b32 s65, s65, 2
	s_add_u32 s65, s65, s32
	s_lshl_b32 s65, s65, 15
	s_add_u32 s42, s18, s65
	s_addc_u32 s43, s19, 0
	s_waitcnt vmcnt(0)
	s_waitcnt vmcnt(0)
	s_mov_b32 s33, 0
	s_add_u32 s46, s42, 0x0
	s_addc_u32 s47, s43, 0
	global_load_dwordx4 v[0:3], v192, s[46:47] offset:0
	global_load_dwordx4 v[4:7], v192, s[46:47] offset:1024
	global_load_dwordx4 v[8:11], v192, s[46:47] offset:2048
	global_load_dwordx4 v[12:15], v192, s[46:47] offset:3072
	s_add_u32 s46, s42, 0x1000
	s_addc_u32 s47, s43, 0
	global_load_dwordx4 v[16:19], v192, s[46:47] offset:0
	global_load_dwordx4 v[20:23], v192, s[46:47] offset:1024
	global_load_dwordx4 v[24:27], v192, s[46:47] offset:2048
	global_load_dwordx4 v[28:31], v192, s[46:47] offset:3072
	s_add_u32 s46, s42, 0x2000
	s_addc_u32 s47, s43, 0
	global_load_dwordx4 v[32:35], v192, s[46:47] offset:0
	global_load_dwordx4 v[36:39], v192, s[46:47] offset:1024
	global_load_dwordx4 v[40:43], v192, s[46:47] offset:2048
	global_load_dwordx4 v[44:47], v192, s[46:47] offset:3072
	s_add_u32 s46, s42, 0x3000
	s_addc_u32 s47, s43, 0
	global_load_dwordx4 v[48:51], v192, s[46:47] offset:0
	global_load_dwordx4 v[52:55], v192, s[46:47] offset:1024
	global_load_dwordx4 v[56:59], v192, s[46:47] offset:2048
	global_load_dwordx4 v[60:63], v192, s[46:47] offset:3072
	s_add_u32 s46, s42, 0x4000
	s_addc_u32 s47, s43, 0
	global_load_dwordx4 v[64:67], v192, s[46:47] offset:0
	global_load_dwordx4 v[68:71], v192, s[46:47] offset:1024
	global_load_dwordx4 v[72:75], v192, s[46:47] offset:2048
	global_load_dwordx4 v[76:79], v192, s[46:47] offset:3072
	s_add_u32 s46, s42, 0x5000
	s_addc_u32 s47, s43, 0
	global_load_dwordx4 v[80:83], v192, s[46:47] offset:0
	global_load_dwordx4 v[84:87], v192, s[46:47] offset:1024
	global_load_dwordx4 v[88:91], v192, s[46:47] offset:2048
	global_load_dwordx4 v[92:95], v192, s[46:47] offset:3072
	s_add_u32 s46, s42, 0x6000
	s_addc_u32 s47, s43, 0
	global_load_dwordx4 v[96:99], v192, s[46:47] offset:0
	global_load_dwordx4 v[100:103], v192, s[46:47] offset:1024
	global_load_dwordx4 v[104:107], v192, s[46:47] offset:2048
	global_load_dwordx4 v[108:111], v192, s[46:47] offset:3072
	s_add_u32 s46, s42, 0x7000
	s_addc_u32 s47, s43, 0
	global_load_dwordx4 v[112:115], v192, s[46:47] offset:0
	global_load_dwordx4 v[116:119], v192, s[46:47] offset:1024
	global_load_dwordx4 v[120:123], v192, s[46:47] offset:2048
	global_load_dwordx4 v[124:127], v192, s[46:47] offset:3072
	s_waitcnt vmcnt(0)
	s_waitcnt lgkmcnt(0)
	s_lshl_b32 s64, s30, 2
	s_add_u32 s64, s64, s32
	s_lshl_b32 s64, s64, 16
	s_add_u32 s44, s4, s64
	s_addc_u32 s45, s5, 0
	global_load_dwordx4 a[0:3], v192, s[44:45] offset:0
	global_load_dwordx4 a[4:7], v192, s[44:45] offset:1024
	global_load_dwordx4 a[8:11], v192, s[44:45] offset:2048
	global_load_dwordx4 a[12:15], v192, s[44:45] offset:3072
	s_add_u32 s44, s44, 0x1000
	s_addc_u32 s45, s45, 0
	global_load_dwordx4 a[16:19], v192, s[44:45] offset:0
	global_load_dwordx4 a[20:23], v192, s[44:45] offset:1024
	global_load_dwordx4 a[24:27], v192, s[44:45] offset:2048
	global_load_dwordx4 a[28:31], v192, s[44:45] offset:3072
	s_add_u32 s44, s44, 0x1000
	s_addc_u32 s45, s45, 0
	global_load_dwordx4 a[32:35], v192, s[44:45] offset:0
	global_load_dwordx4 a[36:39], v192, s[44:45] offset:1024
	global_load_dwordx4 a[40:43], v192, s[44:45] offset:2048
	global_load_dwordx4 a[44:47], v192, s[44:45] offset:3072
	s_add_u32 s44, s44, 0x1000
	s_addc_u32 s45, s45, 0
	global_load_dwordx4 a[48:51], v192, s[44:45] offset:0
	global_load_dwordx4 a[52:55], v192, s[44:45] offset:1024
	global_load_dwordx4 a[56:59], v192, s[44:45] offset:2048
	global_load_dwordx4 a[60:63], v192, s[44:45] offset:3072
	s_add_u32 s44, s44, 0x1000
	s_addc_u32 s45, s45, 0
	global_load_dwordx4 a[64:67], v192, s[44:45] offset:0
	global_load_dwordx4 a[68:71], v192, s[44:45] offset:1024
	global_load_dwordx4 a[72:75], v192, s[44:45] offset:2048
	global_load_dwordx4 a[76:79], v192, s[44:45] offset:3072
	s_add_u32 s44, s44, 0x1000
	s_addc_u32 s45, s45, 0
	global_load_dwordx4 a[80:83], v192, s[44:45] offset:0
	global_load_dwordx4 a[84:87], v192, s[44:45] offset:1024
	global_load_dwordx4 a[88:91], v192, s[44:45] offset:2048
	global_load_dwordx4 a[92:95], v192, s[44:45] offset:3072
	s_add_u32 s44, s44, 0x1000
	s_addc_u32 s45, s45, 0
	global_load_dwordx4 a[96:99], v192, s[44:45] offset:0
	global_load_dwordx4 a[100:103], v192, s[44:45] offset:1024
	global_load_dwordx4 a[104:107], v192, s[44:45] offset:2048
	global_load_dwordx4 a[108:111], v192, s[44:45] offset:3072
	s_add_u32 s44, s44, 0x1000
	s_addc_u32 s45, s45, 0
	global_load_dwordx4 a[112:115], v192, s[44:45] offset:0
	global_load_dwordx4 a[116:119], v192, s[44:45] offset:1024
	global_load_dwordx4 a[120:123], v192, s[44:45] offset:2048
	global_load_dwordx4 a[124:127], v192, s[44:45] offset:3072
	s_add_u32 s44, s44, 0x1000
	s_addc_u32 s45, s45, 0
	s_waitcnt vmcnt(16)
	global_load_dwordx4 a[128:131], v192, s[44:45] offset:0
	global_load_dwordx4 a[132:135], v192, s[44:45] offset:1024
	global_load_dwordx4 a[136:139], v192, s[44:45] offset:2048
	global_load_dwordx4 a[140:143], v192, s[44:45] offset:3072
	s_add_u32 s44, s44, 0x1000
	s_addc_u32 s45, s45, 0
	global_load_dwordx4 a[144:147], v192, s[44:45] offset:0
	global_load_dwordx4 a[148:151], v192, s[44:45] offset:1024
	global_load_dwordx4 a[152:155], v192, s[44:45] offset:2048
	global_load_dwordx4 a[156:159], v192, s[44:45] offset:3072
	s_add_u32 s44, s44, 0x1000
	s_addc_u32 s45, s45, 0
	global_load_dwordx4 a[160:163], v192, s[44:45] offset:0
	global_load_dwordx4 a[164:167], v192, s[44:45] offset:1024
	global_load_dwordx4 a[168:171], v192, s[44:45] offset:2048
	global_load_dwordx4 a[172:175], v192, s[44:45] offset:3072
	s_add_u32 s44, s44, 0x1000
	s_addc_u32 s45, s45, 0
	global_load_dwordx4 a[176:179], v192, s[44:45] offset:0
	global_load_dwordx4 a[180:183], v192, s[44:45] offset:1024
	global_load_dwordx4 a[184:187], v192, s[44:45] offset:2048
	global_load_dwordx4 a[188:191], v192, s[44:45] offset:3072
	s_add_u32 s44, s44, 0x1000
	s_addc_u32 s45, s45, 0
	global_load_dwordx4 a[192:195], v192, s[44:45] offset:0
	global_load_dwordx4 a[196:199], v192, s[44:45] offset:1024
	global_load_dwordx4 a[200:203], v192, s[44:45] offset:2048
	global_load_dwordx4 a[204:207], v192, s[44:45] offset:3072
	s_add_u32 s44, s44, 0x1000
	s_addc_u32 s45, s45, 0
	global_load_dwordx4 a[208:211], v192, s[44:45] offset:0
	global_load_dwordx4 a[212:215], v192, s[44:45] offset:1024
	global_load_dwordx4 a[216:219], v192, s[44:45] offset:2048
	global_load_dwordx4 a[220:223], v192, s[44:45] offset:3072
	s_add_u32 s44, s44, 0x1000
	s_addc_u32 s45, s45, 0
	global_load_dwordx4 a[224:227], v192, s[44:45] offset:0
	global_load_dwordx4 a[228:231], v192, s[44:45] offset:1024
	global_load_dwordx4 a[232:235], v192, s[44:45] offset:2048
	global_load_dwordx4 a[236:239], v192, s[44:45] offset:3072
	s_add_u32 s44, s44, 0x1000
	s_addc_u32 s45, s45, 0
	global_load_dwordx4 a[240:243], v192, s[44:45] offset:0
	global_load_dwordx4 a[244:247], v192, s[44:45] offset:1024
	global_load_dwordx4 a[248:251], v192, s[44:45] offset:2048
	global_load_dwordx4 a[252:255], v192, s[44:45] offset:3072
	s_add_u32 s44, s44, 0x1000
	s_addc_u32 s45, s45, 0
	s_lshl_b32 s64, s33, 3
	s_add_u32 s64, s64, s29
	s_lshl_b32 s64, s64, 5
	s_add_u32 s64, s64, s30
	s_lshl_b32 s64, s64, 2
	s_add_u32 s40, s8, s64
	s_addc_u32 s41, s9, 0
	s_and_b32 s64, s33, 1
	s_lshl_b32 s64, s64, 22
	s_add_u32 s64, s64, s50
	s_add_u32 s36, s6, s64
	s_addc_u32 s37, s7, 0
	v_exp_f32_e32 v200, v0
	v_exp_f32_e32 v201, v1
	v_exp_f32_e32 v202, v2
	v_exp_f32_e32 v203, v3
	v_exp_f32_e32 v204, v4
	v_exp_f32_e32 v205, v5
	v_exp_f32_e32 v206, v6
	v_exp_f32_e32 v207, v7
	v_exp_f32_e32 v208, v8
	v_exp_f32_e32 v209, v9
	v_exp_f32_e32 v210, v10
	v_exp_f32_e32 v211, v11
	v_exp_f32_e32 v212, v12
	v_exp_f32_e32 v213, v13
	v_exp_f32_e32 v214, v14
	v_exp_f32_e32 v215, v15
	v_add_f32_e32 v200, 1.0, v200
	v_add_f32_e32 v201, 1.0, v201
	v_add_f32_e32 v202, 1.0, v202
	v_add_f32_e32 v203, 1.0, v203
	v_add_f32_e32 v204, 1.0, v204
	v_add_f32_e32 v205, 1.0, v205
	v_add_f32_e32 v206, 1.0, v206
	v_add_f32_e32 v207, 1.0, v207
	v_add_f32_e32 v208, 1.0, v208
	v_add_f32_e32 v209, 1.0, v209
	v_add_f32_e32 v210, 1.0, v210
	v_add_f32_e32 v211, 1.0, v211
	v_add_f32_e32 v212, 1.0, v212
	v_add_f32_e32 v213, 1.0, v213
	v_add_f32_e32 v214, 1.0, v214
	v_add_f32_e32 v215, 1.0, v215
	v_rcp_f32_e32 v200, v200
	v_rcp_f32_e32 v201, v201
	v_rcp_f32_e32 v202, v202
	v_rcp_f32_e32 v203, v203
	v_rcp_f32_e32 v204, v204
	v_rcp_f32_e32 v205, v205
	v_rcp_f32_e32 v206, v206
	v_rcp_f32_e32 v207, v207
	v_rcp_f32_e32 v208, v208
	v_rcp_f32_e32 v209, v209
	v_rcp_f32_e32 v210, v210
	v_rcp_f32_e32 v211, v211
	v_rcp_f32_e32 v212, v212
	v_rcp_f32_e32 v213, v213
	v_rcp_f32_e32 v214, v214
	v_rcp_f32_e32 v215, v215
	v_fmamk_f32 v208, v208, 0xc0b8aa3b, v198
	v_fmamk_f32 v209, v209, 0xc0b8aa3b, v198
	v_fmamk_f32 v210, v210, 0xc0b8aa3b, v198
	v_fmamk_f32 v211, v211, 0xc0b8aa3b, v198
	v_mul_f32_e32 v204, v204, v128
	v_mul_f32_e32 v205, v205, v129
	v_mul_f32_e32 v206, v206, v130
	v_mul_f32_e32 v207, v207, v131
	v_fma_f32 v128, v200, v208, v204
	v_fma_f32 v129, v201, v209, v205
	v_fma_f32 v130, v202, v210, v206
	v_fma_f32 v131, v203, v211, v207
	v_exp_f32_e32 v200, v128
	v_exp_f32_e32 v201, v129
	v_exp_f32_e32 v202, v130
	v_exp_f32_e32 v203, v131
	v_add_f32_e32 v200, 1.0, v200
	v_add_f32_e32 v201, 1.0, v201
	v_add_f32_e32 v202, 1.0, v202
	v_add_f32_e32 v203, 1.0, v203
	v_rcp_f32_e32 v200, v200
	v_rcp_f32_e32 v201, v201
	v_rcp_f32_e32 v202, v202
	v_rcp_f32_e32 v203, v203
	v_fma_f32 v200, v200, 2.0, -1.0
	v_fma_f32 v201, v201, 2.0, -1.0
	v_fma_f32 v202, v202, 2.0, -1.0
	v_fma_f32 v203, v203, 2.0, -1.0
	v_mul_f32_e32 v216, v212, v200
	v_mul_f32_e32 v217, v213, v201
	v_mul_f32_e32 v218, v214, v202
	v_mul_f32_e32 v219, v215, v203
	v_mul_f32_e32 v236, v216, v228
	v_mul_f32_e32 v237, v216, v232
	v_fmac_f32_e32 v236, v217, v229
	v_fmac_f32_e32 v237, v217, v233
	v_fmac_f32_e32 v236, v218, v230
	v_fmac_f32_e32 v237, v218, v234
	v_fmac_f32_e32 v236, v219, v231
	v_fmac_f32_e32 v237, v219, v235
	v_mov_b32_e32 v238, v236
	v_mov_b32_e32 v240, v237
	s_nop 1
	v_permlane32_swap_b32_e32 v236, v238
	v_permlane32_swap_b32_e32 v237, v240
	v_add_f32_e32 v238, v236, v238
	v_add_f32_e32 v239, v237, v240
	ds_write_b64 v248, v[238:239] offset:0
	v_cvt_pk_f16_f32 v220, v216, v217
	v_cvt_pk_f16_f32 v221, v218, v219
	v_exp_f32_e32 v200, v16
	v_exp_f32_e32 v201, v17
	v_exp_f32_e32 v202, v18
	v_exp_f32_e32 v203, v19
	v_exp_f32_e32 v204, v20
	v_exp_f32_e32 v205, v21
	v_exp_f32_e32 v206, v22
	v_exp_f32_e32 v207, v23
	v_exp_f32_e32 v208, v24
	v_exp_f32_e32 v209, v25
	v_exp_f32_e32 v210, v26
	v_exp_f32_e32 v211, v27
	v_exp_f32_e32 v212, v28
	v_exp_f32_e32 v213, v29
	v_exp_f32_e32 v214, v30
	v_exp_f32_e32 v215, v31
	v_add_f32_e32 v200, 1.0, v200
	v_add_f32_e32 v201, 1.0, v201
	v_add_f32_e32 v202, 1.0, v202
	v_add_f32_e32 v203, 1.0, v203
	v_add_f32_e32 v204, 1.0, v204
	v_add_f32_e32 v205, 1.0, v205
	v_add_f32_e32 v206, 1.0, v206
	v_add_f32_e32 v207, 1.0, v207
	v_add_f32_e32 v208, 1.0, v208
	v_add_f32_e32 v209, 1.0, v209
	v_add_f32_e32 v210, 1.0, v210
	v_add_f32_e32 v211, 1.0, v211
	v_add_f32_e32 v212, 1.0, v212
	v_add_f32_e32 v213, 1.0, v213
	v_add_f32_e32 v214, 1.0, v214
	v_add_f32_e32 v215, 1.0, v215
	v_rcp_f32_e32 v200, v200
	v_rcp_f32_e32 v201, v201
	v_rcp_f32_e32 v202, v202
	v_rcp_f32_e32 v203, v203
	v_rcp_f32_e32 v204, v204
	v_rcp_f32_e32 v205, v205
	v_rcp_f32_e32 v206, v206
	v_rcp_f32_e32 v207, v207
	v_rcp_f32_e32 v208, v208
	v_rcp_f32_e32 v209, v209
	v_rcp_f32_e32 v210, v210
	v_rcp_f32_e32 v211, v211
	v_rcp_f32_e32 v212, v212
	v_rcp_f32_e32 v213, v213
	v_rcp_f32_e32 v214, v214
	v_rcp_f32_e32 v215, v215
	v_fmamk_f32 v208, v208, 0xc0b8aa3b, v198
	v_fmamk_f32 v209, v209, 0xc0b8aa3b, v198
	v_fmamk_f32 v210, v210, 0xc0b8aa3b, v198
	v_fmamk_f32 v211, v211, 0xc0b8aa3b, v198
	v_mul_f32_e32 v204, v204, v132
	v_mul_f32_e32 v205, v205, v133
	v_mul_f32_e32 v206, v206, v134
	v_mul_f32_e32 v207, v207, v135
	v_fma_f32 v132, v200, v208, v204
	v_fma_f32 v133, v201, v209, v205
	v_fma_f32 v134, v202, v210, v206
	v_fma_f32 v135, v203, v211, v207
	v_exp_f32_e32 v200, v132
	v_exp_f32_e32 v201, v133
	v_exp_f32_e32 v202, v134
	v_exp_f32_e32 v203, v135
	v_add_f32_e32 v200, 1.0, v200
	v_add_f32_e32 v201, 1.0, v201
	v_add_f32_e32 v202, 1.0, v202
	v_add_f32_e32 v203, 1.0, v203
	v_rcp_f32_e32 v200, v200
	v_rcp_f32_e32 v201, v201
	v_rcp_f32_e32 v202, v202
	v_rcp_f32_e32 v203, v203
	v_fma_f32 v200, v200, 2.0, -1.0
	v_fma_f32 v201, v201, 2.0, -1.0
	v_fma_f32 v202, v202, 2.0, -1.0
	v_fma_f32 v203, v203, 2.0, -1.0
	v_mul_f32_e32 v216, v212, v200
	v_mul_f32_e32 v217, v213, v201
	v_mul_f32_e32 v218, v214, v202
	v_mul_f32_e32 v219, v215, v203
	v_mul_f32_e32 v236, v216, v228
	v_mul_f32_e32 v237, v216, v232
	v_fmac_f32_e32 v236, v217, v229
	v_fmac_f32_e32 v237, v217, v233
	v_fmac_f32_e32 v236, v218, v230
	v_fmac_f32_e32 v237, v218, v234
	v_fmac_f32_e32 v236, v219, v231
	v_fmac_f32_e32 v237, v219, v235
	v_mov_b32_e32 v238, v236
	v_mov_b32_e32 v240, v237
	s_nop 1
	v_permlane32_swap_b32_e32 v236, v238
	v_permlane32_swap_b32_e32 v237, v240
	v_add_f32_e32 v238, v236, v238
	v_add_f32_e32 v239, v237, v240
	ds_write_b64 v248, v[238:239] offset:256
	v_cvt_pk_f16_f32 v222, v216, v217
	v_cvt_pk_f16_f32 v223, v218, v219
	s_nop 1
	v_permlane32_swap_b32_e32 v220, v222
	v_permlane32_swap_b32_e32 v221, v223
	s_cmp_eq_u32 s31, 0
	s_cbranch_scc1 .LD_slow4
	global_store_dwordx4 v195, v[220:223], s[36:37] offset:0
.LD_join5:
	s_and_b32 s64, s33, 1
	s_lshl_b32 s64, s64, 22
	s_add_u32 s64, s64, s50
	s_add_u32 s64, s64, 0x20000
	s_add_u32 s36, s6, s64
	s_addc_u32 s37, s7, 0
	v_exp_f32_e32 v200, v32
	v_exp_f32_e32 v201, v33
	v_exp_f32_e32 v202, v34
	v_exp_f32_e32 v203, v35
	v_exp_f32_e32 v204, v36
	v_exp_f32_e32 v205, v37
	v_exp_f32_e32 v206, v38
	v_exp_f32_e32 v207, v39
	v_exp_f32_e32 v208, v40
	v_exp_f32_e32 v209, v41
	v_exp_f32_e32 v210, v42
	v_exp_f32_e32 v211, v43
	v_exp_f32_e32 v212, v44
	v_exp_f32_e32 v213, v45
	v_exp_f32_e32 v214, v46
	v_exp_f32_e32 v215, v47
	v_add_f32_e32 v200, 1.0, v200
	v_add_f32_e32 v201, 1.0, v201
	v_add_f32_e32 v202, 1.0, v202
	v_add_f32_e32 v203, 1.0, v203
	v_add_f32_e32 v204, 1.0, v204
	v_add_f32_e32 v205, 1.0, v205
	v_add_f32_e32 v206, 1.0, v206
	v_add_f32_e32 v207, 1.0, v207
	v_add_f32_e32 v208, 1.0, v208
	v_add_f32_e32 v209, 1.0, v209
	v_add_f32_e32 v210, 1.0, v210
	v_add_f32_e32 v211, 1.0, v211
	v_add_f32_e32 v212, 1.0, v212
	v_add_f32_e32 v213, 1.0, v213
	v_add_f32_e32 v214, 1.0, v214
	v_add_f32_e32 v215, 1.0, v215
	v_rcp_f32_e32 v200, v200
	v_rcp_f32_e32 v201, v201
	v_rcp_f32_e32 v202, v202
	v_rcp_f32_e32 v203, v203
	v_rcp_f32_e32 v204, v204
	v_rcp_f32_e32 v205, v205
	v_rcp_f32_e32 v206, v206
	v_rcp_f32_e32 v207, v207
	v_rcp_f32_e32 v208, v208
	v_rcp_f32_e32 v209, v209
	v_rcp_f32_e32 v210, v210
	v_rcp_f32_e32 v211, v211
	v_rcp_f32_e32 v212, v212
	v_rcp_f32_e32 v213, v213
	v_rcp_f32_e32 v214, v214
	v_rcp_f32_e32 v215, v215
	v_fmamk_f32 v208, v208, 0xc0b8aa3b, v198
	v_fmamk_f32 v209, v209, 0xc0b8aa3b, v198
	v_fmamk_f32 v210, v210, 0xc0b8aa3b, v198
	v_fmamk_f32 v211, v211, 0xc0b8aa3b, v198
	v_mul_f32_e32 v204, v204, v136
	v_mul_f32_e32 v205, v205, v137
	v_mul_f32_e32 v206, v206, v138
	v_mul_f32_e32 v207, v207, v139
	v_fma_f32 v136, v200, v208, v204
	v_fma_f32 v137, v201, v209, v205
	v_fma_f32 v138, v202, v210, v206
	v_fma_f32 v139, v203, v211, v207
	v_exp_f32_e32 v200, v136
	v_exp_f32_e32 v201, v137
	v_exp_f32_e32 v202, v138
	v_exp_f32_e32 v203, v139
	v_add_f32_e32 v200, 1.0, v200
	v_add_f32_e32 v201, 1.0, v201
	v_add_f32_e32 v202, 1.0, v202
	v_add_f32_e32 v203, 1.0, v203
	v_rcp_f32_e32 v200, v200
	v_rcp_f32_e32 v201, v201
	v_rcp_f32_e32 v202, v202
	v_rcp_f32_e32 v203, v203
	v_fma_f32 v200, v200, 2.0, -1.0
	v_fma_f32 v201, v201, 2.0, -1.0
	v_fma_f32 v202, v202, 2.0, -1.0
	v_fma_f32 v203, v203, 2.0, -1.0
	v_mul_f32_e32 v216, v212, v200
	v_mul_f32_e32 v217, v213, v201
	v_mul_f32_e32 v218, v214, v202
	v_mul_f32_e32 v219, v215, v203
	v_mul_f32_e32 v236, v216, v228
	v_mul_f32_e32 v237, v216, v232
	v_fmac_f32_e32 v236, v217, v229
	v_fmac_f32_e32 v237, v217, v233
	v_fmac_f32_e32 v236, v218, v230
	v_fmac_f32_e32 v237, v218, v234
	v_fmac_f32_e32 v236, v219, v231
	v_fmac_f32_e32 v237, v219, v235
	v_mov_b32_e32 v238, v236
	v_mov_b32_e32 v240, v237
	s_nop 1
	v_permlane32_swap_b32_e32 v236, v238
	v_permlane32_swap_b32_e32 v237, v240
	v_add_f32_e32 v238, v236, v238
	v_add_f32_e32 v239, v237, v240
	ds_write_b64 v248, v[238:239] offset:512
	v_cvt_pk_f16_f32 v220, v216, v217
	v_cvt_pk_f16_f32 v221, v218, v219
	v_exp_f32_e32 v200, v48
	v_exp_f32_e32 v201, v49
	v_exp_f32_e32 v202, v50
	v_exp_f32_e32 v203, v51
	v_exp_f32_e32 v204, v52
	v_exp_f32_e32 v205, v53
	v_exp_f32_e32 v206, v54
	v_exp_f32_e32 v207, v55
	v_exp_f32_e32 v208, v56
	v_exp_f32_e32 v209, v57
	v_exp_f32_e32 v210, v58
	v_exp_f32_e32 v211, v59
	v_exp_f32_e32 v212, v60
	v_exp_f32_e32 v213, v61
	v_exp_f32_e32 v214, v62
	v_exp_f32_e32 v215, v63
	v_add_f32_e32 v200, 1.0, v200
	v_add_f32_e32 v201, 1.0, v201
	v_add_f32_e32 v202, 1.0, v202
	v_add_f32_e32 v203, 1.0, v203
	v_add_f32_e32 v204, 1.0, v204
	v_add_f32_e32 v205, 1.0, v205
	v_add_f32_e32 v206, 1.0, v206
	v_add_f32_e32 v207, 1.0, v207
	v_add_f32_e32 v208, 1.0, v208
	v_add_f32_e32 v209, 1.0, v209
	v_add_f32_e32 v210, 1.0, v210
	v_add_f32_e32 v211, 1.0, v211
	v_add_f32_e32 v212, 1.0, v212
	v_add_f32_e32 v213, 1.0, v213
	v_add_f32_e32 v214, 1.0, v214
	v_add_f32_e32 v215, 1.0, v215
	v_rcp_f32_e32 v200, v200
	v_rcp_f32_e32 v201, v201
	v_rcp_f32_e32 v202, v202
	v_rcp_f32_e32 v203, v203
	v_rcp_f32_e32 v204, v204
	v_rcp_f32_e32 v205, v205
	v_rcp_f32_e32 v206, v206
	v_rcp_f32_e32 v207, v207
	v_rcp_f32_e32 v208, v208
	v_rcp_f32_e32 v209, v209
	v_rcp_f32_e32 v210, v210
	v_rcp_f32_e32 v211, v211
	v_rcp_f32_e32 v212, v212
	v_rcp_f32_e32 v213, v213
	v_rcp_f32_e32 v214, v214
	v_rcp_f32_e32 v215, v215
	v_fmamk_f32 v208, v208, 0xc0b8aa3b, v198
	v_fmamk_f32 v209, v209, 0xc0b8aa3b, v198
	v_fmamk_f32 v210, v210, 0xc0b8aa3b, v198
	v_fmamk_f32 v211, v211, 0xc0b8aa3b, v198
	v_mul_f32_e32 v204, v204, v140
	v_mul_f32_e32 v205, v205, v141
	v_mul_f32_e32 v206, v206, v142
	v_mul_f32_e32 v207, v207, v143
	v_fma_f32 v140, v200, v208, v204
	v_fma_f32 v141, v201, v209, v205
	v_fma_f32 v142, v202, v210, v206
	v_fma_f32 v143, v203, v211, v207
	v_exp_f32_e32 v200, v140
	v_exp_f32_e32 v201, v141
	v_exp_f32_e32 v202, v142
	v_exp_f32_e32 v203, v143
	v_add_f32_e32 v200, 1.0, v200
	v_add_f32_e32 v201, 1.0, v201
	v_add_f32_e32 v202, 1.0, v202
	v_add_f32_e32 v203, 1.0, v203
	v_rcp_f32_e32 v200, v200
	v_rcp_f32_e32 v201, v201
	v_rcp_f32_e32 v202, v202
	v_rcp_f32_e32 v203, v203
	v_fma_f32 v200, v200, 2.0, -1.0
	v_fma_f32 v201, v201, 2.0, -1.0
	v_fma_f32 v202, v202, 2.0, -1.0
	v_fma_f32 v203, v203, 2.0, -1.0
	v_mul_f32_e32 v216, v212, v200
	v_mul_f32_e32 v217, v213, v201
	v_mul_f32_e32 v218, v214, v202
	v_mul_f32_e32 v219, v215, v203
	v_mul_f32_e32 v236, v216, v228
	v_mul_f32_e32 v237, v216, v232
	v_fmac_f32_e32 v236, v217, v229
	v_fmac_f32_e32 v237, v217, v233
	v_fmac_f32_e32 v236, v218, v230
	v_fmac_f32_e32 v237, v218, v234
	v_fmac_f32_e32 v236, v219, v231
	v_fmac_f32_e32 v237, v219, v235
	v_mov_b32_e32 v238, v236
	v_mov_b32_e32 v240, v237
	s_nop 1
	v_permlane32_swap_b32_e32 v236, v238
	v_permlane32_swap_b32_e32 v237, v240
	v_add_f32_e32 v238, v236, v238
	v_add_f32_e32 v239, v237, v240
	ds_write_b64 v248, v[238:239] offset:768
	v_cvt_pk_f16_f32 v222, v216, v217
	v_cvt_pk_f16_f32 v223, v218, v219
	s_nop 1
	v_permlane32_swap_b32_e32 v220, v222
	v_permlane32_swap_b32_e32 v221, v223
	s_cmp_eq_u32 s31, 0
	s_cbranch_scc1 .LD_slow6
	global_store_dwordx4 v195, v[220:223], s[36:37] offset:0
.LD_join7:
	s_and_b32 s64, s33, 1
	s_lshl_b32 s64, s64, 22
	s_add_u32 s64, s64, s50
	s_add_u32 s64, s64, 0x40000
	s_add_u32 s36, s6, s64
	s_addc_u32 s37, s7, 0
	v_exp_f32_e32 v200, v64
	v_exp_f32_e32 v201, v65
	v_exp_f32_e32 v202, v66
	v_exp_f32_e32 v203, v67
	v_exp_f32_e32 v204, v68
	v_exp_f32_e32 v205, v69
	v_exp_f32_e32 v206, v70
	v_exp_f32_e32 v207, v71
	v_exp_f32_e32 v208, v72
	v_exp_f32_e32 v209, v73
	v_exp_f32_e32 v210, v74
	v_exp_f32_e32 v211, v75
	v_exp_f32_e32 v212, v76
	v_exp_f32_e32 v213, v77
	v_exp_f32_e32 v214, v78
	v_exp_f32_e32 v215, v79
	v_add_f32_e32 v200, 1.0, v200
	v_add_f32_e32 v201, 1.0, v201
	v_add_f32_e32 v202, 1.0, v202
	v_add_f32_e32 v203, 1.0, v203
	v_add_f32_e32 v204, 1.0, v204
	v_add_f32_e32 v205, 1.0, v205
	v_add_f32_e32 v206, 1.0, v206
	v_add_f32_e32 v207, 1.0, v207
	v_add_f32_e32 v208, 1.0, v208
	v_add_f32_e32 v209, 1.0, v209
	v_add_f32_e32 v210, 1.0, v210
	v_add_f32_e32 v211, 1.0, v211
	v_add_f32_e32 v212, 1.0, v212
	v_add_f32_e32 v213, 1.0, v213
	v_add_f32_e32 v214, 1.0, v214
	v_add_f32_e32 v215, 1.0, v215
	v_rcp_f32_e32 v200, v200
	v_rcp_f32_e32 v201, v201
	v_rcp_f32_e32 v202, v202
	v_rcp_f32_e32 v203, v203
	v_rcp_f32_e32 v204, v204
	v_rcp_f32_e32 v205, v205
	v_rcp_f32_e32 v206, v206
	v_rcp_f32_e32 v207, v207
	v_rcp_f32_e32 v208, v208
	v_rcp_f32_e32 v209, v209
	v_rcp_f32_e32 v210, v210
	v_rcp_f32_e32 v211, v211
	v_rcp_f32_e32 v212, v212
	v_rcp_f32_e32 v213, v213
	v_rcp_f32_e32 v214, v214
	v_rcp_f32_e32 v215, v215
	v_fmamk_f32 v208, v208, 0xc0b8aa3b, v198
	v_fmamk_f32 v209, v209, 0xc0b8aa3b, v198
	v_fmamk_f32 v210, v210, 0xc0b8aa3b, v198
	v_fmamk_f32 v211, v211, 0xc0b8aa3b, v198
	v_mul_f32_e32 v204, v204, v144
	v_mul_f32_e32 v205, v205, v145
	v_mul_f32_e32 v206, v206, v146
	v_mul_f32_e32 v207, v207, v147
	v_fma_f32 v144, v200, v208, v204
	v_fma_f32 v145, v201, v209, v205
	v_fma_f32 v146, v202, v210, v206
	v_fma_f32 v147, v203, v211, v207
	v_exp_f32_e32 v200, v144
	v_exp_f32_e32 v201, v145
	v_exp_f32_e32 v202, v146
	v_exp_f32_e32 v203, v147
	v_add_f32_e32 v200, 1.0, v200
	v_add_f32_e32 v201, 1.0, v201
	v_add_f32_e32 v202, 1.0, v202
	v_add_f32_e32 v203, 1.0, v203
	v_rcp_f32_e32 v200, v200
	v_rcp_f32_e32 v201, v201
	v_rcp_f32_e32 v202, v202
	v_rcp_f32_e32 v203, v203
	v_fma_f32 v200, v200, 2.0, -1.0
	v_fma_f32 v201, v201, 2.0, -1.0
	v_fma_f32 v202, v202, 2.0, -1.0
	v_fma_f32 v203, v203, 2.0, -1.0
	v_mul_f32_e32 v216, v212, v200
	v_mul_f32_e32 v217, v213, v201
	v_mul_f32_e32 v218, v214, v202
	v_mul_f32_e32 v219, v215, v203
	v_mul_f32_e32 v236, v216, v228
	v_mul_f32_e32 v237, v216, v232
	v_fmac_f32_e32 v236, v217, v229
	v_fmac_f32_e32 v237, v217, v233
	v_fmac_f32_e32 v236, v218, v230
	v_fmac_f32_e32 v237, v218, v234
	v_fmac_f32_e32 v236, v219, v231
	v_fmac_f32_e32 v237, v219, v235
	v_mov_b32_e32 v238, v236
	v_mov_b32_e32 v240, v237
	s_nop 1
	v_permlane32_swap_b32_e32 v236, v238
	v_permlane32_swap_b32_e32 v237, v240
	v_add_f32_e32 v238, v236, v238
	v_add_f32_e32 v239, v237, v240
	ds_write_b64 v248, v[238:239] offset:1024
	v_cvt_pk_f16_f32 v220, v216, v217
	v_cvt_pk_f16_f32 v221, v218, v219
	v_exp_f32_e32 v200, v80
	v_exp_f32_e32 v201, v81
	v_exp_f32_e32 v202, v82
	v_exp_f32_e32 v203, v83
	v_exp_f32_e32 v204, v84
	v_exp_f32_e32 v205, v85
	v_exp_f32_e32 v206, v86
	v_exp_f32_e32 v207, v87
	v_exp_f32_e32 v208, v88
	v_exp_f32_e32 v209, v89
	v_exp_f32_e32 v210, v90
	v_exp_f32_e32 v211, v91
	v_exp_f32_e32 v212, v92
	v_exp_f32_e32 v213, v93
	v_exp_f32_e32 v214, v94
	v_exp_f32_e32 v215, v95
	v_add_f32_e32 v200, 1.0, v200
	v_add_f32_e32 v201, 1.0, v201
	v_add_f32_e32 v202, 1.0, v202
	v_add_f32_e32 v203, 1.0, v203
	v_add_f32_e32 v204, 1.0, v204
	v_add_f32_e32 v205, 1.0, v205
	v_add_f32_e32 v206, 1.0, v206
	v_add_f32_e32 v207, 1.0, v207
	v_add_f32_e32 v208, 1.0, v208
	v_add_f32_e32 v209, 1.0, v209
	v_add_f32_e32 v210, 1.0, v210
	v_add_f32_e32 v211, 1.0, v211
	v_add_f32_e32 v212, 1.0, v212
	v_add_f32_e32 v213, 1.0, v213
	v_add_f32_e32 v214, 1.0, v214
	v_add_f32_e32 v215, 1.0, v215
	v_rcp_f32_e32 v200, v200
	v_rcp_f32_e32 v201, v201
	v_rcp_f32_e32 v202, v202
	v_rcp_f32_e32 v203, v203
	v_rcp_f32_e32 v204, v204
	v_rcp_f32_e32 v205, v205
	v_rcp_f32_e32 v206, v206
	v_rcp_f32_e32 v207, v207
	v_rcp_f32_e32 v208, v208
	v_rcp_f32_e32 v209, v209
	v_rcp_f32_e32 v210, v210
	v_rcp_f32_e32 v211, v211
	v_rcp_f32_e32 v212, v212
	v_rcp_f32_e32 v213, v213
	v_rcp_f32_e32 v214, v214
	v_rcp_f32_e32 v215, v215
	v_fmamk_f32 v208, v208, 0xc0b8aa3b, v198
	v_fmamk_f32 v209, v209, 0xc0b8aa3b, v198
	v_fmamk_f32 v210, v210, 0xc0b8aa3b, v198
	v_fmamk_f32 v211, v211, 0xc0b8aa3b, v198
	v_mul_f32_e32 v204, v204, v148
	v_mul_f32_e32 v205, v205, v149
	v_mul_f32_e32 v206, v206, v150
	v_mul_f32_e32 v207, v207, v151
	v_fma_f32 v148, v200, v208, v204
	v_fma_f32 v149, v201, v209, v205
	v_fma_f32 v150, v202, v210, v206
	v_fma_f32 v151, v203, v211, v207
	v_exp_f32_e32 v200, v148
	v_exp_f32_e32 v201, v149
	v_exp_f32_e32 v202, v150
	v_exp_f32_e32 v203, v151
	v_add_f32_e32 v200, 1.0, v200
	v_add_f32_e32 v201, 1.0, v201
	v_add_f32_e32 v202, 1.0, v202
	v_add_f32_e32 v203, 1.0, v203
	v_rcp_f32_e32 v200, v200
	v_rcp_f32_e32 v201, v201
	v_rcp_f32_e32 v202, v202
	v_rcp_f32_e32 v203, v203
	v_fma_f32 v200, v200, 2.0, -1.0
	v_fma_f32 v201, v201, 2.0, -1.0
	v_fma_f32 v202, v202, 2.0, -1.0
	v_fma_f32 v203, v203, 2.0, -1.0
	v_mul_f32_e32 v216, v212, v200
	v_mul_f32_e32 v217, v213, v201
	v_mul_f32_e32 v218, v214, v202
	v_mul_f32_e32 v219, v215, v203
	v_mul_f32_e32 v236, v216, v228
	v_mul_f32_e32 v237, v216, v232
	v_fmac_f32_e32 v236, v217, v229
	v_fmac_f32_e32 v237, v217, v233
	v_fmac_f32_e32 v236, v218, v230
	v_fmac_f32_e32 v237, v218, v234
	v_fmac_f32_e32 v236, v219, v231
	v_fmac_f32_e32 v237, v219, v235
	v_mov_b32_e32 v238, v236
	v_mov_b32_e32 v240, v237
	s_nop 1
	v_permlane32_swap_b32_e32 v236, v238
	v_permlane32_swap_b32_e32 v237, v240
	v_add_f32_e32 v238, v236, v238
	v_add_f32_e32 v239, v237, v240
	ds_write_b64 v248, v[238:239] offset:1280
	v_cvt_pk_f16_f32 v222, v216, v217
	v_cvt_pk_f16_f32 v223, v218, v219
	s_nop 1
	v_permlane32_swap_b32_e32 v220, v222
	v_permlane32_swap_b32_e32 v221, v223
	s_cmp_eq_u32 s31, 0
	s_cbranch_scc1 .LD_slow8
	global_store_dwordx4 v195, v[220:223], s[36:37] offset:0

.LD_loop12:
	s_sub_u32 s71, s33, 1
	s_add_u32 s61, s33, 1
	s_min_u32 s61, s61, s60
	s_and_b32 s64, s71, 1
	s_lshl_b32 s64, s64, 22
	s_add_u32 s64, s64, s50
	s_add_u32 s64, s64, 0x60000
	s_add_u32 s36, s6, s64
	s_addc_u32 s37, s7, 0
	s_lshl_b32 s64, s71, 3
	s_add_u32 s64, s64, s29
	s_lshl_b32 s64, s64, 5
	s_add_u32 s64, s64, s30
	s_lshl_b32 s64, s64, 2
	s_add_u32 s40, s8, s64
	s_addc_u32 s41, s9, 0
	s_lshl_b32 s64, s71, 19
	s_add_u32 s64, s64, 0x600
	s_add_u32 s72, s62, s64
	s_addc_u32 s73, s63, 0
	s_nop 3
	s_waitcnt lgkmcnt(2)
	v_mfma_f32_32x32x16_f16 v[0:15], a[0:3], v[160:163], v[0:15]
	ds_read_b128 v[160:163], v192 offset:8192
	v_exp_f32_e32 v200, v96
	v_mfma_f32_32x32x16_f16 v[16:31], a[0:3], v[164:167], v[16:31]
	ds_read_b128 v[164:167], v192 offset:9216
	s_lshl_b32 s64, s71, 3
	s_add_u32 s64, s64, s29
	s_lshl_b32 s64, s64, 7
	s_add_u32 s38, s8, s64
	s_addc_u32 s39, s9, 0
	global_load_dword v251, v196, s[38:39] sc1
	v_exp_f32_e32 v201, v97
	v_add_f32_e32 v200, 1.0, v200
	v_mfma_f32_32x32x16_f16 v[0:15], a[4:7], v[168:171], v[0:15]
	ds_read_b128 v[168:171], v192 offset:10240
	v_exp_f32_e32 v202, v98
	v_add_f32_e32 v201, 1.0, v201
	v_mfma_f32_32x32x16_f16 v[16:31], a[4:7], v[172:175], v[16:31]
	ds_read_b128 v[172:175], v192 offset:11264
	global_load_lds_dwordx4 v192, s[44:45] offset:1024 sc1
	v_exp_f32_e32 v203, v99
	v_add_f32_e32 v202, 1.0, v202
	v_mfma_f32_32x32x16_f16 v[0:15], a[8:11], v[176:179], v[0:15]
	ds_read_b128 v[176:179], v192 offset:12288
	v_exp_f32_e32 v204, v100
	v_add_f32_e32 v203, 1.0, v203
	v_mfma_f32_32x32x16_f16 v[16:31], a[8:11], v[180:183], v[16:31]
	ds_read_b128 v[180:183], v192 offset:13312
	v_exp_f32_e32 v205, v101
	v_add_f32_e32 v204, 1.0, v204
	s_waitcnt lgkmcnt(2)
	v_mfma_f32_32x32x16_f16 v[0:15], a[12:15], v[184:187], v[0:15]
	ds_read_b128 v[184:187], v192 offset:14336
	v_exp_f32_e32 v206, v102
	v_add_f32_e32 v205, 1.0, v205
	v_mfma_f32_32x32x16_f16 v[16:31], a[12:15], v[188:191], v[16:31]
	ds_read_b128 v[188:191], v192 offset:15360
	global_load_lds_dwordx4 v192, s[44:45] offset:2048 sc1
	v_exp_f32_e32 v207, v103
	v_add_f32_e32 v206, 1.0, v206
	v_mfma_f32_32x32x16_f16 v[0:15], a[16:19], v[160:163], v[0:15]
	ds_read_b128 v[160:163], v192 offset:16384
	v_exp_f32_e32 v208, v104
	v_add_f32_e32 v207, 1.0, v207
	v_mfma_f32_32x32x16_f16 v[16:31], a[16:19], v[164:167], v[16:31]
	ds_read_b128 v[164:167], v192 offset:17408
	v_exp_f32_e32 v209, v105
	v_add_f32_e32 v208, 1.0, v208
	v_mfma_f32_32x32x16_f16 v[0:15], a[20:23], v[168:171], v[0:15]
	ds_read_b128 v[168:171], v192 offset:18432
	v_exp_f32_e32 v210, v106
	v_add_f32_e32 v209, 1.0, v209
	v_mfma_f32_32x32x16_f16 v[16:31], a[20:23], v[172:175], v[16:31]
	ds_read_b128 v[172:175], v192 offset:19456
	global_load_lds_dwordx4 v192, s[44:45] offset:3072 sc1
	v_exp_f32_e32 v211, v107
	v_add_f32_e32 v210, 1.0, v210
	s_waitcnt lgkmcnt(2)
	v_mfma_f32_32x32x16_f16 v[0:15], a[24:27], v[176:179], v[0:15]
	ds_read_b128 v[176:179], v192 offset:20480
	v_exp_f32_e32 v212, v108
	v_add_f32_e32 v211, 1.0, v211
	v_mfma_f32_32x32x16_f16 v[16:31], a[24:27], v[180:183], v[16:31]
	ds_read_b128 v[180:183], v192 offset:21504
	v_exp_f32_e32 v213, v109
	v_add_f32_e32 v212, 1.0, v212
	v_mfma_f32_32x32x16_f16 v[0:15], a[28:31], v[184:187], v[0:15]
	ds_read_b128 v[184:187], v192 offset:22528
	v_exp_f32_e32 v214, v110
	v_add_f32_e32 v213, 1.0, v213
	v_mfma_f32_32x32x16_f16 v[16:31], a[28:31], v[188:191], v[16:31]
	ds_read_b128 v[188:191], v192 offset:23552
	s_mov_b32 m0, s57
	s_add_u32 s44, s34, 0x11000
	s_addc_u32 s45, s35, 0
	global_load_lds_dwordx4 v192, s[44:45] sc1
	v_exp_f32_e32 v215, v111
	v_add_f32_e32 v214, 1.0, v214
	v_mfma_f32_32x32x16_f16 v[0:15], a[32:35], v[160:163], v[0:15]
	ds_read_b128 v[160:163], v192 offset:24576
	v_add_f32_e32 v215, 1.0, v215
	v_rcp_f32_e32 v200, v200
	v_mfma_f32_32x32x16_f16 v[16:31], a[32:35], v[164:167], v[16:31]
	ds_read_b128 v[164:167], v192 offset:25600
	v_rcp_f32_e32 v201, v201
	s_waitcnt lgkmcnt(2)
	v_mfma_f32_32x32x16_f16 v[0:15], a[36:39], v[168:171], v[0:15]
	ds_read_b128 v[168:171], v192 offset:26624
	v_rcp_f32_e32 v202, v202
	v_mfma_f32_32x32x16_f16 v[16:31], a[36:39], v[172:175], v[16:31]
	ds_read_b128 v[172:175], v192 offset:27648
	global_load_lds_dwordx4 v192, s[44:45] offset:1024 sc1
	v_rcp_f32_e32 v203, v203
	v_mfma_f32_32x32x16_f16 v[0:15], a[40:43], v[176:179], v[0:15]
	ds_read_b128 v[176:179], v192 offset:28672
	v_rcp_f32_e32 v204, v204
	v_mfma_f32_32x32x16_f16 v[16:31], a[40:43], v[180:183], v[16:31]
	ds_read_b128 v[180:183], v192 offset:29696
	v_rcp_f32_e32 v205, v205
	v_mul_f32_e32 v204, v204, v152
	v_mfma_f32_32x32x16_f16 v[0:15], a[44:47], v[184:187], v[0:15]
	ds_read_b128 v[184:187], v192 offset:30720
	v_rcp_f32_e32 v206, v206
	v_mul_f32_e32 v205, v205, v153
	v_mfma_f32_32x32x16_f16 v[16:31], a[44:47], v[188:191], v[16:31]
	ds_read_b128 v[188:191], v192 offset:31744
	global_load_lds_dwordx4 v192, s[44:45] offset:2048 sc1
	v_rcp_f32_e32 v207, v207
	v_mul_f32_e32 v206, v206, v154
	s_waitcnt vmcnt(8)
	s_barrier
	s_waitcnt lgkmcnt(2)
	v_mfma_f32_32x32x16_f16 v[0:15], a[48:51], v[160:163], v[0:15]
	ds_read_b128 v[160:163], v192 offset:32768
	v_rcp_f32_e32 v208, v208
	v_mul_f32_e32 v207, v207, v155
	v_mfma_f32_32x32x16_f16 v[16:31], a[48:51], v[164:167], v[16:31]
	ds_read_b128 v[164:167], v192 offset:33792
	v_rcp_f32_e32 v209, v209
	v_fmamk_f32 v208, v208, 0xc0b8aa3b, v198
	v_mfma_f32_32x32x16_f16 v[0:15], a[52:55], v[168:171], v[0:15]
	ds_read_b128 v[168:171], v192 offset:34816
	v_rcp_f32_e32 v210, v210
	v_fmamk_f32 v209, v209, 0xc0b8aa3b, v198
	v_fma_f32 v152, v200, v208, v204
	v_mfma_f32_32x32x16_f16 v[16:31], a[52:55], v[172:175], v[16:31]
	ds_read_b128 v[172:175], v192 offset:35840
	global_load_lds_dwordx4 v192, s[44:45] offset:3072 sc1
	v_rcp_f32_e32 v211, v211
	v_fmamk_f32 v210, v210, 0xc0b8aa3b, v198
	v_fma_f32 v153, v201, v209, v205
	v_mfma_f32_32x32x16_f16 v[0:15], a[56:59], v[176:179], v[0:15]
	ds_read_b128 v[176:179], v192 offset:36864
	v_rcp_f32_e32 v212, v212
	v_fmamk_f32 v211, v211, 0xc0b8aa3b, v198
	v_fma_f32 v154, v202, v210, v206
	v_mfma_f32_32x32x16_f16 v[16:31], a[56:59], v[180:183], v[16:31]
	ds_read_b128 v[180:183], v192 offset:37888
	v_rcp_f32_e32 v213, v213
	v_fma_f32 v155, v203, v211, v207
	s_waitcnt lgkmcnt(2)
	v_mfma_f32_32x32x16_f16 v[0:15], a[60:63], v[184:187], v[0:15]
	ds_read_b128 v[184:187], v192 offset:38912
	v_rcp_f32_e32 v214, v214
	v_mfma_f32_32x32x16_f16 v[16:31], a[60:63], v[188:191], v[16:31]
	ds_read_b128 v[188:191], v192 offset:39936
	s_mov_b32 m0, s58
	s_add_u32 s44, s34, 0x18000
	s_addc_u32 s45, s35, 0
	global_load_lds_dwordx4 v192, s[44:45] sc1
	v_rcp_f32_e32 v215, v215
	v_mfma_f32_32x32x16_f16 v[0:15], a[64:67], v[160:163], v[0:15]
	ds_read_b128 v[160:163], v192 offset:40960
	v_exp_f32_e32 v200, v152
	v_mfma_f32_32x32x16_f16 v[16:31], a[64:67], v[164:167], v[16:31]
	ds_read_b128 v[164:167], v192 offset:41984
	v_exp_f32_e32 v201, v153
	v_add_f32_e32 v200, 1.0, v200
	v_mfma_f32_32x32x16_f16 v[0:15], a[68:71], v[168:171], v[0:15]
	ds_read_b128 v[168:171], v192 offset:43008
	v_exp_f32_e32 v202, v154
	v_add_f32_e32 v201, 1.0, v201
	v_mfma_f32_32x32x16_f16 v[16:31], a[68:71], v[172:175], v[16:31]
	ds_read_b128 v[172:175], v192 offset:44032
	global_load_lds_dwordx4 v192, s[44:45] offset:1024 sc1
	v_exp_f32_e32 v203, v155
	v_add_f32_e32 v202, 1.0, v202
	s_waitcnt lgkmcnt(2)
	v_mfma_f32_32x32x16_f16 v[0:15], a[72:75], v[176:179], v[0:15]
	ds_read_b128 v[176:179], v192 offset:45056
	v_add_f32_e32 v203, 1.0, v203
	v_rcp_f32_e32 v200, v200
	v_mfma_f32_32x32x16_f16 v[16:31], a[72:75], v[180:183], v[16:31]
	ds_read_b128 v[180:183], v192 offset:46080
	v_rcp_f32_e32 v201, v201
	v_fma_f32 v200, v200, 2.0, -1.0
	v_mfma_f32_32x32x16_f16 v[0:15], a[76:79], v[184:187], v[0:15]
	ds_read_b128 v[184:187], v192 offset:47104
	v_rcp_f32_e32 v202, v202
	v_fma_f32 v201, v201, 2.0, -1.0
	v_mul_f32_e32 v216, v212, v200
	v_mfma_f32_32x32x16_f16 v[16:31], a[76:79], v[188:191], v[16:31]
	ds_read_b128 v[188:191], v192 offset:48128
	global_load_lds_dwordx4 v192, s[44:45] offset:2048 sc1
	v_rcp_f32_e32 v203, v203
	v_fma_f32 v202, v202, 2.0, -1.0
	v_mul_f32_e32 v217, v213, v201
	v_mfma_f32_32x32x16_f16 v[0:15], a[80:83], v[160:163], v[0:15]
	ds_read_b128 v[160:163], v192 offset:49152
	v_fma_f32 v203, v203, 2.0, -1.0
	v_mul_f32_e32 v218, v214, v202
	v_exp_f32_e32 v200, v112
	v_mfma_f32_32x32x16_f16 v[16:31], a[80:83], v[164:167], v[16:31]
	ds_read_b128 v[164:167], v192 offset:50176
	v_mul_f32_e32 v219, v215, v203
	v_mul_f32_e32 v236, v216, v228
	v_exp_f32_e32 v201, v113
	s_waitcnt lgkmcnt(2)
	v_mfma_f32_32x32x16_f16 v[0:15], a[84:87], v[168:171], v[0:15]
	ds_read_b128 v[168:171], v192 offset:51200
	v_mul_f32_e32 v237, v216, v232
	v_fmac_f32_e32 v236, v217, v229
	v_exp_f32_e32 v202, v114
	v_mfma_f32_32x32x16_f16 v[16:31], a[84:87], v[172:175], v[16:31]
	ds_read_b128 v[172:175], v192 offset:52224
	global_load_lds_dwordx4 v192, s[44:45] offset:3072 sc1
	v_fmac_f32_e32 v237, v217, v233
	v_fmac_f32_e32 v236, v218, v230
	v_exp_f32_e32 v203, v115
	v_mfma_f32_32x32x16_f16 v[0:15], a[88:91], v[176:179], v[0:15]
	ds_read_b128 v[176:179], v192 offset:53248
	v_fmac_f32_e32 v237, v218, v234
	v_fmac_f32_e32 v236, v219, v231
	v_exp_f32_e32 v204, v116
	v_mfma_f32_32x32x16_f16 v[16:31], a[88:91], v[180:183], v[16:31]
	ds_read_b128 v[180:183], v192 offset:54272
	v_fmac_f32_e32 v237, v219, v235
	v_mov_b32_e32 v238, v236
	v_exp_f32_e32 v205, v117
	v_mfma_f32_32x32x16_f16 v[0:15], a[92:95], v[184:187], v[0:15]
	ds_read_b128 v[184:187], v192 offset:55296
	v_mov_b32_e32 v240, v237
	v_cvt_pk_f16_f32 v220, v216, v217
	v_exp_f32_e32 v206, v118
	v_mfma_f32_32x32x16_f16 v[16:31], a[92:95], v[188:191], v[16:31]
	ds_read_b128 v[188:191], v192 offset:56320
	s_mov_b32 m0, s59
	s_add_u32 s44, s34, 0x19000
	s_addc_u32 s45, s35, 0
	global_load_lds_dwordx4 v192, s[44:45] sc1
	v_permlane32_swap_b32_e32 v236, v238
	v_permlane32_swap_b32_e32 v237, v240
	v_add_f32_e32 v238, v236, v238
	v_add_f32_e32 v239, v237, v240
	ds_write_b64 v248, v[238:239] offset:1536
	v_exp_f32_e32 v207, v119
	s_waitcnt lgkmcnt(3)
	v_mfma_f32_32x32x16_f16 v[0:15], a[96:99], v[160:163], v[0:15]
	ds_read_b128 v[160:163], v192 offset:57344
	v_cvt_pk_f16_f32 v221, v218, v219
	v_exp_f32_e32 v208, v120
	v_add_f32_e32 v200, 1.0, v200
	v_mfma_f32_32x32x16_f16 v[16:31], a[96:99], v[164:167], v[16:31]
	ds_read_b128 v[164:167], v192 offset:58368
	v_exp_f32_e32 v209, v121
	v_add_f32_e32 v201, 1.0, v201
	v_add_f32_e32 v202, 1.0, v202
	v_mfma_f32_32x32x16_f16 v[0:15], a[100:103], v[168:171], v[0:15]
	ds_read_b128 v[168:171], v192 offset:59392
	v_exp_f32_e32 v210, v122
	v_add_f32_e32 v203, 1.0, v203
	v_add_f32_e32 v204, 1.0, v204
	v_mfma_f32_32x32x16_f16 v[16:31], a[100:103], v[172:175], v[16:31]
	ds_read_b128 v[172:175], v192 offset:60416
	global_load_lds_dwordx4 v192, s[44:45] offset:1024 sc1
	v_exp_f32_e32 v211, v123
	v_add_f32_e32 v205, 1.0, v205
	v_add_f32_e32 v206, 1.0, v206
	v_mfma_f32_32x32x16_f16 v[0:15], a[104:107], v[176:179], v[0:15]
	ds_read_b128 v[176:179], v192 offset:61440
	v_exp_f32_e32 v212, v124
	v_add_f32_e32 v207, 1.0, v207
	v_add_f32_e32 v208, 1.0, v208
	v_mfma_f32_32x32x16_f16 v[16:31], a[104:107], v[180:183], v[16:31]
	ds_read_b128 v[180:183], v192 offset:62464
	v_exp_f32_e32 v213, v125
	v_add_f32_e32 v209, 1.0, v209
	v_add_f32_e32 v210, 1.0, v210
	s_waitcnt lgkmcnt(2)
	v_mfma_f32_32x32x16_f16 v[0:15], a[108:111], v[184:187], v[0:15]
	ds_read_b128 v[184:187], v192 offset:63488
	v_exp_f32_e32 v214, v126
	v_add_f32_e32 v211, 1.0, v211
	v_add_f32_e32 v212, 1.0, v212
	v_mfma_f32_32x32x16_f16 v[16:31], a[108:111], v[188:191], v[16:31]
	ds_read_b128 v[188:191], v192 offset:64512
	global_load_lds_dwordx4 v192, s[44:45] offset:2048 sc1
	v_exp_f32_e32 v215, v127
	v_add_f32_e32 v213, 1.0, v213
	v_add_f32_e32 v214, 1.0, v214
	s_waitcnt vmcnt(7)
	s_barrier
	v_mfma_f32_32x32x16_f16 v[0:15], a[112:115], v[160:163], v[0:15]
	ds_read_b128 v[160:163], v193 offset:0
	v_add_f32_e32 v215, 1.0, v215
	v_rcp_f32_e32 v200, v200
	v_mfma_f32_32x32x16_f16 v[16:31], a[112:115], v[164:167], v[16:31]
	ds_read_b128 v[164:167], v193 offset:1024
	v_rcp_f32_e32 v201, v201
	v_mfma_f32_32x32x16_f16 v[0:15], a[116:119], v[168:171], v[0:15]
	ds_read_b128 v[168:171], v193 offset:2048
	v_rcp_f32_e32 v202, v202
	v_mfma_f32_32x32x16_f16 v[16:31], a[116:119], v[172:175], v[16:31]
	ds_read_b128 v[172:175], v193 offset:3072
	global_load_lds_dwordx4 v192, s[44:45] offset:3072 sc1
	v_rcp_f32_e32 v203, v203
	s_waitcnt lgkmcnt(2)
	v_mfma_f32_32x32x16_f16 v[0:15], a[120:123], v[176:179], v[0:15]
	ds_read_b128 v[176:179], v193 offset:4096
	v_rcp_f32_e32 v204, v204
	s_add_u32 s46, s42, 0x4000
	s_addc_u32 s47, s43, 0
	global_load_dwordx4 v[64:67], v192, s[46:47] offset:0
	v_mfma_f32_32x32x16_f16 v[16:31], a[120:123], v[180:183], v[16:31]
	ds_read_b128 v[180:183], v193 offset:5120
	v_rcp_f32_e32 v205, v205
	v_mul_f32_e32 v204, v204, v156
	global_load_dwordx4 v[68:71], v192, s[46:47] offset:1024
	global_load_dwordx4 v[72:75], v192, s[46:47] offset:2048
	v_mfma_f32_32x32x16_f16 v[0:15], a[124:127], v[184:187], v[0:15]
	ds_read_b128 v[184:187], v193 offset:6144
	v_rcp_f32_e32 v206, v206
	v_mul_f32_e32 v205, v205, v157
	global_load_dwordx4 v[76:79], v192, s[46:47] offset:3072
	s_add_u32 s46, s42, 0x5000
	s_addc_u32 s47, s43, 0
	v_mfma_f32_32x32x16_f16 v[16:31], a[124:127], v[188:191], v[16:31]
	ds_read_b128 v[188:191], v193 offset:7168
	v_cmp_gt_u32_e32 vcc, 2, v251
	s_cbranch_vccnz .LD_tpoll17
.LD_tok16:
	s_and_b32 s64, s71, 1
	s_lshl_b32 s64, s64, 22
	s_add_u32 s64, s64, s49
	s_add_u32 s64, s64, 0x20000
	s_add_u32 s34, s6, s64
	s_addc_u32 s35, s7, 0
	s_mov_b32 m0, s52
	s_add_u32 s44, s34, 0x0
	s_addc_u32 s45, s35, 0
	global_load_lds_dwordx4 v192, s[44:45] sc1
	v_rcp_f32_e32 v207, v207
	v_mul_f32_e32 v206, v206, v158
	global_load_dwordx4 v[80:83], v192, s[46:47] offset:0
	global_load_dwordx4 v[84:87], v192, s[46:47] offset:1024
	v_mfma_f32_32x32x16_f16 v[0:15], a[128:131], v[160:163], v[0:15]
	ds_read_b128 v[160:163], v193 offset:8192
	v_rcp_f32_e32 v208, v208
	v_mul_f32_e32 v207, v207, v159
	global_load_dwordx4 v[88:91], v192, s[46:47] offset:2048
	global_load_dwordx4 v[92:95], v192, s[46:47] offset:3072
	v_mfma_f32_32x32x16_f16 v[16:31], a[128:131], v[164:167], v[16:31]
	ds_read_b128 v[164:167], v193 offset:9216
	v_rcp_f32_e32 v209, v209
	v_fmamk_f32 v208, v208, 0xc0b8aa3b, v198
	s_waitcnt lgkmcnt(2)
	v_mfma_f32_32x32x16_f16 v[0:15], a[132:135], v[168:171], v[0:15]
	ds_read_b128 v[168:171], v193 offset:10240
	v_rcp_f32_e32 v210, v210
	v_fmamk_f32 v209, v209, 0xc0b8aa3b, v198
	v_fma_f32 v156, v200, v208, v204
	v_mfma_f32_32x32x16_f16 v[16:31], a[132:135], v[172:175], v[16:31]
	ds_read_b128 v[172:175], v193 offset:11264
	global_load_lds_dwordx4 v192, s[44:45] offset:1024 sc1
	v_rcp_f32_e32 v211, v211
	v_fmamk_f32 v210, v210, 0xc0b8aa3b, v198
	v_fma_f32 v157, v201, v209, v205
	v_mfma_f32_32x32x16_f16 v[0:15], a[136:139], v[176:179], v[0:15]
	ds_read_b128 v[176:179], v193 offset:12288
	v_rcp_f32_e32 v212, v212
	v_fmamk_f32 v211, v211, 0xc0b8aa3b, v198
	v_fma_f32 v158, v202, v210, v206
	v_mfma_f32_32x32x16_f16 v[16:31], a[136:139], v[180:183], v[16:31]
	ds_read_b128 v[180:183], v193 offset:13312
	v_rcp_f32_e32 v213, v213
	v_fma_f32 v159, v203, v211, v207
	v_mfma_f32_32x32x16_f16 v[0:15], a[140:143], v[184:187], v[0:15]
	ds_read_b128 v[184:187], v193 offset:14336
	v_rcp_f32_e32 v214, v214
	v_mfma_f32_32x32x16_f16 v[16:31], a[140:143], v[188:191], v[16:31]
	ds_read_b128 v[188:191], v193 offset:15360
	global_load_lds_dwordx4 v192, s[44:45] offset:2048 sc1
	v_rcp_f32_e32 v215, v215
	s_waitcnt lgkmcnt(2)
	v_mfma_f32_32x32x16_f16 v[0:15], a[144:147], v[160:163], v[0:15]
	ds_read_b128 v[160:163], v193 offset:16384
	v_exp_f32_e32 v200, v156
	v_mfma_f32_32x32x16_f16 v[16:31], a[144:147], v[164:167], v[16:31]
	ds_read_b128 v[164:167], v193 offset:17408
	v_exp_f32_e32 v201, v157
	v_add_f32_e32 v200, 1.0, v200
	v_mfma_f32_32x32x16_f16 v[0:15], a[148:151], v[168:171], v[0:15]
	ds_read_b128 v[168:171], v193 offset:18432
	v_exp_f32_e32 v202, v158
	v_add_f32_e32 v201, 1.0, v201
	v_mfma_f32_32x32x16_f16 v[16:31], a[148:151], v[172:175], v[16:31]
	ds_read_b128 v[172:175], v193 offset:19456
	global_load_lds_dwordx4 v192, s[44:45] offset:3072 sc1
	v_exp_f32_e32 v203, v159
	v_add_f32_e32 v202, 1.0, v202
	v_mfma_f32_32x32x16_f16 v[0:15], a[152:155], v[176:179], v[0:15]
	ds_read_b128 v[176:179], v193 offset:20480
	v_add_f32_e32 v203, 1.0, v203
	v_rcp_f32_e32 v200, v200
	v_mfma_f32_32x32x16_f16 v[16:31], a[152:155], v[180:183], v[16:31]
	ds_read_b128 v[180:183], v193 offset:21504
	v_rcp_f32_e32 v201, v201
	v_fma_f32 v200, v200, 2.0, -1.0
	s_waitcnt lgkmcnt(2)
	v_mfma_f32_32x32x16_f16 v[0:15], a[156:159], v[184:187], v[0:15]
	ds_read_b128 v[184:187], v193 offset:22528
	v_rcp_f32_e32 v202, v202
	v_fma_f32 v201, v201, 2.0, -1.0
	v_mul_f32_e32 v216, v212, v200
	v_mfma_f32_32x32x16_f16 v[16:31], a[156:159], v[188:191], v[16:31]
	ds_read_b128 v[188:191], v193 offset:23552
	s_mov_b32 m0, s53
	s_add_u32 s44, s34, 0x1000
	s_addc_u32 s45, s35, 0
	global_load_lds_dwordx4 v192, s[44:45] sc1
	v_rcp_f32_e32 v203, v203
	v_fma_f32 v202, v202, 2.0, -1.0
	v_mul_f32_e32 v217, v213, v201
	v_mfma_f32_32x32x16_f16 v[0:15], a[160:163], v[160:163], v[0:15]
	ds_read_b128 v[160:163], v193 offset:24576
	v_fma_f32 v203, v203, 2.0, -1.0
	v_mul_f32_e32 v218, v214, v202
	v_mfma_f32_32x32x16_f16 v[16:31], a[160:163], v[164:167], v[16:31]
	ds_read_b128 v[164:167], v193 offset:25600
	v_mul_f32_e32 v219, v215, v203
	v_mul_f32_e32 v236, v216, v228
	v_mfma_f32_32x32x16_f16 v[0:15], a[164:167], v[168:171], v[0:15]
	ds_read_b128 v[168:171], v193 offset:26624
	v_mul_f32_e32 v237, v216, v232
	v_fmac_f32_e32 v236, v217, v229
	v_mfma_f32_32x32x16_f16 v[16:31], a[164:167], v[172:175], v[16:31]
	ds_read_b128 v[172:175], v193 offset:27648
	global_load_lds_dwordx4 v192, s[44:45] offset:1024 sc1
	v_fmac_f32_e32 v237, v217, v233
	v_fmac_f32_e32 v236, v218, v230
	s_waitcnt lgkmcnt(2)
	v_mfma_f32_32x32x16_f16 v[0:15], a[168:171], v[176:179], v[0:15]
	ds_read_b128 v[176:179], v193 offset:28672
	v_fmac_f32_e32 v237, v218, v234
	v_fmac_f32_e32 v236, v219, v231
	v_mfma_f32_32x32x16_f16 v[16:31], a[168:171], v[180:183], v[16:31]
	ds_read_b128 v[180:183], v193 offset:29696
	v_fmac_f32_e32 v237, v219, v235
	v_mov_b32_e32 v238, v236
	v_mfma_f32_32x32x16_f16 v[0:15], a[172:175], v[184:187], v[0:15]
	ds_read_b128 v[184:187], v193 offset:30720
	v_mov_b32_e32 v240, v237
	v_cvt_pk_f16_f32 v222, v216, v217
	v_mfma_f32_32x32x16_f16 v[16:31], a[172:175], v[188:191], v[16:31]
	ds_read_b128 v[188:191], v193 offset:31744
	global_load_lds_dwordx4 v192, s[44:45] offset:2048 sc1
	v_permlane32_swap_b32_e32 v236, v238
	v_permlane32_swap_b32_e32 v237, v240
	v_add_f32_e32 v238, v236, v238
	v_add_f32_e32 v239, v237, v240
	ds_write_b64 v248, v[238:239] offset:1792
	s_waitcnt vmcnt(15)
	s_barrier
	v_mfma_f32_32x32x16_f16 v[0:15], a[176:179], v[160:163], v[0:15]
	ds_read_b128 v[160:163], v193 offset:32768
	v_cvt_pk_f16_f32 v223, v218, v219
	v_mfma_f32_32x32x16_f16 v[16:31], a[176:179], v[164:167], v[16:31]
	ds_read_b128 v[164:167], v193 offset:33792
	v_permlane32_swap_b32_e32 v220, v222
	v_permlane32_swap_b32_e32 v221, v223
	s_cmp_eq_u32 s31, 0
	s_cbranch_scc1 .LD_slow18
	global_store_dwordx4 v195, v[220:223], s[36:37] offset:0
.LD_join19:
	s_waitcnt lgkmcnt(3)
	v_mfma_f32_32x32x16_f16 v[0:15], a[180:183], v[168:171], v[0:15]
	ds_read_b128 v[168:171], v193 offset:34816
	v_mfma_f32_32x32x16_f16 v[16:31], a[180:183], v[172:175], v[16:31]
	ds_read_b128 v[172:175], v193 offset:35840
	global_load_lds_dwordx4 v192, s[44:45] offset:3072 sc1
	v_mfma_f32_32x32x16_f16 v[0:15], a[184:187], v[176:179], v[0:15]
	ds_read_b128 v[176:179], v193 offset:36864
	v_mfma_f32_32x32x16_f16 v[16:31], a[184:187], v[180:183], v[16:31]
	ds_read_b128 v[180:183], v193 offset:37888
	v_mfma_f32_32x32x16_f16 v[0:15], a[188:191], v[184:187], v[0:15]
	ds_read_b128 v[184:187], v193 offset:38912
	v_mfma_f32_32x32x16_f16 v[16:31], a[188:191], v[188:191], v[16:31]
	ds_read_b128 v[188:191], v193 offset:39936
	s_mov_b32 m0, s54
	s_add_u32 s44, s34, 0x8000
	s_addc_u32 s45, s35, 0
	global_load_lds_dwordx4 v192, s[44:45] sc1
	s_waitcnt lgkmcnt(2)
	v_mfma_f32_32x32x16_f16 v[0:15], a[192:195], v[160:163], v[0:15]
	ds_read_b128 v[160:163], v193 offset:40960
	v_mfma_f32_32x32x16_f16 v[16:31], a[192:195], v[164:167], v[16:31]
	ds_read_b128 v[164:167], v193 offset:41984
	v_mfma_f32_32x32x16_f16 v[0:15], a[196:199], v[168:171], v[0:15]
	ds_read_b128 v[168:171], v193 offset:43008
	v_mfma_f32_32x32x16_f16 v[16:31], a[196:199], v[172:175], v[16:31]
	ds_read_b128 v[172:175], v193 offset:44032
	global_load_lds_dwordx4 v192, s[44:45] offset:1024 sc1
	v_mfma_f32_32x32x16_f16 v[0:15], a[200:203], v[176:179], v[0:15]
	ds_read_b128 v[176:179], v193 offset:45056
	v_mfma_f32_32x32x16_f16 v[16:31], a[200:203], v[180:183], v[16:31]
	ds_read_b128 v[180:183], v193 offset:46080
	s_waitcnt lgkmcnt(2)
	v_mfma_f32_32x32x16_f16 v[0:15], a[204:207], v[184:187], v[0:15]
	ds_read_b128 v[184:187], v193 offset:47104
	s_waitcnt vmcnt(3)
	s_barrier
	v_mov_b32_e32 v199, 4
	s_cmp_eq_u32 s31, 0
	s_cbranch_scc1 .LD_slow20
	global_store_dword v197, v199, s[40:41]
.LD_join21:
	ds_read_b64 v[200:201], v249 offset:1536
	ds_read_b64 v[202:203], v249 offset:3584
	ds_read_b64 v[204:205], v249 offset:5632
	ds_read_b64 v[206:207], v249 offset:7680
	v_mfma_f32_32x32x16_f16 v[16:31], a[204:207], v[188:191], v[16:31]
	ds_read_b128 v[188:191], v193 offset:48128
	global_load_lds_dwordx4 v192, s[44:45] offset:2048 sc1
	v_mfma_f32_32x32x16_f16 v[0:15], a[208:211], v[160:163], v[0:15]
	ds_read_b128 v[160:163], v193 offset:49152
	v_mfma_f32_32x32x16_f16 v[16:31], a[208:211], v[164:167], v[16:31]
	ds_read_b128 v[164:167], v193 offset:50176
	v_mfma_f32_32x32x16_f16 v[0:15], a[212:215], v[168:171], v[0:15]
	ds_read_b128 v[168:171], v193 offset:51200
	v_mfma_f32_32x32x16_f16 v[16:31], a[212:215], v[172:175], v[16:31]
	ds_read_b128 v[172:175], v193 offset:52224
	global_load_lds_dwordx4 v192, s[44:45] offset:3072 sc1
	s_waitcnt lgkmcnt(2)
	v_mfma_f32_32x32x16_f16 v[0:15], a[216:219], v[176:179], v[0:15]
	ds_read_b128 v[176:179], v193 offset:53248
	v_mfma_f32_32x32x16_f16 v[16:31], a[216:219], v[180:183], v[16:31]
	ds_read_b128 v[180:183], v193 offset:54272
	v_mfma_f32_32x32x16_f16 v[0:15], a[220:223], v[184:187], v[0:15]
	ds_read_b128 v[184:187], v193 offset:55296
	v_mfma_f32_32x32x16_f16 v[16:31], a[220:223], v[188:191], v[16:31]
	ds_read_b128 v[188:191], v193 offset:56320
	s_mov_b32 m0, s55
	s_add_u32 s44, s34, 0x9000
	s_addc_u32 s45, s35, 0
	global_load_lds_dwordx4 v192, s[44:45] sc1
	v_mfma_f32_32x32x16_f16 v[0:15], a[224:227], v[160:163], v[0:15]
	ds_read_b128 v[160:163], v193 offset:57344
	v_mfma_f32_32x32x16_f16 v[16:31], a[224:227], v[164:167], v[16:31]
	ds_read_b128 v[164:167], v193 offset:58368
	s_waitcnt lgkmcnt(2)
	v_mfma_f32_32x32x16_f16 v[0:15], a[228:231], v[168:171], v[0:15]
	ds_read_b128 v[168:171], v193 offset:59392
	v_add_f32_e32 v200, v200, v202
	v_add_f32_e32 v201, v201, v203
	v_add_f32_e32 v200, v200, v204
	v_add_f32_e32 v201, v201, v205
	v_add_f32_e32 v200, v200, v206
	v_add_f32_e32 v201, v201, v207
	global_store_dwordx2 v250, v[200:201], s[72:73]
	v_mfma_f32_32x32x16_f16 v[16:31], a[228:231], v[172:175], v[16:31]
	ds_read_b128 v[172:175], v193 offset:60416
	global_load_lds_dwordx4 v192, s[44:45] offset:1024 sc1
	v_mfma_f32_32x32x16_f16 v[0:15], a[232:235], v[176:179], v[0:15]
	ds_read_b128 v[176:179], v193 offset:61440
	v_mfma_f32_32x32x16_f16 v[16:31], a[232:235], v[180:183], v[16:31]
	ds_read_b128 v[180:183], v193 offset:62464
	v_mfma_f32_32x32x16_f16 v[0:15], a[236:239], v[184:187], v[0:15]
	ds_read_b128 v[184:187], v193 offset:63488
	s_and_b32 s64, s33, 1
	s_lshl_b32 s64, s64, 22
	s_add_u32 s64, s64, s50
	s_add_u32 s36, s6, s64
	s_addc_u32 s37, s7, 0
	s_lshl_b32 s64, s33, 3
	s_add_u32 s64, s64, s29
	s_lshl_b32 s64, s64, 5
	s_add_u32 s64, s64, s30
	s_lshl_b32 s64, s64, 2
	s_add_u32 s40, s8, s64
	s_addc_u32 s41, s9, 0
	s_lshl_b32 s64, s33, 19
	s_add_u32 s72, s62, s64
	s_addc_u32 s73, s63, 0
	v_mfma_f32_32x32x16_f16 v[16:31], a[236:239], v[188:191], v[16:31]
	ds_read_b128 v[188:191], v193 offset:64512
	global_load_lds_dwordx4 v192, s[44:45] offset:2048 sc1
	s_waitcnt vmcnt(9)
	s_barrier
	s_waitcnt lgkmcnt(2)
	v_mfma_f32_32x32x16_f16 v[0:15], a[240:243], v[160:163], v[0:15]
	ds_read_b128 v[160:163], v192 offset:0
	v_mfma_f32_32x32x16_f16 v[16:31], a[240:243], v[164:167], v[16:31]
	ds_read_b128 v[164:167], v192 offset:1024
	v_mfma_f32_32x32x16_f16 v[0:15], a[244:247], v[168:171], v[0:15]
	ds_read_b128 v[168:171], v192 offset:2048
	v_mfma_f32_32x32x16_f16 v[16:31], a[244:247], v[172:175], v[16:31]
	ds_read_b128 v[172:175], v192 offset:3072
	global_load_lds_dwordx4 v192, s[44:45] offset:3072 sc1
	v_mfma_f32_32x32x16_f16 v[0:15], a[248:251], v[176:179], v[0:15]
	ds_read_b128 v[176:179], v192 offset:4096
	v_mfma_f32_32x32x16_f16 v[16:31], a[248:251], v[180:183], v[16:31]
	ds_read_b128 v[180:183], v192 offset:5120
	s_waitcnt lgkmcnt(2)
	v_mfma_f32_32x32x16_f16 v[0:15], a[252:255], v[184:187], v[0:15]
	ds_read_b128 v[184:187], v192 offset:6144
	v_mfma_f32_32x32x16_f16 v[16:31], a[252:255], v[188:191], v[16:31]
	ds_read_b128 v[188:191], v192 offset:7168
	s_mov_b32 m0, s56
	s_add_u32 s44, s34, 0x10000
	s_addc_u32 s45, s35, 0
	global_load_lds_dwordx4 v192, s[44:45] sc1
	s_nop 3
	s_waitcnt lgkmcnt(2)
	v_mfma_f32_32x32x16_f16 v[32:47], a[0:3], v[160:163], v[32:47]
	ds_read_b128 v[160:163], v192 offset:8192
	v_exp_f32_e32 v200, v0
	v_mfma_f32_32x32x16_f16 v[48:63], a[0:3], v[164:167], v[48:63]
	ds_read_b128 v[164:167], v192 offset:9216
	s_lshl_b32 s64, s71, 3
	s_add_u32 s64, s64, s29
	s_lshl_b32 s64, s64, 7
	s_add_u32 s38, s8, s64
	s_addc_u32 s39, s9, 0
	global_load_dword v251, v196, s[38:39] sc1
	v_exp_f32_e32 v201, v1
	v_add_f32_e32 v200, 1.0, v200
	v_mfma_f32_32x32x16_f16 v[32:47], a[4:7], v[168:171], v[32:47]
	ds_read_b128 v[168:171], v192 offset:10240
	v_exp_f32_e32 v202, v2
	v_add_f32_e32 v201, 1.0, v201
	v_mfma_f32_32x32x16_f16 v[48:63], a[4:7], v[172:175], v[48:63]
	ds_read_b128 v[172:175], v192 offset:11264
	global_load_lds_dwordx4 v192, s[44:45] offset:1024 sc1
	v_exp_f32_e32 v203, v3
	v_add_f32_e32 v202, 1.0, v202
	v_mfma_f32_32x32x16_f16 v[32:47], a[8:11], v[176:179], v[32:47]
	ds_read_b128 v[176:179], v192 offset:12288
	v_exp_f32_e32 v204, v4
	v_add_f32_e32 v203, 1.0, v203
	v_mfma_f32_32x32x16_f16 v[48:63], a[8:11], v[180:183], v[48:63]
	ds_read_b128 v[180:183], v192 offset:13312
	v_exp_f32_e32 v205, v5
	v_add_f32_e32 v204, 1.0, v204
	s_waitcnt lgkmcnt(2)
	v_mfma_f32_32x32x16_f16 v[32:47], a[12:15], v[184:187], v[32:47]
	ds_read_b128 v[184:187], v192 offset:14336
	v_exp_f32_e32 v206, v6
	v_add_f32_e32 v205, 1.0, v205
	v_mfma_f32_32x32x16_f16 v[48:63], a[12:15], v[188:191], v[48:63]
	ds_read_b128 v[188:191], v192 offset:15360
	global_load_lds_dwordx4 v192, s[44:45] offset:2048 sc1
	v_exp_f32_e32 v207, v7
	v_add_f32_e32 v206, 1.0, v206
	v_mfma_f32_32x32x16_f16 v[32:47], a[16:19], v[160:163], v[32:47]
	ds_read_b128 v[160:163], v192 offset:16384
	v_exp_f32_e32 v208, v8
	v_add_f32_e32 v207, 1.0, v207
	v_mfma_f32_32x32x16_f16 v[48:63], a[16:19], v[164:167], v[48:63]
	ds_read_b128 v[164:167], v192 offset:17408
	v_exp_f32_e32 v209, v9
	v_add_f32_e32 v208, 1.0, v208
	v_mfma_f32_32x32x16_f16 v[32:47], a[20:23], v[168:171], v[32:47]
	ds_read_b128 v[168:171], v192 offset:18432
	v_exp_f32_e32 v210, v10
	v_add_f32_e32 v209, 1.0, v209
	v_mfma_f32_32x32x16_f16 v[48:63], a[20:23], v[172:175], v[48:63]
	ds_read_b128 v[172:175], v192 offset:19456
	global_load_lds_dwordx4 v192, s[44:45] offset:3072 sc1
	v_exp_f32_e32 v211, v11
	v_add_f32_e32 v210, 1.0, v210
	s_waitcnt lgkmcnt(2)
	v_mfma_f32_32x32x16_f16 v[32:47], a[24:27], v[176:179], v[32:47]
	ds_read_b128 v[176:179], v192 offset:20480
	v_exp_f32_e32 v212, v12
	v_add_f32_e32 v211, 1.0, v211
	v_mfma_f32_32x32x16_f16 v[48:63], a[24:27], v[180:183], v[48:63]
	ds_read_b128 v[180:183], v192 offset:21504
	v_exp_f32_e32 v213, v13
	v_add_f32_e32 v212, 1.0, v212
	v_mfma_f32_32x32x16_f16 v[32:47], a[28:31], v[184:187], v[32:47]
	ds_read_b128 v[184:187], v192 offset:22528
	v_exp_f32_e32 v214, v14
	v_add_f32_e32 v213, 1.0, v213
	v_mfma_f32_32x32x16_f16 v[48:63], a[28:31], v[188:191], v[48:63]
	ds_read_b128 v[188:191], v192 offset:23552
	s_mov_b32 m0, s57
	s_add_u32 s44, s34, 0x11000
	s_addc_u32 s45, s35, 0
	global_load_lds_dwordx4 v192, s[44:45] sc1
	v_exp_f32_e32 v215, v15
	v_add_f32_e32 v214, 1.0, v214
	v_mfma_f32_32x32x16_f16 v[32:47], a[32:35], v[160:163], v[32:47]
	ds_read_b128 v[160:163], v192 offset:24576
	v_add_f32_e32 v215, 1.0, v215
	v_rcp_f32_e32 v200, v200
	v_mfma_f32_32x32x16_f16 v[48:63], a[32:35], v[164:167], v[48:63]
	ds_read_b128 v[164:167], v192 offset:25600
	v_rcp_f32_e32 v201, v201
	s_waitcnt lgkmcnt(2)
	v_mfma_f32_32x32x16_f16 v[32:47], a[36:39], v[168:171], v[32:47]
	ds_read_b128 v[168:171], v192 offset:26624
	v_rcp_f32_e32 v202, v202
	v_mfma_f32_32x32x16_f16 v[48:63], a[36:39], v[172:175], v[48:63]
	ds_read_b128 v[172:175], v192 offset:27648
	global_load_lds_dwordx4 v192, s[44:45] offset:1024 sc1
	v_rcp_f32_e32 v203, v203
	v_mfma_f32_32x32x16_f16 v[32:47], a[40:43], v[176:179], v[32:47]
	ds_read_b128 v[176:179], v192 offset:28672
	v_rcp_f32_e32 v204, v204
	v_mfma_f32_32x32x16_f16 v[48:63], a[40:43], v[180:183], v[48:63]
	ds_read_b128 v[180:183], v192 offset:29696
	v_rcp_f32_e32 v205, v205
	v_mul_f32_e32 v204, v204, v128
	v_mfma_f32_32x32x16_f16 v[32:47], a[44:47], v[184:187], v[32:47]
	ds_read_b128 v[184:187], v192 offset:30720
	v_rcp_f32_e32 v206, v206
	v_mul_f32_e32 v205, v205, v129
	v_mfma_f32_32x32x16_f16 v[48:63], a[44:47], v[188:191], v[48:63]
	ds_read_b128 v[188:191], v192 offset:31744
	global_load_lds_dwordx4 v192, s[44:45] offset:2048 sc1
	v_rcp_f32_e32 v207, v207
	v_mul_f32_e32 v206, v206, v130
	s_waitcnt vmcnt(8)
	s_barrier
	s_waitcnt lgkmcnt(2)
	v_mfma_f32_32x32x16_f16 v[32:47], a[48:51], v[160:163], v[32:47]
	ds_read_b128 v[160:163], v192 offset:32768
	v_rcp_f32_e32 v208, v208
	v_mul_f32_e32 v207, v207, v131
	v_mfma_f32_32x32x16_f16 v[48:63], a[48:51], v[164:167], v[48:63]
	ds_read_b128 v[164:167], v192 offset:33792
	v_rcp_f32_e32 v209, v209
	v_fmamk_f32 v208, v208, 0xc0b8aa3b, v198
	v_mfma_f32_32x32x16_f16 v[32:47], a[52:55], v[168:171], v[32:47]
	ds_read_b128 v[168:171], v192 offset:34816
	v_rcp_f32_e32 v210, v210
	v_fmamk_f32 v209, v209, 0xc0b8aa3b, v198
	v_fma_f32 v128, v200, v208, v204
	v_mfma_f32_32x32x16_f16 v[48:63], a[52:55], v[172:175], v[48:63]
	ds_read_b128 v[172:175], v192 offset:35840
	global_load_lds_dwordx4 v192, s[44:45] offset:3072 sc1
	v_rcp_f32_e32 v211, v211
	v_fmamk_f32 v210, v210, 0xc0b8aa3b, v198
	v_fma_f32 v129, v201, v209, v205
	v_mfma_f32_32x32x16_f16 v[32:47], a[56:59], v[176:179], v[32:47]
	ds_read_b128 v[176:179], v192 offset:36864
	v_rcp_f32_e32 v212, v212
	v_fmamk_f32 v211, v211, 0xc0b8aa3b, v198
	v_fma_f32 v130, v202, v210, v206
	v_mfma_f32_32x32x16_f16 v[48:63], a[56:59], v[180:183], v[48:63]
	ds_read_b128 v[180:183], v192 offset:37888
	v_rcp_f32_e32 v213, v213
	v_fma_f32 v131, v203, v211, v207
	s_waitcnt lgkmcnt(2)
	v_mfma_f32_32x32x16_f16 v[32:47], a[60:63], v[184:187], v[32:47]
	ds_read_b128 v[184:187], v192 offset:38912
	v_rcp_f32_e32 v214, v214
	v_mfma_f32_32x32x16_f16 v[48:63], a[60:63], v[188:191], v[48:63]
	ds_read_b128 v[188:191], v192 offset:39936
	s_mov_b32 m0, s58
	s_add_u32 s44, s34, 0x18000
	s_addc_u32 s45, s35, 0
	global_load_lds_dwordx4 v192, s[44:45] sc1
	v_rcp_f32_e32 v215, v215
	v_mfma_f32_32x32x16_f16 v[32:47], a[64:67], v[160:163], v[32:47]
	ds_read_b128 v[160:163], v192 offset:40960
	v_exp_f32_e32 v200, v128
	v_mfma_f32_32x32x16_f16 v[48:63], a[64:67], v[164:167], v[48:63]
	ds_read_b128 v[164:167], v192 offset:41984
	v_exp_f32_e32 v201, v129
	v_add_f32_e32 v200, 1.0, v200
	v_mfma_f32_32x32x16_f16 v[32:47], a[68:71], v[168:171], v[32:47]
	ds_read_b128 v[168:171], v192 offset:43008
	v_exp_f32_e32 v202, v130
	v_add_f32_e32 v201, 1.0, v201
	v_mfma_f32_32x32x16_f16 v[48:63], a[68:71], v[172:175], v[48:63]
	ds_read_b128 v[172:175], v192 offset:44032
	global_load_lds_dwordx4 v192, s[44:45] offset:1024 sc1
	v_exp_f32_e32 v203, v131
	v_add_f32_e32 v202, 1.0, v202
	s_waitcnt lgkmcnt(2)
	v_mfma_f32_32x32x16_f16 v[32:47], a[72:75], v[176:179], v[32:47]
	ds_read_b128 v[176:179], v192 offset:45056
	v_add_f32_e32 v203, 1.0, v203
	v_rcp_f32_e32 v200, v200
	v_mfma_f32_32x32x16_f16 v[48:63], a[72:75], v[180:183], v[48:63]
	ds_read_b128 v[180:183], v192 offset:46080
	v_rcp_f32_e32 v201, v201
	v_fma_f32 v200, v200, 2.0, -1.0
	v_mfma_f32_32x32x16_f16 v[32:47], a[76:79], v[184:187], v[32:47]
	ds_read_b128 v[184:187], v192 offset:47104
	v_rcp_f32_e32 v202, v202
	v_fma_f32 v201, v201, 2.0, -1.0
	v_mul_f32_e32 v216, v212, v200
	v_mfma_f32_32x32x16_f16 v[48:63], a[76:79], v[188:191], v[48:63]
	ds_read_b128 v[188:191], v192 offset:48128
	global_load_lds_dwordx4 v192, s[44:45] offset:2048 sc1
	v_rcp_f32_e32 v203, v203
	v_fma_f32 v202, v202, 2.0, -1.0
	v_mul_f32_e32 v217, v213, v201
	v_mfma_f32_32x32x16_f16 v[32:47], a[80:83], v[160:163], v[32:47]
	ds_read_b128 v[160:163], v192 offset:49152
	v_fma_f32 v203, v203, 2.0, -1.0
	v_mul_f32_e32 v218, v214, v202
	v_exp_f32_e32 v200, v16
	v_mfma_f32_32x32x16_f16 v[48:63], a[80:83], v[164:167], v[48:63]
	ds_read_b128 v[164:167], v192 offset:50176
	v_mul_f32_e32 v219, v215, v203
	v_mul_f32_e32 v236, v216, v228
	v_exp_f32_e32 v201, v17
	s_waitcnt lgkmcnt(2)
	v_mfma_f32_32x32x16_f16 v[32:47], a[84:87], v[168:171], v[32:47]
	ds_read_b128 v[168:171], v192 offset:51200
	v_mul_f32_e32 v237, v216, v232
	v_fmac_f32_e32 v236, v217, v229
	v_exp_f32_e32 v202, v18
	v_mfma_f32_32x32x16_f16 v[48:63], a[84:87], v[172:175], v[48:63]
	ds_read_b128 v[172:175], v192 offset:52224
	global_load_lds_dwordx4 v192, s[44:45] offset:3072 sc1
	v_fmac_f32_e32 v237, v217, v233
	v_fmac_f32_e32 v236, v218, v230
	v_exp_f32_e32 v203, v19
	v_mfma_f32_32x32x16_f16 v[32:47], a[88:91], v[176:179], v[32:47]
	ds_read_b128 v[176:179], v192 offset:53248
	v_fmac_f32_e32 v237, v218, v234
	v_fmac_f32_e32 v236, v219, v231
	v_exp_f32_e32 v204, v20
	v_mfma_f32_32x32x16_f16 v[48:63], a[88:91], v[180:183], v[48:63]
	ds_read_b128 v[180:183], v192 offset:54272
	v_fmac_f32_e32 v237, v219, v235
	v_mov_b32_e32 v238, v236
	v_exp_f32_e32 v205, v21
	v_mfma_f32_32x32x16_f16 v[32:47], a[92:95], v[184:187], v[32:47]
	ds_read_b128 v[184:187], v192 offset:55296
	v_mov_b32_e32 v240, v237
	v_cvt_pk_f16_f32 v220, v216, v217
	v_exp_f32_e32 v206, v22
	v_mfma_f32_32x32x16_f16 v[48:63], a[92:95], v[188:191], v[48:63]
	ds_read_b128 v[188:191], v192 offset:56320
	s_mov_b32 m0, s59
	s_add_u32 s44, s34, 0x19000
	s_addc_u32 s45, s35, 0
	global_load_lds_dwordx4 v192, s[44:45] sc1
	v_permlane32_swap_b32_e32 v236, v238
	v_permlane32_swap_b32_e32 v237, v240
	v_add_f32_e32 v238, v236, v238
	v_add_f32_e32 v239, v237, v240
	ds_write_b64 v248, v[238:239] offset:0
	v_exp_f32_e32 v207, v23
	s_waitcnt lgkmcnt(3)
	v_mfma_f32_32x32x16_f16 v[32:47], a[96:99], v[160:163], v[32:47]
	ds_read_b128 v[160:163], v192 offset:57344
	v_cvt_pk_f16_f32 v221, v218, v219
	v_exp_f32_e32 v208, v24
	v_add_f32_e32 v200, 1.0, v200
	v_mfma_f32_32x32x16_f16 v[48:63], a[96:99], v[164:167], v[48:63]
	ds_read_b128 v[164:167], v192 offset:58368
	v_exp_f32_e32 v209, v25
	v_add_f32_e32 v201, 1.0, v201
	v_add_f32_e32 v202, 1.0, v202
	v_mfma_f32_32x32x16_f16 v[32:47], a[100:103], v[168:171], v[32:47]
	ds_read_b128 v[168:171], v192 offset:59392
	v_exp_f32_e32 v210, v26
	v_add_f32_e32 v203, 1.0, v203
	v_add_f32_e32 v204, 1.0, v204
	v_mfma_f32_32x32x16_f16 v[48:63], a[100:103], v[172:175], v[48:63]
	ds_read_b128 v[172:175], v192 offset:60416
	global_load_lds_dwordx4 v192, s[44:45] offset:1024 sc1
	v_exp_f32_e32 v211, v27
	v_add_f32_e32 v205, 1.0, v205
	v_add_f32_e32 v206, 1.0, v206
	v_mfma_f32_32x32x16_f16 v[32:47], a[104:107], v[176:179], v[32:47]
	ds_read_b128 v[176:179], v192 offset:61440
	v_exp_f32_e32 v212, v28
	v_add_f32_e32 v207, 1.0, v207
	v_add_f32_e32 v208, 1.0, v208
	v_mfma_f32_32x32x16_f16 v[48:63], a[104:107], v[180:183], v[48:63]
	ds_read_b128 v[180:183], v192 offset:62464
	v_exp_f32_e32 v213, v29
	v_add_f32_e32 v209, 1.0, v209
	v_add_f32_e32 v210, 1.0, v210
	s_waitcnt lgkmcnt(2)
	v_mfma_f32_32x32x16_f16 v[32:47], a[108:111], v[184:187], v[32:47]
	ds_read_b128 v[184:187], v192 offset:63488
	v_exp_f32_e32 v214, v30
	v_add_f32_e32 v211, 1.0, v211
	v_add_f32_e32 v212, 1.0, v212
	v_mfma_f32_32x32x16_f16 v[48:63], a[108:111], v[188:191], v[48:63]
	ds_read_b128 v[188:191], v192 offset:64512
	global_load_lds_dwordx4 v192, s[44:45] offset:2048 sc1
	v_exp_f32_e32 v215, v31
	v_add_f32_e32 v213, 1.0, v213
	v_add_f32_e32 v214, 1.0, v214
	s_waitcnt vmcnt(7)
	s_barrier
	v_mfma_f32_32x32x16_f16 v[32:47], a[112:115], v[160:163], v[32:47]
	ds_read_b128 v[160:163], v193 offset:0
	v_add_f32_e32 v215, 1.0, v215
	v_rcp_f32_e32 v200, v200
	v_mfma_f32_32x32x16_f16 v[48:63], a[112:115], v[164:167], v[48:63]
	ds_read_b128 v[164:167], v193 offset:1024
	v_rcp_f32_e32 v201, v201
	v_mfma_f32_32x32x16_f16 v[32:47], a[116:119], v[168:171], v[32:47]
	ds_read_b128 v[168:171], v193 offset:2048
	v_rcp_f32_e32 v202, v202
	v_mfma_f32_32x32x16_f16 v[48:63], a[116:119], v[172:175], v[48:63]
	ds_read_b128 v[172:175], v193 offset:3072
	global_load_lds_dwordx4 v192, s[44:45] offset:3072 sc1
	v_rcp_f32_e32 v203, v203
	s_waitcnt lgkmcnt(2)
	v_mfma_f32_32x32x16_f16 v[32:47], a[120:123], v[176:179], v[32:47]
	ds_read_b128 v[176:179], v193 offset:4096
	v_rcp_f32_e32 v204, v204
	s_add_u32 s46, s42, 0x6000
	s_addc_u32 s47, s43, 0
	global_load_dwordx4 v[96:99], v192, s[46:47] offset:0
	v_mfma_f32_32x32x16_f16 v[48:63], a[120:123], v[180:183], v[48:63]
	ds_read_b128 v[180:183], v193 offset:5120
	v_rcp_f32_e32 v205, v205
	v_mul_f32_e32 v204, v204, v132
	global_load_dwordx4 v[100:103], v192, s[46:47] offset:1024
	global_load_dwordx4 v[104:107], v192, s[46:47] offset:2048
	v_mfma_f32_32x32x16_f16 v[32:47], a[124:127], v[184:187], v[32:47]
	ds_read_b128 v[184:187], v193 offset:6144
	v_rcp_f32_e32 v206, v206
	v_mul_f32_e32 v205, v205, v133
	global_load_dwordx4 v[108:111], v192, s[46:47] offset:3072
	s_add_u32 s46, s42, 0x7000
	s_addc_u32 s47, s43, 0
	v_mfma_f32_32x32x16_f16 v[48:63], a[124:127], v[188:191], v[48:63]
	ds_read_b128 v[188:191], v193 offset:7168
	v_cmp_gt_u32_e32 vcc, 3, v251
	s_cbranch_vccnz .LD_tpoll23
.LD_tok22:
	s_and_b32 s64, s71, 1
	s_lshl_b32 s64, s64, 22
	s_add_u32 s64, s64, s49
	s_add_u32 s64, s64, 0x40000
	s_add_u32 s34, s6, s64
	s_addc_u32 s35, s7, 0
	s_mov_b32 m0, s52
	s_add_u32 s44, s34, 0x0
	s_addc_u32 s45, s35, 0
	global_load_lds_dwordx4 v192, s[44:45] sc1
	v_rcp_f32_e32 v207, v207
	v_mul_f32_e32 v206, v206, v134
	global_load_dwordx4 v[112:115], v192, s[46:47] offset:0
	global_load_dwordx4 v[116:119], v192, s[46:47] offset:1024
	v_mfma_f32_32x32x16_f16 v[32:47], a[128:131], v[160:163], v[32:47]
	ds_read_b128 v[160:163], v193 offset:8192
	v_rcp_f32_e32 v208, v208
	v_mul_f32_e32 v207, v207, v135
	global_load_dwordx4 v[120:123], v192, s[46:47] offset:2048
	global_load_dwordx4 v[124:127], v192, s[46:47] offset:3072
	v_mfma_f32_32x32x16_f16 v[48:63], a[128:131], v[164:167], v[48:63]
	ds_read_b128 v[164:167], v193 offset:9216
	v_rcp_f32_e32 v209, v209
	v_fmamk_f32 v208, v208, 0xc0b8aa3b, v198
	s_waitcnt lgkmcnt(2)
	v_mfma_f32_32x32x16_f16 v[32:47], a[132:135], v[168:171], v[32:47]
	ds_read_b128 v[168:171], v193 offset:10240
	v_rcp_f32_e32 v210, v210
	v_fmamk_f32 v209, v209, 0xc0b8aa3b, v198
	v_fma_f32 v132, v200, v208, v204
	v_mfma_f32_32x32x16_f16 v[48:63], a[132:135], v[172:175], v[48:63]
	ds_read_b128 v[172:175], v193 offset:11264
	global_load_lds_dwordx4 v192, s[44:45] offset:1024 sc1
	v_rcp_f32_e32 v211, v211
	v_fmamk_f32 v210, v210, 0xc0b8aa3b, v198
	v_fma_f32 v133, v201, v209, v205
	v_mfma_f32_32x32x16_f16 v[32:47], a[136:139], v[176:179], v[32:47]
	ds_read_b128 v[176:179], v193 offset:12288
	v_rcp_f32_e32 v212, v212
	v_fmamk_f32 v211, v211, 0xc0b8aa3b, v198
	v_fma_f32 v134, v202, v210, v206
	v_mfma_f32_32x32x16_f16 v[48:63], a[136:139], v[180:183], v[48:63]
	ds_read_b128 v[180:183], v193 offset:13312
	v_rcp_f32_e32 v213, v213
	v_fma_f32 v135, v203, v211, v207
	v_mfma_f32_32x32x16_f16 v[32:47], a[140:143], v[184:187], v[32:47]
	ds_read_b128 v[184:187], v193 offset:14336
	v_rcp_f32_e32 v214, v214
	v_mfma_f32_32x32x16_f16 v[48:63], a[140:143], v[188:191], v[48:63]
	ds_read_b128 v[188:191], v193 offset:15360
	global_load_lds_dwordx4 v192, s[44:45] offset:2048 sc1
	v_rcp_f32_e32 v215, v215
	s_waitcnt lgkmcnt(2)
	v_mfma_f32_32x32x16_f16 v[32:47], a[144:147], v[160:163], v[32:47]
	ds_read_b128 v[160:163], v193 offset:16384
	v_exp_f32_e32 v200, v132
	v_mfma_f32_32x32x16_f16 v[48:63], a[144:147], v[164:167], v[48:63]
	ds_read_b128 v[164:167], v193 offset:17408
	v_exp_f32_e32 v201, v133
	v_add_f32_e32 v200, 1.0, v200
	v_mfma_f32_32x32x16_f16 v[32:47], a[148:151], v[168:171], v[32:47]
	ds_read_b128 v[168:171], v193 offset:18432
	v_exp_f32_e32 v202, v134
	v_add_f32_e32 v201, 1.0, v201
	v_mfma_f32_32x32x16_f16 v[48:63], a[148:151], v[172:175], v[48:63]
	ds_read_b128 v[172:175], v193 offset:19456
	global_load_lds_dwordx4 v192, s[44:45] offset:3072 sc1
	v_exp_f32_e32 v203, v135
	v_add_f32_e32 v202, 1.0, v202
	v_mfma_f32_32x32x16_f16 v[32:47], a[152:155], v[176:179], v[32:47]
	ds_read_b128 v[176:179], v193 offset:20480
	v_add_f32_e32 v203, 1.0, v203
	v_rcp_f32_e32 v200, v200
	v_mfma_f32_32x32x16_f16 v[48:63], a[152:155], v[180:183], v[48:63]
	ds_read_b128 v[180:183], v193 offset:21504
	v_rcp_f32_e32 v201, v201
	v_fma_f32 v200, v200, 2.0, -1.0
	s_waitcnt lgkmcnt(2)
	v_mfma_f32_32x32x16_f16 v[32:47], a[156:159], v[184:187], v[32:47]
	ds_read_b128 v[184:187], v193 offset:22528
	v_rcp_f32_e32 v202, v202
	v_fma_f32 v201, v201, 2.0, -1.0
	v_mul_f32_e32 v216, v212, v200
	v_mfma_f32_32x32x16_f16 v[48:63], a[156:159], v[188:191], v[48:63]
	ds_read_b128 v[188:191], v193 offset:23552
	s_mov_b32 m0, s53
	s_add_u32 s44, s34, 0x1000
	s_addc_u32 s45, s35, 0
	global_load_lds_dwordx4 v192, s[44:45] sc1
	v_rcp_f32_e32 v203, v203
	v_fma_f32 v202, v202, 2.0, -1.0
	v_mul_f32_e32 v217, v213, v201
	v_mfma_f32_32x32x16_f16 v[32:47], a[160:163], v[160:163], v[32:47]
	ds_read_b128 v[160:163], v193 offset:24576
	v_fma_f32 v203, v203, 2.0, -1.0
	v_mul_f32_e32 v218, v214, v202
	v_mfma_f32_32x32x16_f16 v[48:63], a[160:163], v[164:167], v[48:63]
	ds_read_b128 v[164:167], v193 offset:25600
	v_mul_f32_e32 v219, v215, v203
	v_mul_f32_e32 v236, v216, v228
	v_mfma_f32_32x32x16_f16 v[32:47], a[164:167], v[168:171], v[32:47]
	ds_read_b128 v[168:171], v193 offset:26624
	v_mul_f32_e32 v237, v216, v232
	v_fmac_f32_e32 v236, v217, v229
	v_mfma_f32_32x32x16_f16 v[48:63], a[164:167], v[172:175], v[48:63]
	ds_read_b128 v[172:175], v193 offset:27648
	global_load_lds_dwordx4 v192, s[44:45] offset:1024 sc1
	v_fmac_f32_e32 v237, v217, v233
	v_fmac_f32_e32 v236, v218, v230
	s_waitcnt lgkmcnt(2)
	v_mfma_f32_32x32x16_f16 v[32:47], a[168:171], v[176:179], v[32:47]
	ds_read_b128 v[176:179], v193 offset:28672
	v_fmac_f32_e32 v237, v218, v234
	v_fmac_f32_e32 v236, v219, v231
	v_mfma_f32_32x32x16_f16 v[48:63], a[168:171], v[180:183], v[48:63]
	ds_read_b128 v[180:183], v193 offset:29696
	v_fmac_f32_e32 v237, v219, v235
	v_mov_b32_e32 v238, v236
	v_mfma_f32_32x32x16_f16 v[32:47], a[172:175], v[184:187], v[32:47]
	ds_read_b128 v[184:187], v193 offset:30720
	v_mov_b32_e32 v240, v237
	v_cvt_pk_f16_f32 v222, v216, v217
	v_mfma_f32_32x32x16_f16 v[48:63], a[172:175], v[188:191], v[48:63]
	ds_read_b128 v[188:191], v193 offset:31744
	global_load_lds_dwordx4 v192, s[44:45] offset:2048 sc1
	v_permlane32_swap_b32_e32 v236, v238
	v_permlane32_swap_b32_e32 v237, v240
	v_add_f32_e32 v238, v236, v238
	v_add_f32_e32 v239, v237, v240
	ds_write_b64 v248, v[238:239] offset:256
	s_waitcnt vmcnt(15)
	s_barrier
	v_mfma_f32_32x32x16_f16 v[32:47], a[176:179], v[160:163], v[32:47]
	ds_read_b128 v[160:163], v193 offset:32768
	v_cvt_pk_f16_f32 v223, v218, v219
	v_mfma_f32_32x32x16_f16 v[48:63], a[176:179], v[164:167], v[48:63]
	ds_read_b128 v[164:167], v193 offset:33792
	v_permlane32_swap_b32_e32 v220, v222
	v_permlane32_swap_b32_e32 v221, v223
	s_cmp_eq_u32 s31, 0
	s_cbranch_scc1 .LD_slow24
	global_store_dwordx4 v195, v[220:223], s[36:37] offset:0
.LD_join25:
	s_waitcnt lgkmcnt(3)
	v_mfma_f32_32x32x16_f16 v[32:47], a[180:183], v[168:171], v[32:47]
	ds_read_b128 v[168:171], v193 offset:34816
	v_mfma_f32_32x32x16_f16 v[48:63], a[180:183], v[172:175], v[48:63]
	ds_read_b128 v[172:175], v193 offset:35840
	global_load_lds_dwordx4 v192, s[44:45] offset:3072 sc1
	v_mfma_f32_32x32x16_f16 v[32:47], a[184:187], v[176:179], v[32:47]
	ds_read_b128 v[176:179], v193 offset:36864
	v_mfma_f32_32x32x16_f16 v[48:63], a[184:187], v[180:183], v[48:63]
	ds_read_b128 v[180:183], v193 offset:37888
	v_mfma_f32_32x32x16_f16 v[32:47], a[188:191], v[184:187], v[32:47]
	ds_read_b128 v[184:187], v193 offset:38912
	v_mfma_f32_32x32x16_f16 v[48:63], a[188:191], v[188:191], v[48:63]
	ds_read_b128 v[188:191], v193 offset:39936
	s_mov_b32 m0, s54
	s_add_u32 s44, s34, 0x8000
	s_addc_u32 s45, s35, 0
	global_load_lds_dwordx4 v192, s[44:45] sc1
	s_waitcnt lgkmcnt(2)
	v_mfma_f32_32x32x16_f16 v[32:47], a[192:195], v[160:163], v[32:47]
	ds_read_b128 v[160:163], v193 offset:40960
	v_mfma_f32_32x32x16_f16 v[48:63], a[192:195], v[164:167], v[48:63]
	ds_read_b128 v[164:167], v193 offset:41984
	v_mfma_f32_32x32x16_f16 v[32:47], a[196:199], v[168:171], v[32:47]
	ds_read_b128 v[168:171], v193 offset:43008
	v_mfma_f32_32x32x16_f16 v[48:63], a[196:199], v[172:175], v[48:63]
	ds_read_b128 v[172:175], v193 offset:44032
	global_load_lds_dwordx4 v192, s[44:45] offset:1024 sc1
	v_mfma_f32_32x32x16_f16 v[32:47], a[200:203], v[176:179], v[32:47]
	ds_read_b128 v[176:179], v193 offset:45056
	v_mfma_f32_32x32x16_f16 v[48:63], a[200:203], v[180:183], v[48:63]
	ds_read_b128 v[180:183], v193 offset:46080
	s_waitcnt lgkmcnt(2)
	v_mfma_f32_32x32x16_f16 v[32:47], a[204:207], v[184:187], v[32:47]
	ds_read_b128 v[184:187], v193 offset:47104
	s_waitcnt vmcnt(3)
	s_barrier
	v_mov_b32_e32 v199, 1
	s_cmp_eq_u32 s31, 0
	s_cbranch_scc1 .LD_slow26
	global_store_dword v197, v199, s[40:41]
.LD_join27:
	ds_read_b64 v[200:201], v249 offset:0
	ds_read_b64 v[202:203], v249 offset:2048
	ds_read_b64 v[204:205], v249 offset:4096
	ds_read_b64 v[206:207], v249 offset:6144
	v_mfma_f32_32x32x16_f16 v[48:63], a[204:207], v[188:191], v[48:63]
	ds_read_b128 v[188:191], v193 offset:48128
	global_load_lds_dwordx4 v192, s[44:45] offset:2048 sc1
	v_mfma_f32_32x32x16_f16 v[32:47], a[208:211], v[160:163], v[32:47]
	ds_read_b128 v[160:163], v193 offset:49152
	v_mfma_f32_32x32x16_f16 v[48:63], a[208:211], v[164:167], v[48:63]
	ds_read_b128 v[164:167], v193 offset:50176
	v_mfma_f32_32x32x16_f16 v[32:47], a[212:215], v[168:171], v[32:47]
	ds_read_b128 v[168:171], v193 offset:51200
	v_mfma_f32_32x32x16_f16 v[48:63], a[212:215], v[172:175], v[48:63]
	ds_read_b128 v[172:175], v193 offset:52224
	global_load_lds_dwordx4 v192, s[44:45] offset:3072 sc1
	s_waitcnt lgkmcnt(2)
	v_mfma_f32_32x32x16_f16 v[32:47], a[216:219], v[176:179], v[32:47]
	ds_read_b128 v[176:179], v193 offset:53248
	v_mfma_f32_32x32x16_f16 v[48:63], a[216:219], v[180:183], v[48:63]
	ds_read_b128 v[180:183], v193 offset:54272
	v_mfma_f32_32x32x16_f16 v[32:47], a[220:223], v[184:187], v[32:47]
	ds_read_b128 v[184:187], v193 offset:55296
	v_mfma_f32_32x32x16_f16 v[48:63], a[220:223], v[188:191], v[48:63]
	ds_read_b128 v[188:191], v193 offset:56320
	s_mov_b32 m0, s55
	s_add_u32 s44, s34, 0x9000
	s_addc_u32 s45, s35, 0
	global_load_lds_dwordx4 v192, s[44:45] sc1
	v_mfma_f32_32x32x16_f16 v[32:47], a[224:227], v[160:163], v[32:47]
	ds_read_b128 v[160:163], v193 offset:57344
	v_mfma_f32_32x32x16_f16 v[48:63], a[224:227], v[164:167], v[48:63]
	ds_read_b128 v[164:167], v193 offset:58368
	s_waitcnt lgkmcnt(2)
	v_mfma_f32_32x32x16_f16 v[32:47], a[228:231], v[168:171], v[32:47]
	ds_read_b128 v[168:171], v193 offset:59392
	v_add_f32_e32 v200, v200, v202
	v_add_f32_e32 v201, v201, v203
	v_add_f32_e32 v200, v200, v204
	v_add_f32_e32 v201, v201, v205
	v_add_f32_e32 v200, v200, v206
	v_add_f32_e32 v201, v201, v207
	global_store_dwordx2 v250, v[200:201], s[72:73]
	v_mfma_f32_32x32x16_f16 v[48:63], a[228:231], v[172:175], v[48:63]
	ds_read_b128 v[172:175], v193 offset:60416
	global_load_lds_dwordx4 v192, s[44:45] offset:1024 sc1
	v_mfma_f32_32x32x16_f16 v[32:47], a[232:235], v[176:179], v[32:47]
	ds_read_b128 v[176:179], v193 offset:61440
	v_mfma_f32_32x32x16_f16 v[48:63], a[232:235], v[180:183], v[48:63]
	ds_read_b128 v[180:183], v193 offset:62464
	v_mfma_f32_32x32x16_f16 v[32:47], a[236:239], v[184:187], v[32:47]
	ds_read_b128 v[184:187], v193 offset:63488
	s_and_b32 s64, s33, 1
	s_lshl_b32 s64, s64, 22
	s_add_u32 s64, s64, s50
	s_add_u32 s64, s64, 0x20000
	s_add_u32 s36, s6, s64
	s_addc_u32 s37, s7, 0
	s_lshl_b32 s64, s33, 3
	s_add_u32 s64, s64, s29
	s_lshl_b32 s64, s64, 5
	s_add_u32 s64, s64, s30
	s_lshl_b32 s64, s64, 2
	s_add_u32 s40, s8, s64
	s_addc_u32 s41, s9, 0
	s_lshl_b32 s64, s33, 19
	s_add_u32 s64, s64, 0x200
	s_add_u32 s72, s62, s64
	s_addc_u32 s73, s63, 0
	v_mfma_f32_32x32x16_f16 v[48:63], a[236:239], v[188:191], v[48:63]
	ds_read_b128 v[188:191], v193 offset:64512
	global_load_lds_dwordx4 v192, s[44:45] offset:2048 sc1
	s_waitcnt vmcnt(9)
	s_barrier
	s_waitcnt lgkmcnt(2)
	v_mfma_f32_32x32x16_f16 v[32:47], a[240:243], v[160:163], v[32:47]
	ds_read_b128 v[160:163], v192 offset:0
	v_mfma_f32_32x32x16_f16 v[48:63], a[240:243], v[164:167], v[48:63]
	ds_read_b128 v[164:167], v192 offset:1024
	v_mfma_f32_32x32x16_f16 v[32:47], a[244:247], v[168:171], v[32:47]
	ds_read_b128 v[168:171], v192 offset:2048
	v_mfma_f32_32x32x16_f16 v[48:63], a[244:247], v[172:175], v[48:63]
	ds_read_b128 v[172:175], v192 offset:3072
	global_load_lds_dwordx4 v192, s[44:45] offset:3072 sc1
	v_mfma_f32_32x32x16_f16 v[32:47], a[248:251], v[176:179], v[32:47]
	ds_read_b128 v[176:179], v192 offset:4096
	v_mfma_f32_32x32x16_f16 v[48:63], a[248:251], v[180:183], v[48:63]
	ds_read_b128 v[180:183], v192 offset:5120
	s_waitcnt lgkmcnt(2)
	v_mfma_f32_32x32x16_f16 v[32:47], a[252:255], v[184:187], v[32:47]
	ds_read_b128 v[184:187], v192 offset:6144
	v_mfma_f32_32x32x16_f16 v[48:63], a[252:255], v[188:191], v[48:63]
	ds_read_b128 v[188:191], v192 offset:7168
	s_mov_b32 m0, s56
	s_add_u32 s44, s34, 0x10000
	s_addc_u32 s45, s35, 0
	global_load_lds_dwordx4 v192, s[44:45] sc1
	s_nop 3
	s_waitcnt lgkmcnt(2)
	v_mfma_f32_32x32x16_f16 v[64:79], a[0:3], v[160:163], v[64:79]
	ds_read_b128 v[160:163], v192 offset:8192
	v_exp_f32_e32 v200, v32
	v_mfma_f32_32x32x16_f16 v[80:95], a[0:3], v[164:167], v[80:95]
	ds_read_b128 v[164:167], v192 offset:9216
	s_lshl_b32 s64, s71, 3
	s_add_u32 s64, s64, s29
	s_lshl_b32 s64, s64, 7
	s_add_u32 s38, s8, s64
	s_addc_u32 s39, s9, 0
	global_load_dword v251, v196, s[38:39] sc1
	v_exp_f32_e32 v201, v33
	v_add_f32_e32 v200, 1.0, v200
	v_mfma_f32_32x32x16_f16 v[64:79], a[4:7], v[168:171], v[64:79]
	ds_read_b128 v[168:171], v192 offset:10240
	v_exp_f32_e32 v202, v34
	v_add_f32_e32 v201, 1.0, v201
	v_mfma_f32_32x32x16_f16 v[80:95], a[4:7], v[172:175], v[80:95]
	ds_read_b128 v[172:175], v192 offset:11264
	global_load_lds_dwordx4 v192, s[44:45] offset:1024 sc1
	v_exp_f32_e32 v203, v35
	v_add_f32_e32 v202, 1.0, v202
	v_mfma_f32_32x32x16_f16 v[64:79], a[8:11], v[176:179], v[64:79]
	ds_read_b128 v[176:179], v192 offset:12288
	v_exp_f32_e32 v204, v36
	v_add_f32_e32 v203, 1.0, v203
	v_mfma_f32_32x32x16_f16 v[80:95], a[8:11], v[180:183], v[80:95]
	ds_read_b128 v[180:183], v192 offset:13312
	v_exp_f32_e32 v205, v37
	v_add_f32_e32 v204, 1.0, v204
	s_waitcnt lgkmcnt(2)
	v_mfma_f32_32x32x16_f16 v[64:79], a[12:15], v[184:187], v[64:79]
	ds_read_b128 v[184:187], v192 offset:14336
	v_exp_f32_e32 v206, v38
	v_add_f32_e32 v205, 1.0, v205
	v_mfma_f32_32x32x16_f16 v[80:95], a[12:15], v[188:191], v[80:95]
	ds_read_b128 v[188:191], v192 offset:15360
	global_load_lds_dwordx4 v192, s[44:45] offset:2048 sc1
	v_exp_f32_e32 v207, v39
	v_add_f32_e32 v206, 1.0, v206
	v_mfma_f32_32x32x16_f16 v[64:79], a[16:19], v[160:163], v[64:79]
	ds_read_b128 v[160:163], v192 offset:16384
	v_exp_f32_e32 v208, v40
	v_add_f32_e32 v207, 1.0, v207
	v_mfma_f32_32x32x16_f16 v[80:95], a[16:19], v[164:167], v[80:95]
	ds_read_b128 v[164:167], v192 offset:17408
	v_exp_f32_e32 v209, v41
	v_add_f32_e32 v208, 1.0, v208
	v_mfma_f32_32x32x16_f16 v[64:79], a[20:23], v[168:171], v[64:79]
	ds_read_b128 v[168:171], v192 offset:18432
	v_exp_f32_e32 v210, v42
	v_add_f32_e32 v209, 1.0, v209
	v_mfma_f32_32x32x16_f16 v[80:95], a[20:23], v[172:175], v[80:95]
	ds_read_b128 v[172:175], v192 offset:19456
	global_load_lds_dwordx4 v192, s[44:45] offset:3072 sc1
	v_exp_f32_e32 v211, v43
	v_add_f32_e32 v210, 1.0, v210
	s_waitcnt lgkmcnt(2)
	v_mfma_f32_32x32x16_f16 v[64:79], a[24:27], v[176:179], v[64:79]
	ds_read_b128 v[176:179], v192 offset:20480
	v_exp_f32_e32 v212, v44
	v_add_f32_e32 v211, 1.0, v211
	v_mfma_f32_32x32x16_f16 v[80:95], a[24:27], v[180:183], v[80:95]
	ds_read_b128 v[180:183], v192 offset:21504
	v_exp_f32_e32 v213, v45
	v_add_f32_e32 v212, 1.0, v212
	v_mfma_f32_32x32x16_f16 v[64:79], a[28:31], v[184:187], v[64:79]
	ds_read_b128 v[184:187], v192 offset:22528
	v_exp_f32_e32 v214, v46
	v_add_f32_e32 v213, 1.0, v213
	v_mfma_f32_32x32x16_f16 v[80:95], a[28:31], v[188:191], v[80:95]
	ds_read_b128 v[188:191], v192 offset:23552
	s_mov_b32 m0, s57
	s_add_u32 s44, s34, 0x11000
	s_addc_u32 s45, s35, 0
	global_load_lds_dwordx4 v192, s[44:45] sc1
	v_exp_f32_e32 v215, v47
	v_add_f32_e32 v214, 1.0, v214
	v_mfma_f32_32x32x16_f16 v[64:79], a[32:35], v[160:163], v[64:79]
	ds_read_b128 v[160:163], v192 offset:24576
	v_add_f32_e32 v215, 1.0, v215
	v_rcp_f32_e32 v200, v200
	v_mfma_f32_32x32x16_f16 v[80:95], a[32:35], v[164:167], v[80:95]
	ds_read_b128 v[164:167], v192 offset:25600
	v_rcp_f32_e32 v201, v201
	s_waitcnt lgkmcnt(2)
	v_mfma_f32_32x32x16_f16 v[64:79], a[36:39], v[168:171], v[64:79]
	ds_read_b128 v[168:171], v192 offset:26624
	v_rcp_f32_e32 v202, v202
	v_mfma_f32_32x32x16_f16 v[80:95], a[36:39], v[172:175], v[80:95]
	ds_read_b128 v[172:175], v192 offset:27648
	global_load_lds_dwordx4 v192, s[44:45] offset:1024 sc1
	v_rcp_f32_e32 v203, v203
	v_mfma_f32_32x32x16_f16 v[64:79], a[40:43], v[176:179], v[64:79]
	ds_read_b128 v[176:179], v192 offset:28672
	v_rcp_f32_e32 v204, v204
	v_mfma_f32_32x32x16_f16 v[80:95], a[40:43], v[180:183], v[80:95]
	ds_read_b128 v[180:183], v192 offset:29696
	v_rcp_f32_e32 v205, v205
	v_mul_f32_e32 v204, v204, v136
	v_mfma_f32_32x32x16_f16 v[64:79], a[44:47], v[184:187], v[64:79]
	ds_read_b128 v[184:187], v192 offset:30720
	v_rcp_f32_e32 v206, v206
	v_mul_f32_e32 v205, v205, v137
	v_mfma_f32_32x32x16_f16 v[80:95], a[44:47], v[188:191], v[80:95]
	ds_read_b128 v[188:191], v192 offset:31744
	global_load_lds_dwordx4 v192, s[44:45] offset:2048 sc1
	v_rcp_f32_e32 v207, v207
	v_mul_f32_e32 v206, v206, v138
	s_waitcnt vmcnt(8)
	s_barrier
	s_waitcnt lgkmcnt(2)
	v_mfma_f32_32x32x16_f16 v[64:79], a[48:51], v[160:163], v[64:79]
	ds_read_b128 v[160:163], v192 offset:32768
	v_rcp_f32_e32 v208, v208
	v_mul_f32_e32 v207, v207, v139
	v_mfma_f32_32x32x16_f16 v[80:95], a[48:51], v[164:167], v[80:95]
	ds_read_b128 v[164:167], v192 offset:33792
	v_rcp_f32_e32 v209, v209
	v_fmamk_f32 v208, v208, 0xc0b8aa3b, v198
	v_mfma_f32_32x32x16_f16 v[64:79], a[52:55], v[168:171], v[64:79]
	ds_read_b128 v[168:171], v192 offset:34816
	v_rcp_f32_e32 v210, v210
	v_fmamk_f32 v209, v209, 0xc0b8aa3b, v198
	v_fma_f32 v136, v200, v208, v204
	v_mfma_f32_32x32x16_f16 v[80:95], a[52:55], v[172:175], v[80:95]
	ds_read_b128 v[172:175], v192 offset:35840
	global_load_lds_dwordx4 v192, s[44:45] offset:3072 sc1
	v_rcp_f32_e32 v211, v211
	v_fmamk_f32 v210, v210, 0xc0b8aa3b, v198
	v_fma_f32 v137, v201, v209, v205
	v_mfma_f32_32x32x16_f16 v[64:79], a[56:59], v[176:179], v[64:79]
	ds_read_b128 v[176:179], v192 offset:36864
	v_rcp_f32_e32 v212, v212
	v_fmamk_f32 v211, v211, 0xc0b8aa3b, v198
	v_fma_f32 v138, v202, v210, v206
	v_mfma_f32_32x32x16_f16 v[80:95], a[56:59], v[180:183], v[80:95]
	ds_read_b128 v[180:183], v192 offset:37888
	v_rcp_f32_e32 v213, v213
	v_fma_f32 v139, v203, v211, v207
	s_waitcnt lgkmcnt(2)
	v_mfma_f32_32x32x16_f16 v[64:79], a[60:63], v[184:187], v[64:79]
	ds_read_b128 v[184:187], v192 offset:38912
	v_rcp_f32_e32 v214, v214
	v_mfma_f32_32x32x16_f16 v[80:95], a[60:63], v[188:191], v[80:95]
	ds_read_b128 v[188:191], v192 offset:39936
	s_mov_b32 m0, s58
	s_add_u32 s44, s34, 0x18000
	s_addc_u32 s45, s35, 0
	global_load_lds_dwordx4 v192, s[44:45] sc1
	v_rcp_f32_e32 v215, v215
	v_mfma_f32_32x32x16_f16 v[64:79], a[64:67], v[160:163], v[64:79]
	ds_read_b128 v[160:163], v192 offset:40960
	v_exp_f32_e32 v200, v136
	v_mfma_f32_32x32x16_f16 v[80:95], a[64:67], v[164:167], v[80:95]
	ds_read_b128 v[164:167], v192 offset:41984
	v_exp_f32_e32 v201, v137
	v_add_f32_e32 v200, 1.0, v200
	v_mfma_f32_32x32x16_f16 v[64:79], a[68:71], v[168:171], v[64:79]
	ds_read_b128 v[168:171], v192 offset:43008
	v_exp_f32_e32 v202, v138
	v_add_f32_e32 v201, 1.0, v201
	v_mfma_f32_32x32x16_f16 v[80:95], a[68:71], v[172:175], v[80:95]
	ds_read_b128 v[172:175], v192 offset:44032
	global_load_lds_dwordx4 v192, s[44:45] offset:1024 sc1
	v_exp_f32_e32 v203, v139
	v_add_f32_e32 v202, 1.0, v202
	s_waitcnt lgkmcnt(2)
	v_mfma_f32_32x32x16_f16 v[64:79], a[72:75], v[176:179], v[64:79]
	ds_read_b128 v[176:179], v192 offset:45056
	v_add_f32_e32 v203, 1.0, v203
	v_rcp_f32_e32 v200, v200
	v_mfma_f32_32x32x16_f16 v[80:95], a[72:75], v[180:183], v[80:95]
	ds_read_b128 v[180:183], v192 offset:46080
	v_rcp_f32_e32 v201, v201
	v_fma_f32 v200, v200, 2.0, -1.0
	v_mfma_f32_32x32x16_f16 v[64:79], a[76:79], v[184:187], v[64:79]
	ds_read_b128 v[184:187], v192 offset:47104
	v_rcp_f32_e32 v202, v202
	v_fma_f32 v201, v201, 2.0, -1.0
	v_mul_f32_e32 v216, v212, v200
	v_mfma_f32_32x32x16_f16 v[80:95], a[76:79], v[188:191], v[80:95]
	ds_read_b128 v[188:191], v192 offset:48128
	global_load_lds_dwordx4 v192, s[44:45] offset:2048 sc1
	v_rcp_f32_e32 v203, v203
	v_fma_f32 v202, v202, 2.0, -1.0
	v_mul_f32_e32 v217, v213, v201
	v_mfma_f32_32x32x16_f16 v[64:79], a[80:83], v[160:163], v[64:79]
	ds_read_b128 v[160:163], v192 offset:49152
	v_fma_f32 v203, v203, 2.0, -1.0
	v_mul_f32_e32 v218, v214, v202
	v_exp_f32_e32 v200, v48
	v_mfma_f32_32x32x16_f16 v[80:95], a[80:83], v[164:167], v[80:95]
	ds_read_b128 v[164:167], v192 offset:50176
	v_mul_f32_e32 v219, v215, v203
	v_mul_f32_e32 v236, v216, v228
	v_exp_f32_e32 v201, v49
	s_waitcnt lgkmcnt(2)
	v_mfma_f32_32x32x16_f16 v[64:79], a[84:87], v[168:171], v[64:79]
	ds_read_b128 v[168:171], v192 offset:51200
	v_mul_f32_e32 v237, v216, v232
	v_fmac_f32_e32 v236, v217, v229
	v_exp_f32_e32 v202, v50
	v_mfma_f32_32x32x16_f16 v[80:95], a[84:87], v[172:175], v[80:95]
	ds_read_b128 v[172:175], v192 offset:52224
	global_load_lds_dwordx4 v192, s[44:45] offset:3072 sc1
	v_fmac_f32_e32 v237, v217, v233
	v_fmac_f32_e32 v236, v218, v230
	v_exp_f32_e32 v203, v51
	v_mfma_f32_32x32x16_f16 v[64:79], a[88:91], v[176:179], v[64:79]
	ds_read_b128 v[176:179], v192 offset:53248
	v_fmac_f32_e32 v237, v218, v234
	v_fmac_f32_e32 v236, v219, v231
	v_exp_f32_e32 v204, v52
	v_mfma_f32_32x32x16_f16 v[80:95], a[88:91], v[180:183], v[80:95]
	ds_read_b128 v[180:183], v192 offset:54272
	v_fmac_f32_e32 v237, v219, v235
	v_mov_b32_e32 v238, v236
	v_exp_f32_e32 v205, v53
	v_mfma_f32_32x32x16_f16 v[64:79], a[92:95], v[184:187], v[64:79]
	ds_read_b128 v[184:187], v192 offset:55296
	v_mov_b32_e32 v240, v237
	v_cvt_pk_f16_f32 v220, v216, v217
	v_exp_f32_e32 v206, v54
	v_mfma_f32_32x32x16_f16 v[80:95], a[92:95], v[188:191], v[80:95]
	ds_read_b128 v[188:191], v192 offset:56320
	s_mov_b32 m0, s59
	s_add_u32 s44, s34, 0x19000
	s_addc_u32 s45, s35, 0
	global_load_lds_dwordx4 v192, s[44:45] sc1
	v_permlane32_swap_b32_e32 v236, v238
	v_permlane32_swap_b32_e32 v237, v240
	v_add_f32_e32 v238, v236, v238
	v_add_f32_e32 v239, v237, v240
	ds_write_b64 v248, v[238:239] offset:512
	v_exp_f32_e32 v207, v55
	s_waitcnt lgkmcnt(3)
	v_mfma_f32_32x32x16_f16 v[64:79], a[96:99], v[160:163], v[64:79]
	ds_read_b128 v[160:163], v192 offset:57344
	v_cvt_pk_f16_f32 v221, v218, v219
	v_exp_f32_e32 v208, v56
	v_add_f32_e32 v200, 1.0, v200
	v_mfma_f32_32x32x16_f16 v[80:95], a[96:99], v[164:167], v[80:95]
	ds_read_b128 v[164:167], v192 offset:58368
	v_exp_f32_e32 v209, v57
	v_add_f32_e32 v201, 1.0, v201
	v_add_f32_e32 v202, 1.0, v202
	v_mfma_f32_32x32x16_f16 v[64:79], a[100:103], v[168:171], v[64:79]
	ds_read_b128 v[168:171], v192 offset:59392
	v_exp_f32_e32 v210, v58
	v_add_f32_e32 v203, 1.0, v203
	v_add_f32_e32 v204, 1.0, v204
	v_mfma_f32_32x32x16_f16 v[80:95], a[100:103], v[172:175], v[80:95]
	ds_read_b128 v[172:175], v192 offset:60416
	global_load_lds_dwordx4 v192, s[44:45] offset:1024 sc1
	v_exp_f32_e32 v211, v59
	v_add_f32_e32 v205, 1.0, v205
	v_add_f32_e32 v206, 1.0, v206
	v_mfma_f32_32x32x16_f16 v[64:79], a[104:107], v[176:179], v[64:79]
	ds_read_b128 v[176:179], v192 offset:61440
	v_exp_f32_e32 v212, v60
	v_add_f32_e32 v207, 1.0, v207
	v_add_f32_e32 v208, 1.0, v208
	v_mfma_f32_32x32x16_f16 v[80:95], a[104:107], v[180:183], v[80:95]
	ds_read_b128 v[180:183], v192 offset:62464
	v_exp_f32_e32 v213, v61
	v_add_f32_e32 v209, 1.0, v209
	v_add_f32_e32 v210, 1.0, v210
	s_waitcnt lgkmcnt(2)
	v_mfma_f32_32x32x16_f16 v[64:79], a[108:111], v[184:187], v[64:79]
	ds_read_b128 v[184:187], v192 offset:63488
	v_exp_f32_e32 v214, v62
	v_add_f32_e32 v211, 1.0, v211
	v_add_f32_e32 v212, 1.0, v212
	v_mfma_f32_32x32x16_f16 v[80:95], a[108:111], v[188:191], v[80:95]
	ds_read_b128 v[188:191], v192 offset:64512
	global_load_lds_dwordx4 v192, s[44:45] offset:2048 sc1
	v_exp_f32_e32 v215, v63
	v_add_f32_e32 v213, 1.0, v213
	v_add_f32_e32 v214, 1.0, v214
	s_waitcnt vmcnt(7)
	s_barrier
	v_mfma_f32_32x32x16_f16 v[64:79], a[112:115], v[160:163], v[64:79]
	ds_read_b128 v[160:163], v193 offset:0
	v_add_f32_e32 v215, 1.0, v215
	v_rcp_f32_e32 v200, v200
	v_mfma_f32_32x32x16_f16 v[80:95], a[112:115], v[164:167], v[80:95]
	ds_read_b128 v[164:167], v193 offset:1024
	v_rcp_f32_e32 v201, v201
	v_mfma_f32_32x32x16_f16 v[64:79], a[116:119], v[168:171], v[64:79]
	ds_read_b128 v[168:171], v193 offset:2048
	v_rcp_f32_e32 v202, v202
	v_mfma_f32_32x32x16_f16 v[80:95], a[116:119], v[172:175], v[80:95]
	ds_read_b128 v[172:175], v193 offset:3072
	global_load_lds_dwordx4 v192, s[44:45] offset:3072 sc1
	v_rcp_f32_e32 v203, v203
	s_waitcnt lgkmcnt(2)
	v_mfma_f32_32x32x16_f16 v[64:79], a[120:123], v[176:179], v[64:79]
	ds_read_b128 v[176:179], v193 offset:4096
	v_rcp_f32_e32 v204, v204
	s_add_u32 s46, s42, 0x0
	s_addc_u32 s47, s43, 0
	global_load_dwordx4 v[0:3], v192, s[46:47] offset:0
	v_mfma_f32_32x32x16_f16 v[80:95], a[120:123], v[180:183], v[80:95]
	ds_read_b128 v[180:183], v193 offset:5120
	v_rcp_f32_e32 v205, v205
	v_mul_f32_e32 v204, v204, v140
	global_load_dwordx4 v[4:7], v192, s[46:47] offset:1024
	global_load_dwordx4 v[8:11], v192, s[46:47] offset:2048
	v_mfma_f32_32x32x16_f16 v[64:79], a[124:127], v[184:187], v[64:79]
	ds_read_b128 v[184:187], v193 offset:6144
	v_rcp_f32_e32 v206, v206
	v_mul_f32_e32 v205, v205, v141
	global_load_dwordx4 v[12:15], v192, s[46:47] offset:3072
	s_add_u32 s46, s42, 0x1000
	s_addc_u32 s47, s43, 0
	v_mfma_f32_32x32x16_f16 v[80:95], a[124:127], v[188:191], v[80:95]
	ds_read_b128 v[188:191], v193 offset:7168
	v_cmp_gt_u32_e32 vcc, 4, v251
	s_cbranch_vccnz .LD_tpoll29
.LD_tok28:
	s_and_b32 s64, s71, 1
	s_lshl_b32 s64, s64, 22
	s_add_u32 s64, s64, s49
	s_add_u32 s64, s64, 0x60000
	s_add_u32 s34, s6, s64
	s_addc_u32 s35, s7, 0
	s_mov_b32 m0, s52
	s_add_u32 s44, s34, 0x0
	s_addc_u32 s45, s35, 0
	global_load_lds_dwordx4 v192, s[44:45] sc1
	v_rcp_f32_e32 v207, v207
	v_mul_f32_e32 v206, v206, v142
	global_load_dwordx4 v[16:19], v192, s[46:47] offset:0
	global_load_dwordx4 v[20:23], v192, s[46:47] offset:1024
	v_mfma_f32_32x32x16_f16 v[64:79], a[128:131], v[160:163], v[64:79]
	ds_read_b128 v[160:163], v193 offset:8192
	v_rcp_f32_e32 v208, v208
	v_mul_f32_e32 v207, v207, v143
	global_load_dwordx4 v[24:27], v192, s[46:47] offset:2048
	global_load_dwordx4 v[28:31], v192, s[46:47] offset:3072
	v_mfma_f32_32x32x16_f16 v[80:95], a[128:131], v[164:167], v[80:95]
	ds_read_b128 v[164:167], v193 offset:9216
	v_rcp_f32_e32 v209, v209
	v_fmamk_f32 v208, v208, 0xc0b8aa3b, v198
	s_waitcnt lgkmcnt(2)
	v_mfma_f32_32x32x16_f16 v[64:79], a[132:135], v[168:171], v[64:79]
	ds_read_b128 v[168:171], v193 offset:10240
	v_rcp_f32_e32 v210, v210
	v_fmamk_f32 v209, v209, 0xc0b8aa3b, v198
	v_fma_f32 v140, v200, v208, v204
	v_mfma_f32_32x32x16_f16 v[80:95], a[132:135], v[172:175], v[80:95]
	ds_read_b128 v[172:175], v193 offset:11264
	global_load_lds_dwordx4 v192, s[44:45] offset:1024 sc1
	v_rcp_f32_e32 v211, v211
	v_fmamk_f32 v210, v210, 0xc0b8aa3b, v198
	v_fma_f32 v141, v201, v209, v205
	v_mfma_f32_32x32x16_f16 v[64:79], a[136:139], v[176:179], v[64:79]
	ds_read_b128 v[176:179], v193 offset:12288
	v_rcp_f32_e32 v212, v212
	v_fmamk_f32 v211, v211, 0xc0b8aa3b, v198
	v_fma_f32 v142, v202, v210, v206
	v_mfma_f32_32x32x16_f16 v[80:95], a[136:139], v[180:183], v[80:95]
	ds_read_b128 v[180:183], v193 offset:13312
	v_rcp_f32_e32 v213, v213
	v_fma_f32 v143, v203, v211, v207
	v_mfma_f32_32x32x16_f16 v[64:79], a[140:143], v[184:187], v[64:79]
	ds_read_b128 v[184:187], v193 offset:14336
	v_rcp_f32_e32 v214, v214
	v_mfma_f32_32x32x16_f16 v[80:95], a[140:143], v[188:191], v[80:95]
	ds_read_b128 v[188:191], v193 offset:15360
	global_load_lds_dwordx4 v192, s[44:45] offset:2048 sc1
	v_rcp_f32_e32 v215, v215
	s_waitcnt lgkmcnt(2)
	v_mfma_f32_32x32x16_f16 v[64:79], a[144:147], v[160:163], v[64:79]
	ds_read_b128 v[160:163], v193 offset:16384
	v_exp_f32_e32 v200, v140
	v_mfma_f32_32x32x16_f16 v[80:95], a[144:147], v[164:167], v[80:95]
	ds_read_b128 v[164:167], v193 offset:17408
	v_exp_f32_e32 v201, v141
	v_add_f32_e32 v200, 1.0, v200
	v_mfma_f32_32x32x16_f16 v[64:79], a[148:151], v[168:171], v[64:79]
	ds_read_b128 v[168:171], v193 offset:18432
	v_exp_f32_e32 v202, v142
	v_add_f32_e32 v201, 1.0, v201
	v_mfma_f32_32x32x16_f16 v[80:95], a[148:151], v[172:175], v[80:95]
	ds_read_b128 v[172:175], v193 offset:19456
	global_load_lds_dwordx4 v192, s[44:45] offset:3072 sc1
	v_exp_f32_e32 v203, v143
	v_add_f32_e32 v202, 1.0, v202
	v_mfma_f32_32x32x16_f16 v[64:79], a[152:155], v[176:179], v[64:79]
	ds_read_b128 v[176:179], v193 offset:20480
	v_add_f32_e32 v203, 1.0, v203
	v_rcp_f32_e32 v200, v200
	v_mfma_f32_32x32x16_f16 v[80:95], a[152:155], v[180:183], v[80:95]
	ds_read_b128 v[180:183], v193 offset:21504
	v_rcp_f32_e32 v201, v201
	v_fma_f32 v200, v200, 2.0, -1.0
	s_waitcnt lgkmcnt(2)
	v_mfma_f32_32x32x16_f16 v[64:79], a[156:159], v[184:187], v[64:79]
	ds_read_b128 v[184:187], v193 offset:22528
	v_rcp_f32_e32 v202, v202
	v_fma_f32 v201, v201, 2.0, -1.0
	v_mul_f32_e32 v216, v212, v200
	v_mfma_f32_32x32x16_f16 v[80:95], a[156:159], v[188:191], v[80:95]
	ds_read_b128 v[188:191], v193 offset:23552
	s_mov_b32 m0, s53
	s_add_u32 s44, s34, 0x1000
	s_addc_u32 s45, s35, 0
	global_load_lds_dwordx4 v192, s[44:45] sc1
	v_rcp_f32_e32 v203, v203
	v_fma_f32 v202, v202, 2.0, -1.0
	v_mul_f32_e32 v217, v213, v201
	v_mfma_f32_32x32x16_f16 v[64:79], a[160:163], v[160:163], v[64:79]
	ds_read_b128 v[160:163], v193 offset:24576
	v_fma_f32 v203, v203, 2.0, -1.0
	v_mul_f32_e32 v218, v214, v202
	v_mfma_f32_32x32x16_f16 v[80:95], a[160:163], v[164:167], v[80:95]
	ds_read_b128 v[164:167], v193 offset:25600
	v_mul_f32_e32 v219, v215, v203
	v_mul_f32_e32 v236, v216, v228
	v_mfma_f32_32x32x16_f16 v[64:79], a[164:167], v[168:171], v[64:79]
	ds_read_b128 v[168:171], v193 offset:26624
	v_mul_f32_e32 v237, v216, v232
	v_fmac_f32_e32 v236, v217, v229
	v_mfma_f32_32x32x16_f16 v[80:95], a[164:167], v[172:175], v[80:95]
	ds_read_b128 v[172:175], v193 offset:27648
	global_load_lds_dwordx4 v192, s[44:45] offset:1024 sc1
	v_fmac_f32_e32 v237, v217, v233
	v_fmac_f32_e32 v236, v218, v230
	s_waitcnt lgkmcnt(2)
	v_mfma_f32_32x32x16_f16 v[64:79], a[168:171], v[176:179], v[64:79]
	ds_read_b128 v[176:179], v193 offset:28672
	v_fmac_f32_e32 v237, v218, v234
	v_fmac_f32_e32 v236, v219, v231
	v_mfma_f32_32x32x16_f16 v[80:95], a[168:171], v[180:183], v[80:95]
	ds_read_b128 v[180:183], v193 offset:29696
	v_fmac_f32_e32 v237, v219, v235
	v_mov_b32_e32 v238, v236
	v_mfma_f32_32x32x16_f16 v[64:79], a[172:175], v[184:187], v[64:79]
	ds_read_b128 v[184:187], v193 offset:30720
	v_mov_b32_e32 v240, v237
	v_cvt_pk_f16_f32 v222, v216, v217
	v_mfma_f32_32x32x16_f16 v[80:95], a[172:175], v[188:191], v[80:95]
	ds_read_b128 v[188:191], v193 offset:31744
	global_load_lds_dwordx4 v192, s[44:45] offset:2048 sc1
	v_permlane32_swap_b32_e32 v236, v238
	v_permlane32_swap_b32_e32 v237, v240
	v_add_f32_e32 v238, v236, v238
	v_add_f32_e32 v239, v237, v240
	ds_write_b64 v248, v[238:239] offset:768
	s_waitcnt vmcnt(15)
	s_barrier
	v_mfma_f32_32x32x16_f16 v[64:79], a[176:179], v[160:163], v[64:79]
	ds_read_b128 v[160:163], v193 offset:32768
	v_cvt_pk_f16_f32 v223, v218, v219
	v_mfma_f32_32x32x16_f16 v[80:95], a[176:179], v[164:167], v[80:95]
	ds_read_b128 v[164:167], v193 offset:33792
	v_permlane32_swap_b32_e32 v220, v222
	v_permlane32_swap_b32_e32 v221, v223
	s_cmp_eq_u32 s31, 0
	s_cbranch_scc1 .LD_slow30
	global_store_dwordx4 v195, v[220:223], s[36:37] offset:0
.LD_join31:
	s_waitcnt lgkmcnt(3)
	v_mfma_f32_32x32x16_f16 v[64:79], a[180:183], v[168:171], v[64:79]
	ds_read_b128 v[168:171], v193 offset:34816
	v_mfma_f32_32x32x16_f16 v[80:95], a[180:183], v[172:175], v[80:95]
	ds_read_b128 v[172:175], v193 offset:35840
	global_load_lds_dwordx4 v192, s[44:45] offset:3072 sc1
	v_mfma_f32_32x32x16_f16 v[64:79], a[184:187], v[176:179], v[64:79]
	ds_read_b128 v[176:179], v193 offset:36864
	v_mfma_f32_32x32x16_f16 v[80:95], a[184:187], v[180:183], v[80:95]
	ds_read_b128 v[180:183], v193 offset:37888
	v_mfma_f32_32x32x16_f16 v[64:79], a[188:191], v[184:187], v[64:79]
	ds_read_b128 v[184:187], v193 offset:38912
	v_mfma_f32_32x32x16_f16 v[80:95], a[188:191], v[188:191], v[80:95]
	ds_read_b128 v[188:191], v193 offset:39936
	s_mov_b32 m0, s54
	s_add_u32 s44, s34, 0x8000
	s_addc_u32 s45, s35, 0
	global_load_lds_dwordx4 v192, s[44:45] sc1
	s_waitcnt lgkmcnt(2)
	v_mfma_f32_32x32x16_f16 v[64:79], a[192:195], v[160:163], v[64:79]
	ds_read_b128 v[160:163], v193 offset:40960
	v_mfma_f32_32x32x16_f16 v[80:95], a[192:195], v[164:167], v[80:95]
	ds_read_b128 v[164:167], v193 offset:41984
	v_mfma_f32_32x32x16_f16 v[64:79], a[196:199], v[168:171], v[64:79]
	ds_read_b128 v[168:171], v193 offset:43008
	v_mfma_f32_32x32x16_f16 v[80:95], a[196:199], v[172:175], v[80:95]
	ds_read_b128 v[172:175], v193 offset:44032
	global_load_lds_dwordx4 v192, s[44:45] offset:1024 sc1
	v_mfma_f32_32x32x16_f16 v[64:79], a[200:203], v[176:179], v[64:79]
	ds_read_b128 v[176:179], v193 offset:45056
	v_mfma_f32_32x32x16_f16 v[80:95], a[200:203], v[180:183], v[80:95]
	ds_read_b128 v[180:183], v193 offset:46080
	s_waitcnt lgkmcnt(2)
	v_mfma_f32_32x32x16_f16 v[64:79], a[204:207], v[184:187], v[64:79]
	ds_read_b128 v[184:187], v193 offset:47104
	s_waitcnt vmcnt(3)
	s_barrier
	v_mov_b32_e32 v199, 2
	s_cmp_eq_u32 s31, 0
	s_cbranch_scc1 .LD_slow32
	global_store_dword v197, v199, s[40:41]
.LD_join33:
	ds_read_b64 v[200:201], v249 offset:512
	ds_read_b64 v[202:203], v249 offset:2560
	ds_read_b64 v[204:205], v249 offset:4608
	ds_read_b64 v[206:207], v249 offset:6656
	v_mfma_f32_32x32x16_f16 v[80:95], a[204:207], v[188:191], v[80:95]
	ds_read_b128 v[188:191], v193 offset:48128
	global_load_lds_dwordx4 v192, s[44:45] offset:2048 sc1
	v_mfma_f32_32x32x16_f16 v[64:79], a[208:211], v[160:163], v[64:79]
	ds_read_b128 v[160:163], v193 offset:49152
	v_mfma_f32_32x32x16_f16 v[80:95], a[208:211], v[164:167], v[80:95]
	ds_read_b128 v[164:167], v193 offset:50176
	v_mfma_f32_32x32x16_f16 v[64:79], a[212:215], v[168:171], v[64:79]
	ds_read_b128 v[168:171], v193 offset:51200
	v_mfma_f32_32x32x16_f16 v[80:95], a[212:215], v[172:175], v[80:95]
	ds_read_b128 v[172:175], v193 offset:52224
	global_load_lds_dwordx4 v192, s[44:45] offset:3072 sc1
	s_waitcnt lgkmcnt(2)
	v_mfma_f32_32x32x16_f16 v[64:79], a[216:219], v[176:179], v[64:79]
	ds_read_b128 v[176:179], v193 offset:53248
	v_mfma_f32_32x32x16_f16 v[80:95], a[216:219], v[180:183], v[80:95]
	ds_read_b128 v[180:183], v193 offset:54272
	v_mfma_f32_32x32x16_f16 v[64:79], a[220:223], v[184:187], v[64:79]
	ds_read_b128 v[184:187], v193 offset:55296
	v_mfma_f32_32x32x16_f16 v[80:95], a[220:223], v[188:191], v[80:95]
	ds_read_b128 v[188:191], v193 offset:56320
	s_mov_b32 m0, s55
	s_add_u32 s44, s34, 0x9000
	s_addc_u32 s45, s35, 0
	global_load_lds_dwordx4 v192, s[44:45] sc1
	v_mfma_f32_32x32x16_f16 v[64:79], a[224:227], v[160:163], v[64:79]
	ds_read_b128 v[160:163], v193 offset:57344
	v_mfma_f32_32x32x16_f16 v[80:95], a[224:227], v[164:167], v[80:95]
	ds_read_b128 v[164:167], v193 offset:58368
	s_waitcnt lgkmcnt(2)
	v_mfma_f32_32x32x16_f16 v[64:79], a[228:231], v[168:171], v[64:79]
	ds_read_b128 v[168:171], v193 offset:59392
	v_add_f32_e32 v200, v200, v202
	v_add_f32_e32 v201, v201, v203
	v_add_f32_e32 v200, v200, v204
	v_add_f32_e32 v201, v201, v205
	v_add_f32_e32 v200, v200, v206
	v_add_f32_e32 v201, v201, v207
	global_store_dwordx2 v250, v[200:201], s[72:73]
	v_mfma_f32_32x32x16_f16 v[80:95], a[228:231], v[172:175], v[80:95]
	ds_read_b128 v[172:175], v193 offset:60416
	global_load_lds_dwordx4 v192, s[44:45] offset:1024 sc1
	v_mfma_f32_32x32x16_f16 v[64:79], a[232:235], v[176:179], v[64:79]
	ds_read_b128 v[176:179], v193 offset:61440
	v_mfma_f32_32x32x16_f16 v[80:95], a[232:235], v[180:183], v[80:95]
	ds_read_b128 v[180:183], v193 offset:62464
	v_mfma_f32_32x32x16_f16 v[64:79], a[236:239], v[184:187], v[64:79]
	ds_read_b128 v[184:187], v193 offset:63488
	s_and_b32 s64, s33, 1
	s_lshl_b32 s64, s64, 22
	s_add_u32 s64, s64, s50
	s_add_u32 s64, s64, 0x40000
	s_add_u32 s36, s6, s64
	s_addc_u32 s37, s7, 0
	s_lshl_b32 s64, s33, 3
	s_add_u32 s64, s64, s29
	s_lshl_b32 s64, s64, 5
	s_add_u32 s64, s64, s30
	s_lshl_b32 s64, s64, 2
	s_add_u32 s40, s8, s64
	s_addc_u32 s41, s9, 0
	s_lshl_b32 s64, s33, 19
	s_add_u32 s64, s64, 0x400
	s_add_u32 s72, s62, s64
	s_addc_u32 s73, s63, 0
	v_mfma_f32_32x32x16_f16 v[80:95], a[236:239], v[188:191], v[80:95]
	ds_read_b128 v[188:191], v193 offset:64512
	global_load_lds_dwordx4 v192, s[44:45] offset:2048 sc1
	s_waitcnt vmcnt(9)
	s_barrier
	s_waitcnt lgkmcnt(2)
	v_mfma_f32_32x32x16_f16 v[64:79], a[240:243], v[160:163], v[64:79]
	ds_read_b128 v[160:163], v192 offset:0
	v_mfma_f32_32x32x16_f16 v[80:95], a[240:243], v[164:167], v[80:95]
	ds_read_b128 v[164:167], v192 offset:1024
	v_mfma_f32_32x32x16_f16 v[64:79], a[244:247], v[168:171], v[64:79]
	ds_read_b128 v[168:171], v192 offset:2048
	v_mfma_f32_32x32x16_f16 v[80:95], a[244:247], v[172:175], v[80:95]
	ds_read_b128 v[172:175], v192 offset:3072
	global_load_lds_dwordx4 v192, s[44:45] offset:3072 sc1
	v_mfma_f32_32x32x16_f16 v[64:79], a[248:251], v[176:179], v[64:79]
	ds_read_b128 v[176:179], v192 offset:4096
	v_mfma_f32_32x32x16_f16 v[80:95], a[248:251], v[180:183], v[80:95]
	ds_read_b128 v[180:183], v192 offset:5120
	s_waitcnt lgkmcnt(2)
	v_mfma_f32_32x32x16_f16 v[64:79], a[252:255], v[184:187], v[64:79]
	ds_read_b128 v[184:187], v192 offset:6144
	v_mfma_f32_32x32x16_f16 v[80:95], a[252:255], v[188:191], v[80:95]
	ds_read_b128 v[188:191], v192 offset:7168
	s_mov_b32 m0, s56
	s_add_u32 s44, s34, 0x10000
	s_addc_u32 s45, s35, 0
	global_load_lds_dwordx4 v192, s[44:45] sc1
	s_nop 3
	s_waitcnt lgkmcnt(2)
	v_mfma_f32_32x32x16_f16 v[96:111], a[0:3], v[160:163], v[96:111]
	ds_read_b128 v[160:163], v192 offset:8192
	v_exp_f32_e32 v200, v64
	v_mfma_f32_32x32x16_f16 v[112:127], a[0:3], v[164:167], v[112:127]
	ds_read_b128 v[164:167], v192 offset:9216
	s_lshl_b32 s64, s33, 3
	s_add_u32 s64, s64, s29
	s_lshl_b32 s64, s64, 7
	s_add_u32 s38, s8, s64
	s_addc_u32 s39, s9, 0
	global_load_dword v251, v196, s[38:39] sc1
	v_exp_f32_e32 v201, v65
	v_add_f32_e32 v200, 1.0, v200
	v_mfma_f32_32x32x16_f16 v[96:111], a[4:7], v[168:171], v[96:111]
	ds_read_b128 v[168:171], v192 offset:10240
	v_exp_f32_e32 v202, v66
	v_add_f32_e32 v201, 1.0, v201
	v_mfma_f32_32x32x16_f16 v[112:127], a[4:7], v[172:175], v[112:127]
	ds_read_b128 v[172:175], v192 offset:11264
	global_load_lds_dwordx4 v192, s[44:45] offset:1024 sc1
	v_exp_f32_e32 v203, v67
	v_add_f32_e32 v202, 1.0, v202
	v_mfma_f32_32x32x16_f16 v[96:111], a[8:11], v[176:179], v[96:111]
	ds_read_b128 v[176:179], v192 offset:12288
	v_exp_f32_e32 v204, v68
	v_add_f32_e32 v203, 1.0, v203
	v_mfma_f32_32x32x16_f16 v[112:127], a[8:11], v[180:183], v[112:127]
	ds_read_b128 v[180:183], v192 offset:13312
	v_exp_f32_e32 v205, v69
	v_add_f32_e32 v204, 1.0, v204
	s_waitcnt lgkmcnt(2)
	v_mfma_f32_32x32x16_f16 v[96:111], a[12:15], v[184:187], v[96:111]
	ds_read_b128 v[184:187], v192 offset:14336
	v_exp_f32_e32 v206, v70
	v_add_f32_e32 v205, 1.0, v205
	v_mfma_f32_32x32x16_f16 v[112:127], a[12:15], v[188:191], v[112:127]
	ds_read_b128 v[188:191], v192 offset:15360
	global_load_lds_dwordx4 v192, s[44:45] offset:2048 sc1
	v_exp_f32_e32 v207, v71
	v_add_f32_e32 v206, 1.0, v206
	v_mfma_f32_32x32x16_f16 v[96:111], a[16:19], v[160:163], v[96:111]
	ds_read_b128 v[160:163], v192 offset:16384
	v_exp_f32_e32 v208, v72
	v_add_f32_e32 v207, 1.0, v207
	v_mfma_f32_32x32x16_f16 v[112:127], a[16:19], v[164:167], v[112:127]
	ds_read_b128 v[164:167], v192 offset:17408
	v_exp_f32_e32 v209, v73
	v_add_f32_e32 v208, 1.0, v208
	v_mfma_f32_32x32x16_f16 v[96:111], a[20:23], v[168:171], v[96:111]
	ds_read_b128 v[168:171], v192 offset:18432
	v_exp_f32_e32 v210, v74
	v_add_f32_e32 v209, 1.0, v209
	v_mfma_f32_32x32x16_f16 v[112:127], a[20:23], v[172:175], v[112:127]
	ds_read_b128 v[172:175], v192 offset:19456
	global_load_lds_dwordx4 v192, s[44:45] offset:3072 sc1
	v_exp_f32_e32 v211, v75
	v_add_f32_e32 v210, 1.0, v210
	s_waitcnt lgkmcnt(2)
	v_mfma_f32_32x32x16_f16 v[96:111], a[24:27], v[176:179], v[96:111]
	ds_read_b128 v[176:179], v192 offset:20480
	v_exp_f32_e32 v212, v76
	v_add_f32_e32 v211, 1.0, v211
	v_mfma_f32_32x32x16_f16 v[112:127], a[24:27], v[180:183], v[112:127]
	ds_read_b128 v[180:183], v192 offset:21504
	v_exp_f32_e32 v213, v77
	v_add_f32_e32 v212, 1.0, v212
	v_mfma_f32_32x32x16_f16 v[96:111], a[28:31], v[184:187], v[96:111]
	ds_read_b128 v[184:187], v192 offset:22528
	v_exp_f32_e32 v214, v78
	v_add_f32_e32 v213, 1.0, v213
	v_mfma_f32_32x32x16_f16 v[112:127], a[28:31], v[188:191], v[112:127]
	ds_read_b128 v[188:191], v192 offset:23552
	s_mov_b32 m0, s57
	s_add_u32 s44, s34, 0x11000
	s_addc_u32 s45, s35, 0
	global_load_lds_dwordx4 v192, s[44:45] sc1
	v_exp_f32_e32 v215, v79
	v_add_f32_e32 v214, 1.0, v214
	v_mfma_f32_32x32x16_f16 v[96:111], a[32:35], v[160:163], v[96:111]
	ds_read_b128 v[160:163], v192 offset:24576
	v_add_f32_e32 v215, 1.0, v215
	v_rcp_f32_e32 v200, v200
	v_mfma_f32_32x32x16_f16 v[112:127], a[32:35], v[164:167], v[112:127]
	ds_read_b128 v[164:167], v192 offset:25600
	v_rcp_f32_e32 v201, v201
	s_waitcnt lgkmcnt(2)
	v_mfma_f32_32x32x16_f16 v[96:111], a[36:39], v[168:171], v[96:111]
	ds_read_b128 v[168:171], v192 offset:26624
	v_rcp_f32_e32 v202, v202
	v_mfma_f32_32x32x16_f16 v[112:127], a[36:39], v[172:175], v[112:127]
	ds_read_b128 v[172:175], v192 offset:27648
	global_load_lds_dwordx4 v192, s[44:45] offset:1024 sc1
	v_rcp_f32_e32 v203, v203
	v_mfma_f32_32x32x16_f16 v[96:111], a[40:43], v[176:179], v[96:111]
	ds_read_b128 v[176:179], v192 offset:28672
	v_rcp_f32_e32 v204, v204
	v_mfma_f32_32x32x16_f16 v[112:127], a[40:43], v[180:183], v[112:127]
	ds_read_b128 v[180:183], v192 offset:29696
	v_rcp_f32_e32 v205, v205
	v_mul_f32_e32 v204, v204, v144
	v_mfma_f32_32x32x16_f16 v[96:111], a[44:47], v[184:187], v[96:111]
	ds_read_b128 v[184:187], v192 offset:30720
	v_rcp_f32_e32 v206, v206
	v_mul_f32_e32 v205, v205, v145
	v_mfma_f32_32x32x16_f16 v[112:127], a[44:47], v[188:191], v[112:127]
	ds_read_b128 v[188:191], v192 offset:31744
	global_load_lds_dwordx4 v192, s[44:45] offset:2048 sc1
	v_rcp_f32_e32 v207, v207
	v_mul_f32_e32 v206, v206, v146
	s_waitcnt vmcnt(8)
	s_barrier
	s_waitcnt lgkmcnt(2)
	v_mfma_f32_32x32x16_f16 v[96:111], a[48:51], v[160:163], v[96:111]
	ds_read_b128 v[160:163], v192 offset:32768
	v_rcp_f32_e32 v208, v208
	v_mul_f32_e32 v207, v207, v147
	v_mfma_f32_32x32x16_f16 v[112:127], a[48:51], v[164:167], v[112:127]
	ds_read_b128 v[164:167], v192 offset:33792
	v_rcp_f32_e32 v209, v209
	v_fmamk_f32 v208, v208, 0xc0b8aa3b, v198
	v_mfma_f32_32x32x16_f16 v[96:111], a[52:55], v[168:171], v[96:111]
	ds_read_b128 v[168:171], v192 offset:34816
	v_rcp_f32_e32 v210, v210
	v_fmamk_f32 v209, v209, 0xc0b8aa3b, v198
	v_fma_f32 v144, v200, v208, v204
	v_mfma_f32_32x32x16_f16 v[112:127], a[52:55], v[172:175], v[112:127]
	ds_read_b128 v[172:175], v192 offset:35840
	global_load_lds_dwordx4 v192, s[44:45] offset:3072 sc1
	v_rcp_f32_e32 v211, v211
	v_fmamk_f32 v210, v210, 0xc0b8aa3b, v198
	v_fma_f32 v145, v201, v209, v205
	v_mfma_f32_32x32x16_f16 v[96:111], a[56:59], v[176:179], v[96:111]
	ds_read_b128 v[176:179], v192 offset:36864
	v_rcp_f32_e32 v212, v212
	v_fmamk_f32 v211, v211, 0xc0b8aa3b, v198
	v_fma_f32 v146, v202, v210, v206
	v_mfma_f32_32x32x16_f16 v[112:127], a[56:59], v[180:183], v[112:127]
	ds_read_b128 v[180:183], v192 offset:37888
	v_rcp_f32_e32 v213, v213
	v_fma_f32 v147, v203, v211, v207
	s_waitcnt lgkmcnt(2)
	v_mfma_f32_32x32x16_f16 v[96:111], a[60:63], v[184:187], v[96:111]
	ds_read_b128 v[184:187], v192 offset:38912
	v_rcp_f32_e32 v214, v214
	v_mfma_f32_32x32x16_f16 v[112:127], a[60:63], v[188:191], v[112:127]
	ds_read_b128 v[188:191], v192 offset:39936
	s_mov_b32 m0, s58
	s_add_u32 s44, s34, 0x18000
	s_addc_u32 s45, s35, 0
	global_load_lds_dwordx4 v192, s[44:45] sc1
	v_rcp_f32_e32 v215, v215
	v_mfma_f32_32x32x16_f16 v[96:111], a[64:67], v[160:163], v[96:111]
	ds_read_b128 v[160:163], v192 offset:40960
	v_exp_f32_e32 v200, v144
	v_mfma_f32_32x32x16_f16 v[112:127], a[64:67], v[164:167], v[112:127]
	ds_read_b128 v[164:167], v192 offset:41984
	v_exp_f32_e32 v201, v145
	v_add_f32_e32 v200, 1.0, v200
	v_mfma_f32_32x32x16_f16 v[96:111], a[68:71], v[168:171], v[96:111]
	ds_read_b128 v[168:171], v192 offset:43008
	v_exp_f32_e32 v202, v146
	v_add_f32_e32 v201, 1.0, v201
	v_mfma_f32_32x32x16_f16 v[112:127], a[68:71], v[172:175], v[112:127]
	ds_read_b128 v[172:175], v192 offset:44032
	global_load_lds_dwordx4 v192, s[44:45] offset:1024 sc1
	v_exp_f32_e32 v203, v147
	v_add_f32_e32 v202, 1.0, v202
	s_waitcnt lgkmcnt(2)
	v_mfma_f32_32x32x16_f16 v[96:111], a[72:75], v[176:179], v[96:111]
	ds_read_b128 v[176:179], v192 offset:45056
	v_add_f32_e32 v203, 1.0, v203
	v_rcp_f32_e32 v200, v200
	v_mfma_f32_32x32x16_f16 v[112:127], a[72:75], v[180:183], v[112:127]
	ds_read_b128 v[180:183], v192 offset:46080
	v_rcp_f32_e32 v201, v201
	v_fma_f32 v200, v200, 2.0, -1.0
	v_mfma_f32_32x32x16_f16 v[96:111], a[76:79], v[184:187], v[96:111]
	ds_read_b128 v[184:187], v192 offset:47104
	v_rcp_f32_e32 v202, v202
	v_fma_f32 v201, v201, 2.0, -1.0
	v_mul_f32_e32 v216, v212, v200
	v_mfma_f32_32x32x16_f16 v[112:127], a[76:79], v[188:191], v[112:127]
	ds_read_b128 v[188:191], v192 offset:48128
	global_load_lds_dwordx4 v192, s[44:45] offset:2048 sc1
	v_rcp_f32_e32 v203, v203
	v_fma_f32 v202, v202, 2.0, -1.0
	v_mul_f32_e32 v217, v213, v201
	v_mfma_f32_32x32x16_f16 v[96:111], a[80:83], v[160:163], v[96:111]
	ds_read_b128 v[160:163], v192 offset:49152
	v_fma_f32 v203, v203, 2.0, -1.0
	v_mul_f32_e32 v218, v214, v202
	v_exp_f32_e32 v200, v80
	v_mfma_f32_32x32x16_f16 v[112:127], a[80:83], v[164:167], v[112:127]
	ds_read_b128 v[164:167], v192 offset:50176
	v_mul_f32_e32 v219, v215, v203
	v_mul_f32_e32 v236, v216, v228
	v_exp_f32_e32 v201, v81
	s_waitcnt lgkmcnt(2)
	v_mfma_f32_32x32x16_f16 v[96:111], a[84:87], v[168:171], v[96:111]
	ds_read_b128 v[168:171], v192 offset:51200
	v_mul_f32_e32 v237, v216, v232
	v_fmac_f32_e32 v236, v217, v229
	v_exp_f32_e32 v202, v82
	v_mfma_f32_32x32x16_f16 v[112:127], a[84:87], v[172:175], v[112:127]
	ds_read_b128 v[172:175], v192 offset:52224
	global_load_lds_dwordx4 v192, s[44:45] offset:3072 sc1
	v_fmac_f32_e32 v237, v217, v233
	v_fmac_f32_e32 v236, v218, v230
	v_exp_f32_e32 v203, v83
	v_mfma_f32_32x32x16_f16 v[96:111], a[88:91], v[176:179], v[96:111]
	ds_read_b128 v[176:179], v192 offset:53248
	v_fmac_f32_e32 v237, v218, v234
	v_fmac_f32_e32 v236, v219, v231
	v_exp_f32_e32 v204, v84
	v_mfma_f32_32x32x16_f16 v[112:127], a[88:91], v[180:183], v[112:127]
	ds_read_b128 v[180:183], v192 offset:54272
	v_fmac_f32_e32 v237, v219, v235
	v_mov_b32_e32 v238, v236
	v_exp_f32_e32 v205, v85
	v_mfma_f32_32x32x16_f16 v[96:111], a[92:95], v[184:187], v[96:111]
	ds_read_b128 v[184:187], v192 offset:55296
	v_mov_b32_e32 v240, v237
	v_cvt_pk_f16_f32 v220, v216, v217
	v_exp_f32_e32 v206, v86
	v_mfma_f32_32x32x16_f16 v[112:127], a[92:95], v[188:191], v[112:127]
	ds_read_b128 v[188:191], v192 offset:56320
	s_mov_b32 m0, s59
	s_add_u32 s44, s34, 0x19000
	s_addc_u32 s45, s35, 0
	global_load_lds_dwordx4 v192, s[44:45] sc1
	v_permlane32_swap_b32_e32 v236, v238
	v_permlane32_swap_b32_e32 v237, v240
	v_add_f32_e32 v238, v236, v238
	v_add_f32_e32 v239, v237, v240
	ds_write_b64 v248, v[238:239] offset:1024
	v_exp_f32_e32 v207, v87
	s_waitcnt lgkmcnt(3)
	v_mfma_f32_32x32x16_f16 v[96:111], a[96:99], v[160:163], v[96:111]
	ds_read_b128 v[160:163], v192 offset:57344
	v_cvt_pk_f16_f32 v221, v218, v219
	v_exp_f32_e32 v208, v88
	v_add_f32_e32 v200, 1.0, v200
	v_mfma_f32_32x32x16_f16 v[112:127], a[96:99], v[164:167], v[112:127]
	ds_read_b128 v[164:167], v192 offset:58368
	v_exp_f32_e32 v209, v89
	v_add_f32_e32 v201, 1.0, v201
	v_add_f32_e32 v202, 1.0, v202
	v_mfma_f32_32x32x16_f16 v[96:111], a[100:103], v[168:171], v[96:111]
	ds_read_b128 v[168:171], v192 offset:59392
	v_exp_f32_e32 v210, v90
	v_add_f32_e32 v203, 1.0, v203
	v_add_f32_e32 v204, 1.0, v204
	v_mfma_f32_32x32x16_f16 v[112:127], a[100:103], v[172:175], v[112:127]
	ds_read_b128 v[172:175], v192 offset:60416
	global_load_lds_dwordx4 v192, s[44:45] offset:1024 sc1
	v_exp_f32_e32 v211, v91
	v_add_f32_e32 v205, 1.0, v205
	v_add_f32_e32 v206, 1.0, v206
	v_mfma_f32_32x32x16_f16 v[96:111], a[104:107], v[176:179], v[96:111]
	ds_read_b128 v[176:179], v192 offset:61440
	v_exp_f32_e32 v212, v92
	v_add_f32_e32 v207, 1.0, v207
	v_add_f32_e32 v208, 1.0, v208
	v_mfma_f32_32x32x16_f16 v[112:127], a[104:107], v[180:183], v[112:127]
	ds_read_b128 v[180:183], v192 offset:62464
	v_exp_f32_e32 v213, v93
	v_add_f32_e32 v209, 1.0, v209
	v_add_f32_e32 v210, 1.0, v210
	s_waitcnt lgkmcnt(2)
	v_mfma_f32_32x32x16_f16 v[96:111], a[108:111], v[184:187], v[96:111]
	ds_read_b128 v[184:187], v192 offset:63488
	v_exp_f32_e32 v214, v94
	v_add_f32_e32 v211, 1.0, v211
	v_add_f32_e32 v212, 1.0, v212
	v_mfma_f32_32x32x16_f16 v[112:127], a[108:111], v[188:191], v[112:127]
	ds_read_b128 v[188:191], v192 offset:64512
	global_load_lds_dwordx4 v192, s[44:45] offset:2048 sc1
	v_exp_f32_e32 v215, v95
	v_add_f32_e32 v213, 1.0, v213
	v_add_f32_e32 v214, 1.0, v214
	s_waitcnt vmcnt(7)
	s_barrier
	v_mfma_f32_32x32x16_f16 v[96:111], a[112:115], v[160:163], v[96:111]
	ds_read_b128 v[160:163], v193 offset:0
	v_add_f32_e32 v215, 1.0, v215
	v_rcp_f32_e32 v200, v200
	v_mfma_f32_32x32x16_f16 v[112:127], a[112:115], v[164:167], v[112:127]
	ds_read_b128 v[164:167], v193 offset:1024
	v_rcp_f32_e32 v201, v201
	v_mfma_f32_32x32x16_f16 v[96:111], a[116:119], v[168:171], v[96:111]
	ds_read_b128 v[168:171], v193 offset:2048
	v_rcp_f32_e32 v202, v202
	v_mfma_f32_32x32x16_f16 v[112:127], a[116:119], v[172:175], v[112:127]
	ds_read_b128 v[172:175], v193 offset:3072
	global_load_lds_dwordx4 v192, s[44:45] offset:3072 sc1
	v_rcp_f32_e32 v203, v203
	s_waitcnt lgkmcnt(2)
	v_mfma_f32_32x32x16_f16 v[96:111], a[120:123], v[176:179], v[96:111]
	ds_read_b128 v[176:179], v193 offset:4096
	v_rcp_f32_e32 v204, v204
	s_add_u32 s46, s42, 0x2000
	s_addc_u32 s47, s43, 0
	global_load_dwordx4 v[32:35], v192, s[46:47] offset:0
	v_mfma_f32_32x32x16_f16 v[112:127], a[120:123], v[180:183], v[112:127]
	ds_read_b128 v[180:183], v193 offset:5120
	v_rcp_f32_e32 v205, v205
	v_mul_f32_e32 v204, v204, v148
	global_load_dwordx4 v[36:39], v192, s[46:47] offset:1024
	global_load_dwordx4 v[40:43], v192, s[46:47] offset:2048
	v_mfma_f32_32x32x16_f16 v[96:111], a[124:127], v[184:187], v[96:111]
	ds_read_b128 v[184:187], v193 offset:6144
	v_rcp_f32_e32 v206, v206
	v_mul_f32_e32 v205, v205, v149
	global_load_dwordx4 v[44:47], v192, s[46:47] offset:3072
	s_add_u32 s46, s42, 0x3000
	s_addc_u32 s47, s43, 0
	v_mfma_f32_32x32x16_f16 v[112:127], a[124:127], v[188:191], v[112:127]
	ds_read_b128 v[188:191], v193 offset:7168
	v_cmp_gt_u32_e32 vcc, 1, v251
	s_cbranch_vccnz .LD_tpoll35
.LD_tok34:
	s_and_b32 s64, s33, 1
	s_lshl_b32 s64, s64, 22
	s_add_u32 s64, s64, s49
	s_add_u32 s34, s6, s64
	s_addc_u32 s35, s7, 0
	s_mov_b32 m0, s52
	s_add_u32 s44, s34, 0x0
	s_addc_u32 s45, s35, 0
	global_load_lds_dwordx4 v192, s[44:45] sc1
	v_rcp_f32_e32 v207, v207
	v_mul_f32_e32 v206, v206, v150
	global_load_dwordx4 v[48:51], v192, s[46:47] offset:0
	global_load_dwordx4 v[52:55], v192, s[46:47] offset:1024
	v_mfma_f32_32x32x16_f16 v[96:111], a[128:131], v[160:163], v[96:111]
	ds_read_b128 v[160:163], v193 offset:8192
	v_rcp_f32_e32 v208, v208
	v_mul_f32_e32 v207, v207, v151
	global_load_dwordx4 v[56:59], v192, s[46:47] offset:2048
	global_load_dwordx4 v[60:63], v192, s[46:47] offset:3072
	v_mfma_f32_32x32x16_f16 v[112:127], a[128:131], v[164:167], v[112:127]
	ds_read_b128 v[164:167], v193 offset:9216
	v_rcp_f32_e32 v209, v209
	v_fmamk_f32 v208, v208, 0xc0b8aa3b, v198
	s_waitcnt lgkmcnt(2)
	v_mfma_f32_32x32x16_f16 v[96:111], a[132:135], v[168:171], v[96:111]
	ds_read_b128 v[168:171], v193 offset:10240
	v_rcp_f32_e32 v210, v210
	v_fmamk_f32 v209, v209, 0xc0b8aa3b, v198
	v_fma_f32 v148, v200, v208, v204
	v_mfma_f32_32x32x16_f16 v[112:127], a[132:135], v[172:175], v[112:127]
	ds_read_b128 v[172:175], v193 offset:11264
	global_load_lds_dwordx4 v192, s[44:45] offset:1024 sc1
	v_rcp_f32_e32 v211, v211
	v_fmamk_f32 v210, v210, 0xc0b8aa3b, v198
	v_fma_f32 v149, v201, v209, v205
	v_mfma_f32_32x32x16_f16 v[96:111], a[136:139], v[176:179], v[96:111]
	ds_read_b128 v[176:179], v193 offset:12288
	v_rcp_f32_e32 v212, v212
	v_fmamk_f32 v211, v211, 0xc0b8aa3b, v198
	v_fma_f32 v150, v202, v210, v206
	v_mfma_f32_32x32x16_f16 v[112:127], a[136:139], v[180:183], v[112:127]
	ds_read_b128 v[180:183], v193 offset:13312
	v_rcp_f32_e32 v213, v213
	v_fma_f32 v151, v203, v211, v207
	v_mfma_f32_32x32x16_f16 v[96:111], a[140:143], v[184:187], v[96:111]
	ds_read_b128 v[184:187], v193 offset:14336
	v_rcp_f32_e32 v214, v214
	v_mfma_f32_32x32x16_f16 v[112:127], a[140:143], v[188:191], v[112:127]
	ds_read_b128 v[188:191], v193 offset:15360
	global_load_lds_dwordx4 v192, s[44:45] offset:2048 sc1
	v_rcp_f32_e32 v215, v215
	s_waitcnt lgkmcnt(2)
	v_mfma_f32_32x32x16_f16 v[96:111], a[144:147], v[160:163], v[96:111]
	ds_read_b128 v[160:163], v193 offset:16384
	v_exp_f32_e32 v200, v148
	v_mfma_f32_32x32x16_f16 v[112:127], a[144:147], v[164:167], v[112:127]
	ds_read_b128 v[164:167], v193 offset:17408
	v_exp_f32_e32 v201, v149
	v_add_f32_e32 v200, 1.0, v200
	v_mfma_f32_32x32x16_f16 v[96:111], a[148:151], v[168:171], v[96:111]
	ds_read_b128 v[168:171], v193 offset:18432
	v_exp_f32_e32 v202, v150
	v_add_f32_e32 v201, 1.0, v201
	v_mfma_f32_32x32x16_f16 v[112:127], a[148:151], v[172:175], v[112:127]
	ds_read_b128 v[172:175], v193 offset:19456
	global_load_lds_dwordx4 v192, s[44:45] offset:3072 sc1
	v_exp_f32_e32 v203, v151
	v_add_f32_e32 v202, 1.0, v202
	v_mfma_f32_32x32x16_f16 v[96:111], a[152:155], v[176:179], v[96:111]
	ds_read_b128 v[176:179], v193 offset:20480
	v_add_f32_e32 v203, 1.0, v203
	v_rcp_f32_e32 v200, v200
	v_mfma_f32_32x32x16_f16 v[112:127], a[152:155], v[180:183], v[112:127]
	ds_read_b128 v[180:183], v193 offset:21504
	v_rcp_f32_e32 v201, v201
	v_fma_f32 v200, v200, 2.0, -1.0
	s_waitcnt lgkmcnt(2)
	v_mfma_f32_32x32x16_f16 v[96:111], a[156:159], v[184:187], v[96:111]
	ds_read_b128 v[184:187], v193 offset:22528
	v_rcp_f32_e32 v202, v202
	v_fma_f32 v201, v201, 2.0, -1.0
	v_mul_f32_e32 v216, v212, v200
	v_mfma_f32_32x32x16_f16 v[112:127], a[156:159], v[188:191], v[112:127]
	ds_read_b128 v[188:191], v193 offset:23552
	s_mov_b32 m0, s53
	s_add_u32 s44, s34, 0x1000
	s_addc_u32 s45, s35, 0
	global_load_lds_dwordx4 v192, s[44:45] sc1
	v_rcp_f32_e32 v203, v203
	v_fma_f32 v202, v202, 2.0, -1.0
	v_mul_f32_e32 v217, v213, v201
	v_mfma_f32_32x32x16_f16 v[96:111], a[160:163], v[160:163], v[96:111]
	ds_read_b128 v[160:163], v193 offset:24576
	v_fma_f32 v203, v203, 2.0, -1.0
	v_mul_f32_e32 v218, v214, v202
	v_mfma_f32_32x32x16_f16 v[112:127], a[160:163], v[164:167], v[112:127]
	ds_read_b128 v[164:167], v193 offset:25600
	v_mul_f32_e32 v219, v215, v203
	v_mul_f32_e32 v236, v216, v228
	v_mfma_f32_32x32x16_f16 v[96:111], a[164:167], v[168:171], v[96:111]
	ds_read_b128 v[168:171], v193 offset:26624
	v_mul_f32_e32 v237, v216, v232
	v_fmac_f32_e32 v236, v217, v229
	v_mfma_f32_32x32x16_f16 v[112:127], a[164:167], v[172:175], v[112:127]
	ds_read_b128 v[172:175], v193 offset:27648
	global_load_lds_dwordx4 v192, s[44:45] offset:1024 sc1
	v_fmac_f32_e32 v237, v217, v233
	v_fmac_f32_e32 v236, v218, v230
	s_waitcnt lgkmcnt(2)
	v_mfma_f32_32x32x16_f16 v[96:111], a[168:171], v[176:179], v[96:111]
	ds_read_b128 v[176:179], v193 offset:28672
	v_fmac_f32_e32 v237, v218, v234
	v_fmac_f32_e32 v236, v219, v231
	v_mfma_f32_32x32x16_f16 v[112:127], a[168:171], v[180:183], v[112:127]
	ds_read_b128 v[180:183], v193 offset:29696
	v_fmac_f32_e32 v237, v219, v235
	v_mov_b32_e32 v238, v236
	v_mfma_f32_32x32x16_f16 v[96:111], a[172:175], v[184:187], v[96:111]
	ds_read_b128 v[184:187], v193 offset:30720
	v_mov_b32_e32 v240, v237
	v_cvt_pk_f16_f32 v222, v216, v217
	v_mfma_f32_32x32x16_f16 v[112:127], a[172:175], v[188:191], v[112:127]
	ds_read_b128 v[188:191], v193 offset:31744
	global_load_lds_dwordx4 v192, s[44:45] offset:2048 sc1
	v_permlane32_swap_b32_e32 v236, v238
	v_permlane32_swap_b32_e32 v237, v240
	v_add_f32_e32 v238, v236, v238
	v_add_f32_e32 v239, v237, v240
	ds_write_b64 v248, v[238:239] offset:1280
	s_waitcnt vmcnt(15)
	s_barrier
	v_mfma_f32_32x32x16_f16 v[96:111], a[176:179], v[160:163], v[96:111]
	ds_read_b128 v[160:163], v193 offset:32768
	v_cvt_pk_f16_f32 v223, v218, v219
	v_mfma_f32_32x32x16_f16 v[112:127], a[176:179], v[164:167], v[112:127]
	ds_read_b128 v[164:167], v193 offset:33792
	v_permlane32_swap_b32_e32 v220, v222
	v_permlane32_swap_b32_e32 v221, v223
	s_cmp_eq_u32 s31, 0
	s_cbranch_scc1 .LD_slow36
	global_store_dwordx4 v195, v[220:223], s[36:37] offset:0
.LD_join37:
	s_waitcnt lgkmcnt(3)
	v_mfma_f32_32x32x16_f16 v[96:111], a[180:183], v[168:171], v[96:111]
	ds_read_b128 v[168:171], v193 offset:34816
	v_mfma_f32_32x32x16_f16 v[112:127], a[180:183], v[172:175], v[112:127]
	ds_read_b128 v[172:175], v193 offset:35840
	global_load_lds_dwordx4 v192, s[44:45] offset:3072 sc1
	v_mfma_f32_32x32x16_f16 v[96:111], a[184:187], v[176:179], v[96:111]
	ds_read_b128 v[176:179], v193 offset:36864
	v_mfma_f32_32x32x16_f16 v[112:127], a[184:187], v[180:183], v[112:127]
	ds_read_b128 v[180:183], v193 offset:37888
	v_mfma_f32_32x32x16_f16 v[96:111], a[188:191], v[184:187], v[96:111]
	ds_read_b128 v[184:187], v193 offset:38912
	v_mfma_f32_32x32x16_f16 v[112:127], a[188:191], v[188:191], v[112:127]
	ds_read_b128 v[188:191], v193 offset:39936
	s_mov_b32 m0, s54
	s_add_u32 s44, s34, 0x8000
	s_addc_u32 s45, s35, 0
	global_load_lds_dwordx4 v192, s[44:45] sc1
	s_waitcnt lgkmcnt(2)
	v_mfma_f32_32x32x16_f16 v[96:111], a[192:195], v[160:163], v[96:111]
	ds_read_b128 v[160:163], v193 offset:40960
	v_mfma_f32_32x32x16_f16 v[112:127], a[192:195], v[164:167], v[112:127]
	ds_read_b128 v[164:167], v193 offset:41984
	v_mfma_f32_32x32x16_f16 v[96:111], a[196:199], v[168:171], v[96:111]
	ds_read_b128 v[168:171], v193 offset:43008
	v_mfma_f32_32x32x16_f16 v[112:127], a[196:199], v[172:175], v[112:127]
	ds_read_b128 v[172:175], v193 offset:44032
	global_load_lds_dwordx4 v192, s[44:45] offset:1024 sc1
	v_mfma_f32_32x32x16_f16 v[96:111], a[200:203], v[176:179], v[96:111]
	ds_read_b128 v[176:179], v193 offset:45056
	v_mfma_f32_32x32x16_f16 v[112:127], a[200:203], v[180:183], v[112:127]
	ds_read_b128 v[180:183], v193 offset:46080
	s_waitcnt lgkmcnt(2)
	v_mfma_f32_32x32x16_f16 v[96:111], a[204:207], v[184:187], v[96:111]
	ds_read_b128 v[184:187], v193 offset:47104
	s_waitcnt vmcnt(3)
	s_barrier
	v_mov_b32_e32 v199, 3
	s_cmp_eq_u32 s31, 0
	s_cbranch_scc1 .LD_slow38
	global_store_dword v197, v199, s[40:41]
.LD_join39:
	ds_read_b64 v[200:201], v249 offset:1024
	ds_read_b64 v[202:203], v249 offset:3072
	ds_read_b64 v[204:205], v249 offset:5120
	ds_read_b64 v[206:207], v249 offset:7168
	v_mfma_f32_32x32x16_f16 v[112:127], a[204:207], v[188:191], v[112:127]
	ds_read_b128 v[188:191], v193 offset:48128
	global_load_lds_dwordx4 v192, s[44:45] offset:2048 sc1
	v_mfma_f32_32x32x16_f16 v[96:111], a[208:211], v[160:163], v[96:111]
	ds_read_b128 v[160:163], v193 offset:49152
	v_mfma_f32_32x32x16_f16 v[112:127], a[208:211], v[164:167], v[112:127]
	ds_read_b128 v[164:167], v193 offset:50176
	v_mfma_f32_32x32x16_f16 v[96:111], a[212:215], v[168:171], v[96:111]
	ds_read_b128 v[168:171], v193 offset:51200
	v_mfma_f32_32x32x16_f16 v[112:127], a[212:215], v[172:175], v[112:127]
	ds_read_b128 v[172:175], v193 offset:52224
	global_load_lds_dwordx4 v192, s[44:45] offset:3072 sc1
	s_waitcnt lgkmcnt(2)
	v_mfma_f32_32x32x16_f16 v[96:111], a[216:219], v[176:179], v[96:111]
	ds_read_b128 v[176:179], v193 offset:53248
	v_mfma_f32_32x32x16_f16 v[112:127], a[216:219], v[180:183], v[112:127]
	ds_read_b128 v[180:183], v193 offset:54272
	v_mfma_f32_32x32x16_f16 v[96:111], a[220:223], v[184:187], v[96:111]
	ds_read_b128 v[184:187], v193 offset:55296
	v_mfma_f32_32x32x16_f16 v[112:127], a[220:223], v[188:191], v[112:127]
	ds_read_b128 v[188:191], v193 offset:56320
	s_mov_b32 m0, s55
	s_add_u32 s44, s34, 0x9000
	s_addc_u32 s45, s35, 0
	global_load_lds_dwordx4 v192, s[44:45] sc1
	v_mfma_f32_32x32x16_f16 v[96:111], a[224:227], v[160:163], v[96:111]
	ds_read_b128 v[160:163], v193 offset:57344
	v_mfma_f32_32x32x16_f16 v[112:127], a[224:227], v[164:167], v[112:127]
	ds_read_b128 v[164:167], v193 offset:58368
	s_waitcnt lgkmcnt(2)
	v_mfma_f32_32x32x16_f16 v[96:111], a[228:231], v[168:171], v[96:111]
	ds_read_b128 v[168:171], v193 offset:59392
	v_add_f32_e32 v200, v200, v202
	v_add_f32_e32 v201, v201, v203
	v_add_f32_e32 v200, v200, v204
	v_add_f32_e32 v201, v201, v205
	v_add_f32_e32 v200, v200, v206
	v_add_f32_e32 v201, v201, v207
	global_store_dwordx2 v250, v[200:201], s[72:73]
	v_mfma_f32_32x32x16_f16 v[112:127], a[228:231], v[172:175], v[112:127]
	ds_read_b128 v[172:175], v193 offset:60416
	global_load_lds_dwordx4 v192, s[44:45] offset:1024 sc1
	v_mfma_f32_32x32x16_f16 v[96:111], a[232:235], v[176:179], v[96:111]
	ds_read_b128 v[176:179], v193 offset:61440
	v_mfma_f32_32x32x16_f16 v[112:127], a[232:235], v[180:183], v[112:127]
	ds_read_b128 v[180:183], v193 offset:62464
	v_mfma_f32_32x32x16_f16 v[96:111], a[236:239], v[184:187], v[96:111]
	ds_read_b128 v[184:187], v193 offset:63488
	v_mfma_f32_32x32x16_f16 v[112:127], a[236:239], v[188:191], v[112:127]
	ds_read_b128 v[188:191], v193 offset:64512
	global_load_lds_dwordx4 v192, s[44:45] offset:2048 sc1
	s_waitcnt vmcnt(9)
	s_barrier
	s_waitcnt lgkmcnt(2)
	v_mfma_f32_32x32x16_f16 v[96:111], a[240:243], v[160:163], v[96:111]
	ds_read_b128 v[160:163], v192 offset:0
	v_mfma_f32_32x32x16_f16 v[112:127], a[240:243], v[164:167], v[112:127]
	ds_read_b128 v[164:167], v192 offset:1024
	v_mfma_f32_32x32x16_f16 v[96:111], a[244:247], v[168:171], v[96:111]
	ds_read_b128 v[168:171], v192 offset:2048
	v_mfma_f32_32x32x16_f16 v[112:127], a[244:247], v[172:175], v[112:127]
	ds_read_b128 v[172:175], v192 offset:3072
	global_load_lds_dwordx4 v192, s[44:45] offset:3072 sc1
	v_mfma_f32_32x32x16_f16 v[96:111], a[248:251], v[176:179], v[96:111]
	ds_read_b128 v[176:179], v192 offset:4096
	v_mfma_f32_32x32x16_f16 v[112:127], a[248:251], v[180:183], v[112:127]
	ds_read_b128 v[180:183], v192 offset:5120
	s_waitcnt lgkmcnt(2)
	v_mfma_f32_32x32x16_f16 v[96:111], a[252:255], v[184:187], v[96:111]
	ds_read_b128 v[184:187], v192 offset:6144
	v_mfma_f32_32x32x16_f16 v[112:127], a[252:255], v[188:191], v[112:127]
	ds_read_b128 v[188:191], v192 offset:7168
	s_mov_b32 m0, s56
	s_add_u32 s44, s34, 0x10000
	s_addc_u32 s45, s35, 0
	global_load_lds_dwordx4 v192, s[44:45] sc1
	s_add_u32 s33, s33, 1
	s_cmp_lt_u32 s33, s28
	s_cbranch_scc1 .LD_loop12
.LD_end13:
	s_nop 15
	s_nop 3
	s_sub_u32 s71, s33, 1
	s_and_b32 s64, s71, 1
	s_lshl_b32 s64, s64, 22
	s_add_u32 s64, s64, s50
	s_add_u32 s64, s64, 0x60000
	s_add_u32 s36, s6, s64
	s_addc_u32 s37, s7, 0
	s_lshl_b32 s64, s71, 3
	s_add_u32 s64, s64, s29
	s_lshl_b32 s64, s64, 5
	s_add_u32 s64, s64, s30
	s_lshl_b32 s64, s64, 2
	s_add_u32 s40, s8, s64
	s_addc_u32 s41, s9, 0
	s_lshl_b32 s64, s71, 19
	s_add_u32 s64, s64, 0x600
	s_add_u32 s72, s62, s64
	s_addc_u32 s73, s63, 0
	v_exp_f32_e32 v200, v96
	v_exp_f32_e32 v201, v97
	v_exp_f32_e32 v202, v98
	v_exp_f32_e32 v203, v99
	v_exp_f32_e32 v204, v100
	v_exp_f32_e32 v205, v101
	v_exp_f32_e32 v206, v102
	v_exp_f32_e32 v207, v103
	v_exp_f32_e32 v208, v104
	v_exp_f32_e32 v209, v105
	v_exp_f32_e32 v210, v106
	v_exp_f32_e32 v211, v107
	v_exp_f32_e32 v212, v108
	v_exp_f32_e32 v213, v109
	v_exp_f32_e32 v214, v110
	v_exp_f32_e32 v215, v111
	v_add_f32_e32 v200, 1.0, v200
	v_add_f32_e32 v201, 1.0, v201
	v_add_f32_e32 v202, 1.0, v202
	v_add_f32_e32 v203, 1.0, v203
	v_add_f32_e32 v204, 1.0, v204
	v_add_f32_e32 v205, 1.0, v205
	v_add_f32_e32 v206, 1.0, v206
	v_add_f32_e32 v207, 1.0, v207
	v_add_f32_e32 v208, 1.0, v208
	v_add_f32_e32 v209, 1.0, v209
	v_add_f32_e32 v210, 1.0, v210
	v_add_f32_e32 v211, 1.0, v211
	v_add_f32_e32 v212, 1.0, v212
	v_add_f32_e32 v213, 1.0, v213
	v_add_f32_e32 v214, 1.0, v214
	v_add_f32_e32 v215, 1.0, v215
	v_rcp_f32_e32 v200, v200
	v_rcp_f32_e32 v201, v201
	v_rcp_f32_e32 v202, v202
	v_rcp_f32_e32 v203, v203
	v_rcp_f32_e32 v204, v204
	v_rcp_f32_e32 v205, v205
	v_rcp_f32_e32 v206, v206
	v_rcp_f32_e32 v207, v207
	v_rcp_f32_e32 v208, v208
	v_rcp_f32_e32 v209, v209
	v_rcp_f32_e32 v210, v210
	v_rcp_f32_e32 v211, v211
	v_rcp_f32_e32 v212, v212
	v_rcp_f32_e32 v213, v213
	v_rcp_f32_e32 v214, v214
	v_rcp_f32_e32 v215, v215
	v_fmamk_f32 v208, v208, 0xc0b8aa3b, v198
	v_fmamk_f32 v209, v209, 0xc0b8aa3b, v198
	v_fmamk_f32 v210, v210, 0xc0b8aa3b, v198
	v_fmamk_f32 v211, v211, 0xc0b8aa3b, v198
	v_mul_f32_e32 v204, v204, v152
	v_mul_f32_e32 v205, v205, v153
	v_mul_f32_e32 v206, v206, v154
	v_mul_f32_e32 v207, v207, v155
	v_fma_f32 v152, v200, v208, v204
	v_fma_f32 v153, v201, v209, v205
	v_fma_f32 v154, v202, v210, v206
	v_fma_f32 v155, v203, v211, v207
	v_exp_f32_e32 v200, v152
	v_exp_f32_e32 v201, v153
	v_exp_f32_e32 v202, v154
	v_exp_f32_e32 v203, v155
	v_add_f32_e32 v200, 1.0, v200
	v_add_f32_e32 v201, 1.0, v201
	v_add_f32_e32 v202, 1.0, v202
	v_add_f32_e32 v203, 1.0, v203
	v_rcp_f32_e32 v200, v200
	v_rcp_f32_e32 v201, v201
	v_rcp_f32_e32 v202, v202
	v_rcp_f32_e32 v203, v203
	v_fma_f32 v200, v200, 2.0, -1.0
	v_fma_f32 v201, v201, 2.0, -1.0
	v_fma_f32 v202, v202, 2.0, -1.0
	v_fma_f32 v203, v203, 2.0, -1.0
	v_mul_f32_e32 v216, v212, v200
	v_mul_f32_e32 v217, v213, v201
	v_mul_f32_e32 v218, v214, v202
	v_mul_f32_e32 v219, v215, v203
	v_mul_f32_e32 v236, v216, v228
	v_mul_f32_e32 v237, v216, v232
	v_fmac_f32_e32 v236, v217, v229
	v_fmac_f32_e32 v237, v217, v233
	v_fmac_f32_e32 v236, v218, v230
	v_fmac_f32_e32 v237, v218, v234
	v_fmac_f32_e32 v236, v219, v231
	v_fmac_f32_e32 v237, v219, v235
	v_mov_b32_e32 v238, v236
	v_mov_b32_e32 v240, v237
	s_nop 1
	v_permlane32_swap_b32_e32 v236, v238
	v_permlane32_swap_b32_e32 v237, v240
	v_add_f32_e32 v238, v236, v238
	v_add_f32_e32 v239, v237, v240
	ds_write_b64 v248, v[238:239] offset:1536
	v_cvt_pk_f16_f32 v220, v216, v217
	v_cvt_pk_f16_f32 v221, v218, v219
	v_exp_f32_e32 v200, v112
	v_exp_f32_e32 v201, v113
	v_exp_f32_e32 v202, v114
	v_exp_f32_e32 v203, v115
	v_exp_f32_e32 v204, v116
	v_exp_f32_e32 v205, v117
	v_exp_f32_e32 v206, v118
	v_exp_f32_e32 v207, v119
	v_exp_f32_e32 v208, v120
	v_exp_f32_e32 v209, v121
	v_exp_f32_e32 v210, v122
	v_exp_f32_e32 v211, v123
	v_exp_f32_e32 v212, v124
	v_exp_f32_e32 v213, v125
	v_exp_f32_e32 v214, v126
	v_exp_f32_e32 v215, v127
	v_add_f32_e32 v200, 1.0, v200
	v_add_f32_e32 v201, 1.0, v201
	v_add_f32_e32 v202, 1.0, v202
	v_add_f32_e32 v203, 1.0, v203
	v_add_f32_e32 v204, 1.0, v204
	v_add_f32_e32 v205, 1.0, v205
	v_add_f32_e32 v206, 1.0, v206
	v_add_f32_e32 v207, 1.0, v207
	v_add_f32_e32 v208, 1.0, v208
	v_add_f32_e32 v209, 1.0, v209
	v_add_f32_e32 v210, 1.0, v210
	v_add_f32_e32 v211, 1.0, v211
	v_add_f32_e32 v212, 1.0, v212
	v_add_f32_e32 v213, 1.0, v213
	v_add_f32_e32 v214, 1.0, v214
	v_add_f32_e32 v215, 1.0, v215
	v_rcp_f32_e32 v200, v200
	v_rcp_f32_e32 v201, v201
	v_rcp_f32_e32 v202, v202
	v_rcp_f32_e32 v203, v203
	v_rcp_f32_e32 v204, v204
	v_rcp_f32_e32 v205, v205
	v_rcp_f32_e32 v206, v206
	v_rcp_f32_e32 v207, v207
	v_rcp_f32_e32 v208, v208
	v_rcp_f32_e32 v209, v209
	v_rcp_f32_e32 v210, v210
	v_rcp_f32_e32 v211, v211
	v_rcp_f32_e32 v212, v212
	v_rcp_f32_e32 v213, v213
	v_rcp_f32_e32 v214, v214
	v_rcp_f32_e32 v215, v215
	v_fmamk_f32 v208, v208, 0xc0b8aa3b, v198
	v_fmamk_f32 v209, v209, 0xc0b8aa3b, v198
	v_fmamk_f32 v210, v210, 0xc0b8aa3b, v198
	v_fmamk_f32 v211, v211, 0xc0b8aa3b, v198
	v_mul_f32_e32 v204, v204, v156
	v_mul_f32_e32 v205, v205, v157
	v_mul_f32_e32 v206, v206, v158
	v_mul_f32_e32 v207, v207, v159
	v_fma_f32 v156, v200, v208, v204
	v_fma_f32 v157, v201, v209, v205
	v_fma_f32 v158, v202, v210, v206
	v_fma_f32 v159, v203, v211, v207
	v_exp_f32_e32 v200, v156
	v_exp_f32_e32 v201, v157
	v_exp_f32_e32 v202, v158
	v_exp_f32_e32 v203, v159
	v_add_f32_e32 v200, 1.0, v200
	v_add_f32_e32 v201, 1.0, v201
	v_add_f32_e32 v202, 1.0, v202
	v_add_f32_e32 v203, 1.0, v203
	v_rcp_f32_e32 v200, v200
	v_rcp_f32_e32 v201, v201
	v_rcp_f32_e32 v202, v202
	v_rcp_f32_e32 v203, v203
	v_fma_f32 v200, v200, 2.0, -1.0
	v_fma_f32 v201, v201, 2.0, -1.0
	v_fma_f32 v202, v202, 2.0, -1.0
	v_fma_f32 v203, v203, 2.0, -1.0
	v_mul_f32_e32 v216, v212, v200
	v_mul_f32_e32 v217, v213, v201
	v_mul_f32_e32 v218, v214, v202
	v_mul_f32_e32 v219, v215, v203
	v_mul_f32_e32 v236, v216, v228
	v_mul_f32_e32 v237, v216, v232
	v_fmac_f32_e32 v236, v217, v229
	v_fmac_f32_e32 v237, v217, v233
	v_fmac_f32_e32 v236, v218, v230
	v_fmac_f32_e32 v237, v218, v234
	v_fmac_f32_e32 v236, v219, v231
	v_fmac_f32_e32 v237, v219, v235
	v_mov_b32_e32 v238, v236
	v_mov_b32_e32 v240, v237
	s_nop 1
	v_permlane32_swap_b32_e32 v236, v238
	v_permlane32_swap_b32_e32 v237, v240
	v_add_f32_e32 v238, v236, v238
	v_add_f32_e32 v239, v237, v240
	ds_write_b64 v248, v[238:239] offset:1792
	v_cvt_pk_f16_f32 v222, v216, v217
	v_cvt_pk_f16_f32 v223, v218, v219
	s_nop 1
	v_permlane32_swap_b32_e32 v220, v222
	v_permlane32_swap_b32_e32 v221, v223
	s_cmp_eq_u32 s31, 0
	s_cbranch_scc1 .LD_slow40
	global_store_dwordx4 v195, v[220:223], s[36:37] offset:0
